# RWKV prep items: four mu parameter loads issued at the top of the item (into v236..v251) instead of right before their use
# speedup vs baseline: 1.0089x; 1.0031x over previous
; DI unsigned cvtpk(float lo, float hi) { const f2_t v = {lo, hi}; return __builtin_bit_cast(unsigned, __builtin_convertvector(v, bf2_t)); }
; DI void rwkv_r1_item(const Args& A, int l, LAS unsigned char* lds, int item, int& dh_staged, int tid, int wave, int lane) {
;     ...
;     const int sgn = dir ? -1 : 1; const int tok0 = b * SEQ + (dir ? SEQ - 1 - 16 * cc : 16 * cc);
;     const float* mu = A.in[I_MU] + (size_t)(l * 2 + dir) * 1280;
;     float er[4][4], ek[4][4], ev[4][4];
;     u32x4_t ld[7];
; #pragma unroll
;     for (int i = 0; i < 7; ++i) { const int idx = lane + 64 * i; const int ri = idx / 24, pc = idx % 24; const bool ok = (idx < 17 * 24) && (ri > 0 || cc > 0);
;         ld[i] = (u32x4_t){0u, 0u, 0u, 0u};
;         if (ok) ld[i] = *(const u32x4_t*)(Z + (size_t)(tok0 + sgn * (ri - 1)) * ZLD + ZRKV + (pc >> 3) * RW + hh * 64 + (pc & 7) * 8); }
;     uint4 zcw[2], zca[2], zpw[2], zpa[2];
;     { const int zwd = dir ? ZWDB : ZWDF, zad = dir ? ZADB : ZADF; const bool hasp = !(cc == 0 && fr == 0);
;       const bf16* zc = Z + (size_t)(tok0 + sgn * fr) * ZLD; const bf16* zq = Z + (size_t)(tok0 + sgn * (fr - 1)) * ZLD;
; #pragma unroll
;       for (int ks = 0; ks < 2; ++ks) { zcw[ks] = *(const uint4*)(zc + zwd + 32 * ks + 8 * qd); zca[ks] = *(const uint4*)(zc + zad + 32 * ks + 8 * qd);
;           zpw[ks] = make_uint4(0u, 0u, 0u, 0u); zpa[ks] = make_uint4(0u, 0u, 0u, 0u);
;           if (hasp) { zpw[ks] = *(const uint4*)(zq + zwd + 32 * ks + 8 * qd); zpa[ks] = *(const uint4*)(zq + zad + 32 * ks + 8 * qd); } } }
;     if (dh_staged != dir * 6 + hh) { dh_staged = dir * 6 + hh;
;     const int ch = tid & 63, i0 = (tid >> 6) * 8; const float* w2 = A.in[I_W2] + ((size_t)(l * 2 + dir) * 64 + i0) * RW + hh * 64 + ch; const float* a2 = A.in[I_A2] + ((size_t)(l * 2 + dir) * 64 + i0) * RW + hh * 64 + ch;
;     u32x4_t pw, pa; pw.x = cvtpk(w2[0], w2[RW]); pw.y = cvtpk(w2[2 * RW], w2[3 * RW]); pw.z = cvtpk(w2[4 * RW], w2[5 * RW]); pw.w = cvtpk(w2[6 * RW], w2[7 * RW]);
;     pa.x = cvtpk(a2[0], a2[RW]); pa.y = cvtpk(a2[2 * RW], a2[3 * RW]); pa.z = cvtpk(a2[4 * RW], a2[5 * RW]); pa.w = cvtpk(a2[6 * RW], a2[7 * RW]);
;     float prmv; { const int pi = tid >> 6, pc = hh * 64 + (tid & 63); const float* mu_ = A.in[I_MU] + (size_t)(l * 2 + dir) * 1280;
.LBB0_347:
	s_or_b64 exec, exec, s[38:39]
	s_ashr_i32 s0, s44, 3
	s_add_i32 s38, s0, s45
	v_readlane_b32 s72, v235, 17
	s_ashr_i32 s39, s38, 31
	s_mul_i32 s42, s38, 0x1400
	v_readlane_b32 s82, v235, 27
	s_mul_hi_i32 s0, s38, 0x1400
	v_readlane_b32 s83, v235, 28
	s_add_u32 s42, s82, s42
	s_addc_u32 s43, s83, s0
	v_lshlrev_b32_e32 v252, 2, v64
	v_mov_b32_e32 v253, v63
	v_add_u32_e32 v254, 0x1200, v252
	v_mov_b32_e32 v255, v63
	v_add_u32_e32 v252, s97, v252
	v_lshl_add_u64 v[252:253], s[42:43], 0, v[252:253]
	v_lshl_add_u64 v[254:255], s[42:43], 0, v[254:255]
	global_load_dwordx4 v[236:239], v[252:253], off offset:512
	global_load_dwordx4 v[240:243], v[254:255], off offset:16
	global_load_dwordx4 v[244:247], v[252:253], off offset:768
	global_load_dwordx4 v[248:251], v[254:255], off offset:272
	s_mul_i32 s0, s38, 6
	s_add_i32 s0, s0, s2
	s_cmp_eq_u32 s48, s0
	v_lshlrev_b32_e32 v102, 2, v146
	v_readlane_b32 s73, v235, 18
	v_readlane_b32 s74, v235, 19
	v_readlane_b32 s75, v235, 20
	v_readlane_b32 s76, v235, 21
	v_readlane_b32 s77, v235, 22
	v_readlane_b32 s78, v235, 23
	v_readlane_b32 s79, v235, 24
	v_readlane_b32 s80, v235, 25
	v_readlane_b32 s81, v235, 26
	v_readlane_b32 s84, v235, 29
	v_readlane_b32 s85, v235, 30
	v_readlane_b32 s86, v235, 31
	v_readlane_b32 s87, v235, 32
	s_cbranch_scc1 .LBB0_358
	v_readlane_b32 s72, v235, 17
	s_lshl_b64 s[44:45], s[38:39], 6
	v_readlane_b32 s86, v235, 31
	v_readlane_b32 s87, v235, 32
	v_or_b32_e32 v89, s44, v66
	s_movk_i32 s44, 0x600
	v_mov_b64_e32 v[104:105], s[86:87]
	v_readlane_b32 s73, v235, 18
	v_readlane_b32 s74, v235, 19
	v_readlane_b32 s75, v235, 20
	v_readlane_b32 s76, v235, 21
	v_readlane_b32 s77, v235, 22
	v_readlane_b32 s78, v235, 23
	v_readlane_b32 s79, v235, 24
	v_readlane_b32 s80, v235, 25
	v_readlane_b32 s81, v235, 26
	v_readlane_b32 s82, v235, 27
	v_readlane_b32 s83, v235, 28
	v_readlane_b32 s84, v235, 29
	v_readlane_b32 s85, v235, 30
	v_mad_u64_u32 v[104:105], s[46:47], v89, s44, v[104:105]
	v_mad_i32_i24 v105, s45, v214, v105
	s_lshl_b64 s[46:47], s[40:41], 2
	v_readlane_b32 s72, v235, 36
	v_lshl_add_u64 v[104:105], v[104:105], 0, s[46:47]
	v_mov_b32_e32 v103, v63
	v_readlane_b32 s74, v235, 38
	v_readlane_b32 s75, v235, 39
	v_lshl_add_u64 v[104:105], v[104:105], 0, v[102:103]
	v_add_co_u32_e32 v108, vcc, s97, v104
	v_mov_b64_e32 v[106:107], s[74:75]
	v_mad_u64_u32 v[106:107], s[48:49], v89, s44, v[106:107]
	v_mad_i32_i24 v107, s45, v214, v107
	v_addc_co_u32_e32 v109, vcc, 0, v105, vcc
	v_lshl_add_u64 v[106:107], v[106:107], 0, s[46:47]
	global_load_dword v89, v[104:105], off
	global_load_dword v91, v[104:105], off offset:1536
	global_load_dword v93, v[104:105], off offset:3072
	v_add_co_u32_e32 v104, vcc, 0x2000, v104
	v_lshl_add_u64 v[106:107], v[106:107], 0, v[102:103]
	s_nop 0
	v_addc_co_u32_e32 v105, vcc, 0, v105, vcc
	global_load_dword v95, v[108:109], off offset:512
	global_load_dword v97, v[108:109], off offset:2048
	global_load_dword v99, v[108:109], off offset:3584
	global_load_dword v101, v[104:105], off offset:1024
	global_load_dword v103, v[104:105], off offset:2560
	s_nop 0
	global_load_dword v108, v[106:107], off
	global_load_dword v109, v[106:107], off offset:1536
	global_load_dword v110, v[106:107], off offset:3072
	v_add_co_u32_e32 v104, vcc, 0x1000, v106
	v_readlane_b32 s73, v235, 37
	s_nop 0
	v_addc_co_u32_e32 v105, vcc, 0, v107, vcc
	global_load_dword v111, v[104:105], off offset:512
	global_load_dword v112, v[104:105], off offset:2048
	global_load_dword v113, v[104:105], off offset:3584
	v_add_co_u32_e32 v104, vcc, 0x2000, v106
	v_readlane_b32 s76, v235, 40
	s_nop 0
	v_addc_co_u32_e32 v105, vcc, 0, v107, vcc
	global_load_dword v114, v[104:105], off offset:1024
	global_load_dword v115, v[104:105], off offset:2560
	v_or_b32_e32 v104, s40, v146
	v_readlane_b32 s77, v235, 41
	v_readlane_b32 s78, v235, 42
	v_readlane_b32 s79, v235, 43
	v_readlane_b32 s80, v235, 44
	v_readlane_b32 s81, v235, 45
	v_readlane_b32 s82, v235, 46
	v_readlane_b32 s83, v235, 47
	v_readlane_b32 s84, v235, 48
	v_readlane_b32 s85, v235, 49
	v_readlane_b32 s86, v235, 50
	v_readlane_b32 s87, v235, 51
	s_mov_b64 s[44:45], exec
	v_readlane_b32 s46, v234, 1
	v_readlane_b32 s47, v234, 2
	s_and_b64 s[46:47], s[44:45], s[46:47]
	s_xor_b64 s[44:45], s[46:47], s[44:45]
	s_mov_b64 exec, s[46:47]
	s_cbranch_execz .LBB0_355
	v_ashrrev_i32_e32 v105, 31, v104
	v_cmp_lt_i32_e32 vcc, 4, v169
	s_mov_b64 s[46:47], 0
	s_mov_b64 s[48:49], 0
	s_and_saveexec_b64 s[64:65], vcc
	s_xor_b64 s[64:65], exec, s[64:65]
	s_cbranch_execnz .LBB0_408
	s_andn2_saveexec_b64 s[64:65], s[64:65]
	s_cbranch_execnz .LBB0_415

; #define LAS __attribute__((address_space(3)))
; DI float bf2f(unsigned v) { return __uint_as_float(v << 16); }
; DI void rwkv_r1_item(const Args& A, int l, LAS unsigned char* lds, int item, int& dh_staged, int tid, int wave, int lane) {
;     ...
;     { LAS bf16* stg = IMG; constexpr int SLD = 200;
; #pragma unroll
;       for (int i = 0; i < 7; ++i) { const int idx = lane + 64 * i; const int ri = idx / 24, pc = idx % 24; if (idx < 17 * 24) *(LAS u32x4_t*)(stg + ri * SLD + pc * 8) = ld[i]; }
;       asm volatile("s_waitcnt lgkmcnt(0)" ::: "memory");
; #pragma unroll
;       for (int nt = 0; nt < 4; ++nt) { const LAS bf16* sp = stg + (4 * qd) * SLD + 16 * nt + fr;
;           float qr = bf2f(sp[0]), qk = bf2f(sp[64]), qv = bf2f(sp[128]);
;           const float mr = prm[16 * nt + fr], mk = prm[64 + 16 * nt + fr], mv = prm[128 + 16 * nt + fr];
; #pragma unroll
;           for (int r = 0; r < 4; ++r) { const float cr = bf2f(sp[(r + 1) * SLD]), ck = bf2f(sp[(r + 1) * SLD + 64]), cv = bf2f(sp[(r + 1) * SLD + 128]);
;               er[nt][r] = cr + mr * (qr - cr); ek[nt][r] = ck + mk * (qk - ck); ev[nt][r] = cv + mv * (qv - cv); qr = cr; qk = ck; qv = cv; } }
.LBB0_358:
	s_waitcnt vmcnt(9)
	ds_write_b128 v198, v[34:37] offset:18432
	s_waitcnt vmcnt(8)
	ds_write_b128 v199, v[38:41] offset:18432
	s_waitcnt vmcnt(7)
	ds_write_b128 v200, v[42:45] offset:18432
	s_waitcnt vmcnt(6)
	ds_write_b128 v201, v[46:49] offset:18432
	s_waitcnt vmcnt(5)
	ds_write_b128 v202, v[50:53] offset:18432
	s_waitcnt vmcnt(4)
	ds_write_b128 v203, v[54:57] offset:18432
	s_and_saveexec_b64 s[44:45], s[4:5]
	ds_write_b128 v204, v[58:61] offset:24832
	s_or_b64 exec, exec, s[44:45]
	s_waitcnt lgkmcnt(0)
	ds_read2_b32 v[58:59], v174 offset1:16
	ds_read2_b32 v[106:107], v174 offset0:64 offset1:80
	ds_read2_b32 v[34:35], v174 offset0:128 offset1:144
	ds_read_u16 v36, v173 offset:19488
	ds_read_u16 v37, v173 offset:19888
	ds_read_u16 v38, v173 offset:20288
	s_waitcnt vmcnt(3)
	v_lshlrev_b32_e32 v216, 16, v26
	v_and_b32_e32 v217, 0xffff0000, v26
	s_waitcnt lgkmcnt(2)
	v_lshlrev_b32_e32 v36, 16, v36
	s_waitcnt lgkmcnt(1)
	v_lshlrev_b32_e32 v37, 16, v37
	s_waitcnt lgkmcnt(0)
	v_lshlrev_b32_e32 v39, 16, v38
	ds_read_u16 v38, v173 offset:18688
	ds_read_u16 v40, v173 offset:19088
	v_lshlrev_b32_e32 v160, 16, v27
	v_and_b32_e32 v158, 0xffff0000, v27
	v_lshlrev_b32_e32 v215, 16, v30
	v_and_b32_e32 v218, 0xffff0000, v30
	s_waitcnt lgkmcnt(0)
	v_lshlrev_b32_e32 v41, 16, v40
	v_lshlrev_b32_e32 v40, 16, v38
	v_pk_mov_b32 v[42:43], v[40:41], v[36:37] op_sel:[1,0]
	v_mov_b32_e32 v38, v37
	v_pk_add_f32 v[40:41], v[40:41], v[42:43] neg_lo:[0,1] neg_hi:[0,1]
	v_pk_add_f32 v[36:37], v[36:37], v[38:39] neg_lo:[0,1] neg_hi:[0,1]
	v_pk_fma_f32 v[46:47], v[34:35], v[40:41], v[42:43] op_sel_hi:[0,1,1]
	v_pk_fma_f32 v[48:49], v[34:35], v[36:37], v[38:39] op_sel_hi:[0,1,1]
	ds_read_u16 v34, v173 offset:18592
	v_lshlrev_b32_e32 v161, 16, v31
	v_and_b32_e32 v159, 0xffff0000, v31
	v_lshlrev_b32_e32 v157, 16, v32
	v_and_b32_e32 v129, 0xffff0000, v32
	s_waitcnt lgkmcnt(0)
	v_lshlrev_b32_e32 v108, 16, v34
	ds_read_u16 v34, v173 offset:18992
	ds_read_u16 v36, v173 offset:19392
	v_lshlrev_b32_e32 v125, 16, v33
	v_and_b32_e32 v123, 0xffff0000, v33
	s_waitcnt vmcnt(2)
	v_lshlrev_b32_e32 v118, 16, v22
	s_waitcnt lgkmcnt(1)
	v_lshlrev_b32_e32 v60, 16, v34
	s_waitcnt lgkmcnt(0)
	v_lshlrev_b32_e32 v61, 16, v36
	ds_read_u16 v34, v173 offset:20192
	ds_read_u16 v36, v173 offset:19792
	v_and_b32_e32 v119, 0xffff0000, v22
	v_lshlrev_b32_e32 v114, 16, v23
	v_and_b32_e32 v115, 0xffff0000, v23
	s_waitcnt lgkmcnt(1)
	v_lshlrev_b32_e32 v105, 16, v34
	ds_read_u16 v34, v173 offset:19520
	ds_read_u16 v37, v173 offset:19920
	ds_read_u16 v38, v173 offset:20320
	s_waitcnt lgkmcnt(3)
	v_lshlrev_b32_e32 v104, 16, v36
	v_lshlrev_b32_e32 v30, 16, v25
	s_waitcnt lgkmcnt(2)
	v_lshlrev_b32_e32 v36, 16, v34
	s_waitcnt lgkmcnt(1)
	v_lshlrev_b32_e32 v37, 16, v37
	s_waitcnt lgkmcnt(0)
	v_lshlrev_b32_e32 v39, 16, v38
	ds_read_u16 v34, v173 offset:18720
	ds_read_u16 v38, v173 offset:19120
	v_and_b32_e32 v31, 0xffff0000, v25
	v_lshlrev_b32_e32 v120, 16, v18
	v_and_b32_e32 v121, 0xffff0000, v18
	s_waitcnt lgkmcnt(1)
	v_lshlrev_b32_e32 v40, 16, v34
	s_waitcnt lgkmcnt(0)
	v_lshlrev_b32_e32 v41, 16, v38
	v_pk_mov_b32 v[42:43], v[40:41], v[36:37] op_sel:[1,0]
	v_mov_b32_e32 v38, v37
	v_pk_add_f32 v[40:41], v[40:41], v[42:43] neg_lo:[0,1] neg_hi:[0,1]
	v_mov_b32_e32 v34, v35
	v_pk_add_f32 v[36:37], v[36:37], v[38:39] neg_lo:[0,1] neg_hi:[0,1]
	v_pk_fma_f32 v[42:43], v[34:35], v[40:41], v[42:43] op_sel_hi:[0,1,1]
	v_pk_fma_f32 v[44:45], v[34:35], v[36:37], v[38:39] op_sel_hi:[0,1,1]
	ds_read2_b32 v[110:111], v174 offset0:32 offset1:48
	ds_read2_b32 v[112:113], v174 offset0:96 offset1:112
	ds_read2_b32 v[34:35], v174 offset0:160 offset1:176
	ds_read_u16 v36, v173 offset:19552
	ds_read_u16 v37, v173 offset:19952
	ds_read_u16 v38, v173 offset:20352
	v_lshlrev_b32_e32 v116, 16, v19
	v_and_b32_e32 v117, 0xffff0000, v19
	s_waitcnt lgkmcnt(2)
	v_lshlrev_b32_e32 v36, 16, v36
	s_waitcnt lgkmcnt(1)
	v_lshlrev_b32_e32 v37, 16, v37
	s_waitcnt lgkmcnt(0)
	v_lshlrev_b32_e32 v39, 16, v38
	ds_read_u16 v38, v173 offset:18752
	ds_read_u16 v40, v173 offset:19152
	v_lshlrev_b32_e32 v32, 16, v21
	v_and_b32_e32 v33, 0xffff0000, v21
	v_lshlrev_b32_e32 v153, 16, v28
	v_and_b32_e32 v128, 0xffff0000, v28
	s_waitcnt lgkmcnt(0)
	v_lshlrev_b32_e32 v41, 16, v40
	v_lshlrev_b32_e32 v40, 16, v38
	v_pk_mov_b32 v[50:51], v[40:41], v[36:37] op_sel:[1,0]
	v_mov_b32_e32 v38, v37
	v_pk_add_f32 v[40:41], v[40:41], v[50:51] neg_lo:[0,1] neg_hi:[0,1]
	v_pk_add_f32 v[36:37], v[36:37], v[38:39] neg_lo:[0,1] neg_hi:[0,1]
	v_pk_fma_f32 v[50:51], v[34:35], v[40:41], v[50:51] op_sel_hi:[0,1,1]
	v_pk_fma_f32 v[52:53], v[34:35], v[36:37], v[38:39] op_sel_hi:[0,1,1]
	ds_read_u16 v34, v173 offset:19584
	ds_read_u16 v37, v173 offset:19984
	ds_read_u16 v38, v173 offset:20384
	v_sub_f32_e32 v28, v215, v216
	v_lshlrev_b32_e32 v124, 16, v29
	s_waitcnt lgkmcnt(2)
	v_lshlrev_b32_e32 v36, 16, v34
	s_waitcnt lgkmcnt(1)
	v_lshlrev_b32_e32 v37, 16, v37
	s_waitcnt lgkmcnt(0)
; DI float bf2f(unsigned v) { return __uint_as_float(v << 16); }
; DI void rwkv_r1_item(const Args& A, int l, LAS unsigned char* lds, int item, int& dh_staged, int tid, int wave, int lane) {
;     ...
;           float qr = bf2f(sp[0]), qk = bf2f(sp[64]), qv = bf2f(sp[128]);
;           const float mr = prm[16 * nt + fr], mk = prm[64 + 16 * nt + fr], mv = prm[128 + 16 * nt + fr];
; #pragma unroll
;           for (int r = 0; r < 4; ++r) { const float cr = bf2f(sp[(r + 1) * SLD]), ck = bf2f(sp[(r + 1) * SLD + 64]), cv = bf2f(sp[(r + 1) * SLD + 128]);
;               er[nt][r] = cr + mr * (qr - cr); ek[nt][r] = ck + mk * (qk - ck); ev[nt][r] = cv + mv * (qv - cv); qr = cr; qk = ck; qv = cv; } }
;       asm volatile("s_waitcnt lgkmcnt(0)" ::: "memory"); }
;     bf16x8_t thA[2], adA[2];
;     {
; #pragma unroll
;       for (int ks = 0; ks < 2; ++ks) { float cw[8], pw[8], ca[8], pa[8];
;           unpack8(zcw[ks], cw); unpack8(zca[ks], ca); unpack8(zpw[ks], pw); unpack8(zpa[ks], pa);
;           const float* muw = mu + 1152 + 32 * ks + 8 * qd; const float* mua = mu + 1216 + 32 * ks + 8 * qd;
; #pragma unroll
;           for (int e = 0; e < 8; ++e) { const float xw = cw[e] + muw[e] * (pw[e] - cw[e]); cw[e] = 1.f - 2.f * __builtin_amdgcn_rcpf(1.f + __expf(2.f * xw)); ca[e] = ca[e] + mua[e] * (pa[e] - ca[e]); }
	v_lshlrev_b32_e32 v39, 16, v38
	ds_read_u16 v34, v173 offset:18784
	ds_read_u16 v38, v173 offset:19184
	ds_read_u16 v127, v173 offset:19024
	ds_read_u16 v152, v173 offset:19056
	ds_read_u16 v126, v173 offset:19424
	ds_read_u16 v151, v173 offset:19456
	ds_read_u16 v130, v173 offset:18624
	ds_read_u16 v131, v173 offset:18656
	ds_read_u16 v148, v173 offset:19824
	ds_read_u16 v150, v173 offset:19856
	ds_read_u16 v101, v173 offset:20224
	ds_read_u16 v149, v173 offset:20256
	ds_read_u16 v136, v173 offset:18560
	ds_read_u16 v142, v173 offset:18960
	ds_read_u16 v143, v173 offset:19360
	ds_read_u16 v137, v173 offset:18832
	ds_read_u16 v139, v173 offset:19232
	ds_read_u16 v109, v173 offset:20160
	ds_read_u16 v155, v173 offset:19760
	ds_read_u16 v144, v173 offset:20032
	ds_read_u16 v145, v173 offset:19632
	ds_read_u16 v156, v173 offset:18432
	ds_read_u16 v141, v173 offset:18464
	ds_read_u16 v140, v173 offset:18864
	ds_read_u16 v154, v173 offset:19264
	ds_read_u16 v135, v173 offset:20064
	ds_read_u16 v138, v173 offset:19664
	ds_read_u16 v133, v173 offset:18496
	ds_read_u16 v132, v173 offset:18896
	ds_read_u16 v134, v173 offset:19296
	ds_read_u16 v95, v173 offset:20096
	ds_read_u16 v97, v173 offset:19696
	ds_read_u16 v89, v173 offset:18528
	ds_read_u16 v93, v173 offset:18928
	ds_read_u16 v103, v173 offset:19328
	ds_read_u16 v91, v173 offset:20128
	ds_read_u16 v99, v173 offset:19728
	s_waitcnt lgkmcnt(0)
	v_and_b32_e32 v122, 0xffff0000, v29
	s_waitcnt lgkmcnt(14)
	v_lshlrev_b32_e32 v40, 16, v34
	v_lshlrev_b32_e32 v41, 16, v38
	v_pk_mov_b32 v[54:55], v[40:41], v[36:37] op_sel:[1,0]
	v_mov_b32_e32 v38, v37
	v_pk_add_f32 v[40:41], v[40:41], v[54:55] neg_lo:[0,1] neg_hi:[0,1]
	v_mov_b32_e32 v34, v35
	v_pk_add_f32 v[36:37], v[36:37], v[38:39] neg_lo:[0,1] neg_hi:[0,1]
	v_pk_fma_f32 v[54:55], v[34:35], v[40:41], v[54:55] op_sel_hi:[0,1,1]
	v_pk_fma_f32 v[56:57], v[34:35], v[36:37], v[38:39] op_sel_hi:[0,1,1]
	v_lshlrev_b32_e32 v34, 2, v64
	v_mov_b32_e32 v35, v63
	v_lshl_add_u64 v[162:163], s[42:43], 0, v[34:35]
	v_add_co_u32_e32 v26, vcc, s97, v162
	s_mov_b64 s[42:43], 0x1200
	s_nop 0
	v_addc_co_u32_e32 v27, vcc, 0, v163, vcc
	v_lshl_add_u64 v[36:37], v[162:163], 0, s[42:43]
	v_lshlrev_b32_e32 v38, 16, v24
	v_and_b32_e32 v39, 0xffff0000, v24
	v_lshlrev_b32_e32 v40, 16, v20
	v_and_b32_e32 v41, 0xffff0000, v20
	s_waitcnt vmcnt(0)
	v_mov_b32_e32 v22, v236
	v_mov_b32_e32 v23, v237
	v_mov_b32_e32 v24, v238
	v_mov_b32_e32 v25, v239
	v_mov_b32_e32 v18, v240
	v_mov_b32_e32 v19, v241
	v_mov_b32_e32 v20, v242
	v_mov_b32_e32 v21, v243
	s_mov_b64 s[42:43], 0x1300
	v_lshl_add_u64 v[34:35], v[162:163], 0, s[42:43]
	v_pk_add_f32 v[116:117], v[116:117], v[114:115] neg_lo:[0,1] neg_hi:[0,1]
	v_pk_add_f32 v[120:121], v[120:121], v[118:119] neg_lo:[0,1] neg_hi:[0,1]
	s_lshl_b64 s[42:43], s[38:39], 14
	s_ashr_i32 s0, s68, 31
	s_add_u32 s42, s68, s42
	s_addc_u32 s43, s0, s43
	s_movk_i32 s0, 0x300
	s_waitcnt vmcnt(1)
	v_fmac_f32_e32 v216, v28, v22
	v_sub_f32_e32 v28, v218, v217
	v_fmac_f32_e32 v217, v28, v23
	v_add_f32_e32 v22, v216, v216
	v_add_f32_e32 v23, v217, v217
	v_mov_b32_e32 v26, v244
	v_mov_b32_e32 v27, v245
	v_mov_b32_e32 v28, v246
	v_mov_b32_e32 v29, v247
	s_nop 0
	v_mov_b32_e32 v216, v248
	v_mov_b32_e32 v217, v249
	v_mov_b32_e32 v218, v250
	v_mov_b32_e32 v219, v251
	v_mul_f32_e32 v22, 0x3fb8aa3b, v22
	v_mul_f32_e32 v23, 0x3fb8aa3b, v23
	v_exp_f32_e32 v22, v22
	v_exp_f32_e32 v23, v23
	v_add_f32_e32 v22, 1.0, v22
	v_add_f32_e32 v23, 1.0, v23
	v_rcp_f32_e32 v22, v22
	v_rcp_f32_e32 v23, v23
	s_waitcnt vmcnt(1)
	v_pk_fma_f32 v[28:29], v[116:117], v[28:29], v[114:115]
	v_sub_f32_e32 v114, v157, v153
	v_fmac_f32_e32 v153, v114, v18
	v_sub_f32_e32 v114, v129, v128
	v_fmac_f32_e32 v128, v114, v19
	v_add_f32_e32 v18, v153, v153
	v_add_f32_e32 v19, v128, v128
	v_mul_f32_e32 v18, 0x3fb8aa3b, v18
	v_mul_f32_e32 v19, 0x3fb8aa3b, v19
	v_exp_f32_e32 v18, v18
	v_exp_f32_e32 v19, v19
	v_pk_fma_f32 v[26:27], v[120:121], v[26:27], v[118:119]
	v_sub_f32_e32 v118, v161, v160
	v_add_f32_e32 v18, 1.0, v18
	v_add_f32_e32 v19, 1.0, v19
	v_rcp_f32_e32 v18, v18
	v_rcp_f32_e32 v19, v19
	v_fmac_f32_e32 v160, v118, v24
	v_sub_f32_e32 v118, v159, v158
	v_fmac_f32_e32 v158, v118, v25
	v_pk_fma_f32 v[114:115], v[18:19], 2.0, 1.0 op_sel_hi:[1,0,0] neg_lo:[1,0,0] neg_hi:[1,0,0]
	v_pk_add_f32 v[18:19], v[40:41], v[38:39] neg_lo:[0,1] neg_hi:[0,1]
	v_add_f32_e32 v24, v160, v160
	s_waitcnt vmcnt(0)
; #define LAS __attribute__((address_space(3)))
; DI unsigned cvtpk(float lo, float hi) { const f2_t v = {lo, hi}; return __builtin_bit_cast(unsigned, __builtin_convertvector(v, bf2_t)); }
; DI void rwkv_r1_item(const Args& A, int l, LAS unsigned char* lds, int item, int& dh_staged, int tid, int wave, int lane) {
;     ...
;       for (int ks = 0; ks < 2; ++ks) { float cw[8], pw[8], ca[8], pa[8];
;           unpack8(zcw[ks], cw); unpack8(zca[ks], ca); unpack8(zpw[ks], pw); unpack8(zpa[ks], pa);
;           const float* muw = mu + 1152 + 32 * ks + 8 * qd; const float* mua = mu + 1216 + 32 * ks + 8 * qd;
; #pragma unroll
;           for (int e = 0; e < 8; ++e) { const float xw = cw[e] + muw[e] * (pw[e] - cw[e]); cw[e] = 1.f - 2.f * __builtin_amdgcn_rcpf(1.f + __expf(2.f * xw)); ca[e] = ca[e] + mua[e] * (pa[e] - ca[e]); }
;           union { unsigned u[4]; bf16x8_t v; } x, y;
; #pragma unroll
;           for (int e = 0; e < 4; ++e) { x.u[e] = cvtpk(cw[2 * e], cw[2 * e + 1]); y.u[e] = cvtpk(ca[2 * e], ca[2 * e + 1]); }
;           thA[ks] = x.v; adA[ks] = y.v; } }
;     f32x4 wl[4], al[4];
; #pragma unroll
;     for (int nt = 0; nt < 4; ++nt) { wl[nt] = (f32x4){0.f, 0.f, 0.f, 0.f}; al[nt] = (f32x4){0.f, 0.f, 0.f, 0.f};
; #pragma unroll
;         for (int ks = 0; ks < 2; ++ks) { const bf16x8_t bw = *(const LAS bf16x8_t*)(W2T + (16 * nt + fr) * 72 + 32 * ks + 8 * qd); const bf16x8_t ba = *(const LAS bf16x8_t*)(A2T + (16 * nt + fr) * 72 + 32 * ks + 8 * qd);
	v_pk_fma_f32 v[38:39], v[18:19], v[216:217], v[38:39]
	v_sub_f32_e32 v18, v125, v124
	v_sub_f32_e32 v19, v123, v122
	v_fmac_f32_e32 v124, v18, v20
	v_fmac_f32_e32 v122, v19, v21
	v_add_f32_e32 v18, v124, v124
	v_add_f32_e32 v19, v122, v122
	v_add_f32_e32 v25, v158, v158
	v_mul_f32_e32 v18, 0x3fb8aa3b, v18
	v_mul_f32_e32 v19, 0x3fb8aa3b, v19
	v_mul_f32_e32 v24, 0x3fb8aa3b, v24
	v_mul_f32_e32 v25, 0x3fb8aa3b, v25
	v_exp_f32_e32 v18, v18
	v_exp_f32_e32 v19, v19
	v_exp_f32_e32 v24, v24
	v_exp_f32_e32 v25, v25
	v_add_f32_e32 v18, 1.0, v18
	v_add_f32_e32 v19, 1.0, v19
	v_add_f32_e32 v24, 1.0, v24
	v_add_f32_e32 v25, 1.0, v25
	v_rcp_f32_e32 v18, v18
	v_rcp_f32_e32 v19, v19
	v_rcp_f32_e32 v24, v24
	v_rcp_f32_e32 v25, v25
	v_pk_fma_f32 v[22:23], v[22:23], 2.0, 1.0 op_sel_hi:[1,0,0] neg_lo:[1,0,0] neg_hi:[1,0,0]
	v_pk_fma_f32 v[40:41], v[18:19], 2.0, 1.0 op_sel_hi:[1,0,0] neg_lo:[1,0,0] neg_hi:[1,0,0]
	v_pk_add_f32 v[18:19], v[32:33], v[30:31] neg_lo:[0,1] neg_hi:[0,1]
	v_pk_fma_f32 v[24:25], v[24:25], 2.0, 1.0 op_sel_hi:[1,0,0] neg_lo:[1,0,0] neg_hi:[1,0,0]
	v_pk_fma_f32 v[30:31], v[18:19], v[218:219], v[30:31]
	v_cvt_pk_bf16_f32 v22, v22, v23
	v_cvt_pk_bf16_f32 v18, v26, v27
	v_cvt_pk_bf16_f32 v23, v24, v25
	v_cvt_pk_bf16_f32 v19, v28, v29
	v_cvt_pk_bf16_f32 v24, v114, v115
	v_cvt_pk_bf16_f32 v20, v38, v39
	v_cvt_pk_bf16_f32 v21, v30, v31
	v_lshlrev_b32_e32 v157, 16, v10
	v_and_b32_e32 v158, 0xffff0000, v10
	v_lshlrev_b32_e32 v128, 16, v11
	v_and_b32_e32 v124, 0xffff0000, v11
	v_lshlrev_b32_e32 v123, 16, v16
	v_and_b32_e32 v121, 0xffff0000, v16
	v_lshlrev_b32_e32 v119, 16, v17
	v_and_b32_e32 v117, 0xffff0000, v17
	v_lshlrev_b32_e32 v28, 16, v8
	v_and_b32_e32 v29, 0xffff0000, v8
	v_lshlrev_b32_e32 v16, 16, v9
	v_and_b32_e32 v17, 0xffff0000, v9
	v_lshlrev_b32_e32 v114, 16, v2
	v_and_b32_e32 v115, 0xffff0000, v2
	v_lshlrev_b32_e32 v38, 16, v3
	v_and_b32_e32 v39, 0xffff0000, v3
	v_lshlrev_b32_e32 v30, 16, v4
	v_and_b32_e32 v31, 0xffff0000, v4
	v_lshlrev_b32_e32 v26, 16, v5
	v_and_b32_e32 v27, 0xffff0000, v5
	global_load_dwordx4 v[2:5], v[36:37], off offset:144
	global_load_dwordx4 v[8:11], v[36:37], off offset:128
	v_lshlrev_b32_e32 v153, 16, v14
	v_and_b32_e32 v14, 0xffff0000, v14
	v_cvt_pk_bf16_f32 v25, v40, v41
	v_lshlrev_b32_e32 v40, 16, v6
	v_and_b32_e32 v41, 0xffff0000, v6
	v_lshlrev_b32_e32 v32, 16, v7
	v_and_b32_e32 v33, 0xffff0000, v7
	v_sub_f32_e32 v6, v153, v157
	v_sub_f32_e32 v7, v14, v158
	v_lshlrev_b32_e32 v129, 16, v15
	v_and_b32_e32 v125, 0xffff0000, v15
	v_lshlrev_b32_e32 v122, 16, v12
	v_and_b32_e32 v120, 0xffff0000, v12
	v_lshlrev_b32_e32 v118, 16, v13
	v_and_b32_e32 v116, 0xffff0000, v13
	s_waitcnt vmcnt(0)
	v_fmac_f32_e32 v157, v6, v8
	v_fmac_f32_e32 v158, v7, v9
	v_add_f32_e32 v6, v157, v157
	v_add_f32_e32 v7, v158, v158
	v_mul_f32_e32 v6, 0x3fb8aa3b, v6
	v_mul_f32_e32 v7, 0x3fb8aa3b, v7
	v_exp_f32_e32 v6, v6
	v_exp_f32_e32 v7, v7
	v_add_f32_e32 v6, 1.0, v6
	v_add_f32_e32 v7, 1.0, v7
	v_rcp_f32_e32 v6, v6
	v_rcp_f32_e32 v7, v7
	s_nop 0
	v_pk_fma_f32 v[36:37], v[6:7], 2.0, 1.0 op_sel_hi:[1,0,0] neg_lo:[1,0,0] neg_hi:[1,0,0]
	global_load_dwordx4 v[6:9], v[34:35], off offset:144
	global_load_dwordx4 v[12:15], v[34:35], off offset:128
	v_pk_add_f32 v[34:35], v[114:115], v[40:41] neg_lo:[0,1] neg_hi:[0,1]
	s_waitcnt vmcnt(0)
	v_pk_fma_f32 v[12:13], v[34:35], v[12:13], v[40:41]
	v_sub_f32_e32 v34, v129, v128
	v_fmac_f32_e32 v128, v34, v10
	v_sub_f32_e32 v34, v125, v124
	v_fmac_f32_e32 v124, v34, v11
	v_pk_add_f32 v[34:35], v[38:39], v[32:33] neg_lo:[0,1] neg_hi:[0,1]
	v_add_f32_e32 v10, v128, v128
	v_pk_fma_f32 v[14:15], v[34:35], v[14:15], v[32:33]
	v_sub_f32_e32 v32, v123, v122
	v_fmac_f32_e32 v122, v32, v2
	v_sub_f32_e32 v32, v121, v120
	v_fmac_f32_e32 v120, v32, v3
	v_add_f32_e32 v2, v122, v122
	v_add_f32_e32 v3, v120, v120
	v_mul_f32_e32 v2, 0x3fb8aa3b, v2
	v_mul_f32_e32 v3, 0x3fb8aa3b, v3
	v_exp_f32_e32 v2, v2
	v_exp_f32_e32 v3, v3
	v_add_f32_e32 v11, v124, v124
	v_mul_f32_e32 v10, 0x3fb8aa3b, v10
	v_add_f32_e32 v2, 1.0, v2
	v_add_f32_e32 v3, 1.0, v3
	v_rcp_f32_e32 v2, v2
	v_rcp_f32_e32 v3, v3
	v_mul_f32_e32 v11, 0x3fb8aa3b, v11
	v_exp_f32_e32 v10, v10
	v_exp_f32_e32 v11, v11
	v_pk_fma_f32 v[32:33], v[2:3], 2.0, 1.0 op_sel_hi:[1,0,0] neg_lo:[1,0,0] neg_hi:[1,0,0]
	v_pk_add_f32 v[2:3], v[30:31], v[28:29] neg_lo:[0,1] neg_hi:[0,1]
	v_add_f32_e32 v10, 1.0, v10
	v_pk_fma_f32 v[28:29], v[2:3], v[6:7], v[28:29]
	v_sub_f32_e32 v2, v119, v118
	v_sub_f32_e32 v3, v117, v116
	v_fmac_f32_e32 v118, v2, v4
	v_fmac_f32_e32 v116, v3, v5
	v_add_f32_e32 v2, v118, v118
	v_add_f32_e32 v3, v116, v116
	v_mul_f32_e32 v2, 0x3fb8aa3b, v2
	v_mul_f32_e32 v3, 0x3fb8aa3b, v3
	v_exp_f32_e32 v2, v2
	v_exp_f32_e32 v3, v3
	v_add_f32_e32 v11, 1.0, v11
	v_rcp_f32_e32 v10, v10
	v_add_f32_e32 v2, 1.0, v2
	v_add_f32_e32 v3, 1.0, v3
	v_rcp_f32_e32 v2, v2
	v_rcp_f32_e32 v3, v3
	v_rcp_f32_e32 v11, v11
	v_cvt_pk_bf16_f32 v6, v36, v37
	v_cvt_pk_bf16_f32 v4, v28, v29
	v_pk_fma_f32 v[30:31], v[2:3], 2.0, 1.0 op_sel_hi:[1,0,0] neg_lo:[1,0,0] neg_hi:[1,0,0]
	v_pk_add_f32 v[2:3], v[26:27], v[16:17] neg_lo:[0,1] neg_hi:[0,1]
	v_pk_fma_f32 v[10:11], v[10:11], 2.0, 1.0 op_sel_hi:[1,0,0] neg_lo:[1,0,0] neg_hi:[1,0,0]
	v_pk_fma_f32 v[16:17], v[2:3], v[8:9], v[16:17]
	v_cvt_pk_bf16_f32 v2, v12, v13
	v_cvt_pk_bf16_f32 v7, v10, v11
	v_cvt_pk_bf16_f32 v3, v14, v15
	v_cvt_pk_bf16_f32 v5, v16, v17
	ds_read_b128 v[10:13], v175
	ds_read_b128 v[14:17], v175 offset:9216
	v_cvt_pk_bf16_f32 v8, v32, v33
	v_cvt_pk_bf16_f32 v9, v30, v31
	ds_read_b128 v[26:29], v175 offset:64
	ds_read_b128 v[30:33], v175 offset:9280
	s_waitcnt lgkmcnt(3)
; #define LAS __attribute__((address_space(3)))
; #define MFMA16(a, b, c) __builtin_amdgcn_mfma_f32_16x16x32_bf16((a), (b), (c), 0, 0, 0)
; DI void rwkv_r1_item(const Args& A, int l, LAS unsigned char* lds, int item, int& dh_staged, int tid, int wave, int lane) {
;     ...
;     f32x4 wl[4], al[4];
; #pragma unroll
;     for (int nt = 0; nt < 4; ++nt) { wl[nt] = (f32x4){0.f, 0.f, 0.f, 0.f}; al[nt] = (f32x4){0.f, 0.f, 0.f, 0.f};
; #pragma unroll
;         for (int ks = 0; ks < 2; ++ks) { const bf16x8_t bw = *(const LAS bf16x8_t*)(W2T + (16 * nt + fr) * 72 + 32 * ks + 8 * qd); const bf16x8_t ba = *(const LAS bf16x8_t*)(A2T + (16 * nt + fr) * 72 + 32 * ks + 8 * qd);
;             wl[nt] = MFMA16(thA[ks], bw, wl[nt]); al[nt] = MFMA16(adA[ks], ba, al[nt]); } }
;     float lw[4][4], alp[4][4], kap[4][4]; float ssq[4] = {0.f, 0.f, 0.f, 0.f}, bsm[4] = {0.f, 0.f, 0.f, 0.f};
; #pragma unroll
;     for (int nt = 0; nt < 4; ++nt) { const int ch = hh * 64 + 16 * nt + fr;
;         const float w0v = prm[192 + 16 * nt + fr], a0v = prm[256 + 16 * nt + fr], kkw = prm[320 + 16 * nt + fr], kaw = prm[384 + 16 * nt + fr], rkw = prm[448 + 16 * nt + fr];
; #pragma unroll
;         for (int r = 0; r < 4; ++r) { const float x = w0v + wl[nt][r];
;             lw[nt][r] = -0.6065306597126334f * __builtin_amdgcn_rcpf(1.f + __expf(-x));
;             const float a = __builtin_amdgcn_rcpf(1.f + __expf(-(a0v + al[nt][r]))); alp[nt][r] = a;
	v_mfma_f32_16x16x32_bf16 v[10:13], v[22:25], v[10:13], 0
	v_add_u32_e32 v128, 0x400, v174
	s_waitcnt lgkmcnt(2)
	v_mfma_f32_16x16x32_bf16 v[14:17], v[18:21], v[14:17], 0
	s_waitcnt lgkmcnt(1)
	v_mfma_f32_16x16x32_bf16 v[38:41], v[6:9], v[26:29], v[10:13]
	s_waitcnt lgkmcnt(0)
	v_mfma_f32_16x16x32_bf16 v[34:37], v[2:5], v[30:33], v[14:17]
	s_nop 0
	ds_read_b128 v[10:13], v175 offset:2304
	s_nop 1
	ds_read_b128 v[14:17], v175 offset:11520
	ds_read_b128 v[26:29], v175 offset:2368
	ds_read_b128 v[114:117], v175 offset:11584
	s_waitcnt lgkmcnt(3)
	v_mfma_f32_16x16x32_bf16 v[10:13], v[22:25], v[10:13], 0
	s_waitcnt lgkmcnt(2)
	v_mfma_f32_16x16x32_bf16 v[14:17], v[18:21], v[14:17], 0
	s_waitcnt lgkmcnt(1)
	v_mfma_f32_16x16x32_bf16 v[30:33], v[6:9], v[26:29], v[10:13]
	s_waitcnt lgkmcnt(0)
	v_mfma_f32_16x16x32_bf16 v[26:29], v[2:5], v[114:117], v[14:17]
	s_nop 1
	ds_read_b128 v[10:13], v175 offset:4608
	s_nop 0
	ds_read_b128 v[14:17], v175 offset:13824
	s_waitcnt lgkmcnt(0)
	v_mfma_f32_16x16x32_bf16 v[114:117], v[18:21], v[14:17], 0
	ds_read_b128 v[14:17], v175 offset:4672
	ds_read_b128 v[118:121], v175 offset:13888
	v_mfma_f32_16x16x32_bf16 v[10:13], v[22:25], v[10:13], 0
	s_waitcnt lgkmcnt(1)
	v_mfma_f32_16x16x32_bf16 v[14:17], v[6:9], v[14:17], v[10:13]
	s_waitcnt lgkmcnt(0)
	v_mfma_f32_16x16x32_bf16 v[10:13], v[2:5], v[118:121], v[114:117]
	s_nop 2
	ds_read_b128 v[114:117], v176
	ds_read_b128 v[118:121], v176 offset:9216
	s_waitcnt lgkmcnt(1)
	v_mfma_f32_16x16x32_bf16 v[22:25], v[22:25], v[114:117], 0
	s_waitcnt lgkmcnt(0)
	v_mfma_f32_16x16x32_bf16 v[18:21], v[18:21], v[118:121], 0
	ds_read_b128 v[114:117], v176 offset:64
	ds_read_b128 v[118:121], v176 offset:9280
	s_waitcnt lgkmcnt(1)
	v_mfma_f32_16x16x32_bf16 v[6:9], v[6:9], v[114:117], v[22:25]
	ds_read2_b32 v[114:115], v174 offset0:192 offset1:208
	s_waitcnt lgkmcnt(0)
	s_nop 0
	v_add_f32_e32 v22, v30, v115
	v_mfma_f32_16x16x32_bf16 v[2:5], v[2:5], v[118:121], v[18:21]
	v_mul_f32_e32 v22, 0xbfb8aa3b, v22
	v_exp_f32_e32 v22, v22
	v_add_f32_e32 v23, v31, v115
	v_add_f32_e32 v18, v38, v114
	v_add_f32_e32 v19, v39, v114
	v_mul_f32_e32 v18, 0xbfb8aa3b, v18
	v_mul_f32_e32 v19, 0xbfb8aa3b, v19
	v_exp_f32_e32 v18, v18
	v_exp_f32_e32 v19, v19
	v_mul_f32_e32 v23, 0xbfb8aa3b, v23
	ds_read2_b32 v[24:25], v128 offset1:16
	ds_read2_b32 v[122:123], v128 offset0:64 offset1:80
	ds_read2_b32 v[124:125], v128 offset0:128 offset1:144
	ds_read2_b32 v[120:121], v128 offset0:192 offset1:208
	v_add_f32_e32 v18, 1.0, v18
	v_add_f32_e32 v19, 1.0, v19
	v_rcp_f32_e32 v20, v18
	v_rcp_f32_e32 v21, v19
	v_exp_f32_e32 v23, v23
	v_add_f32_e32 v22, 1.0, v22
	s_waitcnt lgkmcnt(3)
	v_add_f32_e32 v18, v34, v24
	v_pk_mul_f32 v[116:117], v[20:21], s[36:37]
	v_add_f32_e32 v20, v40, v114
	v_add_f32_e32 v21, v41, v114
	v_mul_f32_e32 v20, 0xbfb8aa3b, v20
	v_mul_f32_e32 v21, 0xbfb8aa3b, v21
	v_exp_f32_e32 v20, v20
	v_exp_f32_e32 v21, v21
	v_add_f32_e32 v19, v35, v24
	v_rcp_f32_e32 v30, v22
	v_add_f32_e32 v20, 1.0, v20
	v_add_f32_e32 v21, 1.0, v21
	v_rcp_f32_e32 v40, v20
	v_add_f32_e32 v20, v36, v24
	v_rcp_f32_e32 v36, v21
	v_add_f32_e32 v21, v37, v24
	v_add_f32_e32 v22, v26, v25
	v_add_f32_e32 v24, v32, v115
	v_add_f32_e32 v26, v33, v115
	v_mul_f32_e32 v24, 0xbfb8aa3b, v24
	v_mul_f32_e32 v26, 0xbfb8aa3b, v26
	v_add_f32_e32 v23, 1.0, v23
	v_exp_f32_e32 v24, v24
	v_exp_f32_e32 v26, v26
	v_rcp_f32_e32 v31, v23
	v_add_f32_e32 v23, v27, v25
	v_add_f32_e32 v24, 1.0, v24
	v_add_f32_e32 v26, 1.0, v26
	v_pk_mul_f32 v[118:119], v[30:31], s[36:37]
	v_rcp_f32_e32 v157, v24
	v_add_f32_e32 v24, v28, v25
	v_rcp_f32_e32 v162, v26
	v_add_f32_e32 v25, v29, v25
	ds_read2_b32 v[28:29], v174 offset0:224 offset1:240
	ds_read2_b32 v[30:31], v128 offset0:32 offset1:48
	ds_read2_b32 v[26:27], v128 offset0:96 offset1:112
	ds_read2_b32 v[34:35], v128 offset0:160 offset1:176
	ds_read2_b32 v[128:129], v128 offset0:224 offset1:240
	s_waitcnt lgkmcnt(4)
	v_add_f32_e32 v14, v14, v28
	v_add_f32_e32 v15, v15, v28
	v_mul_f32_e32 v14, 0xbfb8aa3b, v14
	v_mul_f32_e32 v15, 0xbfb8aa3b, v15
	v_exp_f32_e32 v14, v14
	v_exp_f32_e32 v15, v15
	v_add_f32_e32 v8, v8, v29
	v_add_f32_e32 v6, v6, v29
	v_add_f32_e32 v14, 1.0, v14
	v_add_f32_e32 v15, 1.0, v15
	v_rcp_f32_e32 v14, v14
	v_rcp_f32_e32 v15, v15
	v_add_f32_e32 v7, v7, v29
	v_mul_f32_e32 v8, 0xbfb8aa3b, v8
	v_mul_f32_e32 v6, 0xbfb8aa3b, v6
	v_pk_mul_f32 v[114:115], v[14:15], s[36:37]
	v_add_f32_e32 v14, v16, v28
	v_mul_f32_e32 v14, 0xbfb8aa3b, v14
	v_exp_f32_e32 v14, v14
	v_mul_f32_e32 v7, 0xbfb8aa3b, v7
	v_exp_f32_e32 v8, v8
	v_exp_f32_e32 v6, v6
	v_exp_f32_e32 v7, v7
	v_add_f32_e32 v14, 1.0, v14
	v_rcp_f32_e32 v163, v14
	v_add_f32_e32 v14, v17, v28
	v_mul_f32_e32 v14, 0xbfb8aa3b, v14
	v_add_f32_e32 v8, 1.0, v8
	v_exp_f32_e32 v14, v14
	v_add_f32_e32 v6, 1.0, v6
	v_add_f32_e32 v7, 1.0, v7
	v_rcp_f32_e32 v216, v8
	v_add_f32_e32 v8, v9, v29
	v_rcp_f32_e32 v6, v6
	v_rcp_f32_e32 v7, v7
	v_mul_f32_e32 v8, 0xbfb8aa3b, v8
	v_exp_f32_e32 v8, v8
	v_add_f32_e32 v14, 1.0, v14
	v_rcp_f32_e32 v215, v14
	v_pk_mul_f32 v[14:15], v[6:7], s[36:37]
	v_lshlrev_b32_e32 v7, 16, v152
	v_lshlrev_b32_e32 v6, 16, v127
	v_lshlrev_b32_e32 v17, 16, v151
	v_lshlrev_b32_e32 v16, 16, v126
	v_pk_add_f32 v[32:33], v[6:7], v[16:17] neg_lo:[0,1] neg_hi:[0,1]
	v_add_f32_e32 v8, 1.0, v8
	v_pk_fma_f32 v[126:127], v[112:113], v[32:33], v[16:17]
	v_lshlrev_b32_e32 v33, 16, v131
	v_lshlrev_b32_e32 v32, 16, v130
	v_rcp_f32_e32 v217, v8
	v_lshlrev_b32_e32 v9, 16, v150
	v_lshlrev_b32_e32 v8, 16, v148
	v_lshlrev_b32_e32 v29, 16, v149
	v_lshlrev_b32_e32 v28, 16, v101
	v_mul_f32_e32 v18, 0xbfb8aa3b, v18
	v_mul_f32_e32 v19, 0xbfb8aa3b, v19
	s_waitcnt lgkmcnt(3)
; #define LAS __attribute__((address_space(3)))
; DI float row16_sum(float v) { v += DPPF(v, 0xB1); v += DPPF(v, 0x4E); v += DPPF(v, 0x141); v += DPPF(v, 0x140); return v; }
; DI unsigned cvtpk(float lo, float hi) { const f2_t v = {lo, hi}; return __builtin_bit_cast(unsigned, __builtin_convertvector(v, bf2_t)); }
; DI void rwkv_r1_item(const Args& A, int l, LAS unsigned char* lds, int item, int& dh_staged, int tid, int wave, int lane) {
;     ...
;     for (int nt = 0; nt < 4; ++nt) { const int ch = hh * 64 + 16 * nt + fr;
;         const float w0v = prm[192 + 16 * nt + fr], a0v = prm[256 + 16 * nt + fr], kkw = prm[320 + 16 * nt + fr], kaw = prm[384 + 16 * nt + fr], rkw = prm[448 + 16 * nt + fr];
; #pragma unroll
;         for (int r = 0; r < 4; ++r) { const float x = w0v + wl[nt][r];
;             lw[nt][r] = -0.6065306597126334f * __builtin_amdgcn_rcpf(1.f + __expf(-x));
;             const float a = __builtin_amdgcn_rcpf(1.f + __expf(-(a0v + al[nt][r]))); alp[nt][r] = a;
;             const float k0 = ek[nt][r]; kap[nt][r] = k0 * kkw; ek[nt][r] = k0 * (1.f + (a - 1.f) * kaw);
;             ssq[r] += kap[nt][r] * kap[nt][r]; bsm[r] += er[nt][r] * ek[nt][r] * rkw; } }
; #pragma unroll
;     for (int r = 0; r < 4; ++r) {
;         ssq[r] = row16_sum(ssq[r]); bsm[r] = row16_sum(bsm[r]);
;         ssq[r] = __builtin_amdgcn_rsqf(fmaxf(ssq[r], 1e-24f)); }
;     { bf16* bon = (bf16*)(A.ws + WS_RKB);
; #pragma unroll
;       for (int nt = 0; nt < 4; ++nt)
; #pragma unroll
;           for (int r = 0; r < 4; ++r) { kap[nt][r] *= ssq[r]; MT[(4 * qd + r) * 72 + 16 * nt + fr] = (bf16)cvtpk(bsm[r] * ev[nt][r], 0.f); }
;       asm volatile("s_waitcnt lgkmcnt(0)" ::: "memory");
;       const int p = lane >> 2, c16 = (lane & 3) * 16; const LAS u32x4_t* sp = (const LAS u32x4_t*)(MT + p * 72 + c16); const u32x4_t w0 = sp[0], w1 = sp[1];
;       bf16* dst = bon + ((size_t)dir * NT + tok0 + sgn * p) * RW + hh * 64 + c16;
	v_add_f32_e32 v10, v10, v30
	v_add_f32_e32 v11, v11, v30
	v_add_f32_e32 v12, v12, v30
	v_add_f32_e32 v13, v13, v30
	v_add_f32_e32 v2, v2, v31
	v_add_f32_e32 v3, v3, v31
	v_pk_add_f32 v[32:33], v[32:33], v[6:7] neg_lo:[0,1] neg_hi:[0,1]
	v_add_f32_e32 v4, v4, v31
	v_add_f32_e32 v5, v5, v31
	v_pk_add_f32 v[30:31], v[8:9], v[28:29] neg_lo:[0,1] neg_hi:[0,1]
	v_pk_add_f32 v[16:17], v[16:17], v[8:9] neg_lo:[0,1] neg_hi:[0,1]
	v_exp_f32_e32 v18, v18
	v_exp_f32_e32 v19, v19
	v_pk_fma_f32 v[130:131], v[112:113], v[32:33], v[6:7]
	v_pk_fma_f32 v[150:151], v[112:113], v[30:31], v[28:29]
	v_pk_fma_f32 v[152:153], v[112:113], v[16:17], v[8:9]
	s_waitcnt lgkmcnt(2)
	v_pk_mul_f32 v[38:39], v[130:131], v[26:27]
	v_pk_mul_f32 v[6:7], v[126:127], v[26:27]
	v_pk_mul_f32 v[8:9], v[152:153], v[26:27]
	v_pk_mul_f32 v[16:17], v[150:151], v[26:27]
	v_mul_i32_i24_e32 v26, s69, v177
	v_ashrrev_i32_e32 v27, 31, v26
	v_lshl_add_u64 v[26:27], s[42:43], 0, v[26:27]
	v_mov_b64_e32 v[28:29], s[34:35]
	v_add_f32_e32 v18, 1.0, v18
	v_add_f32_e32 v19, 1.0, v19
	v_mul_f32_e32 v20, 0xbfb8aa3b, v20
	v_mul_f32_e32 v21, 0xbfb8aa3b, v21
	v_mad_u64_u32 v[28:29], s[42:43], v26, s0, v[28:29]
	v_rcp_f32_e32 v18, v18
	v_rcp_f32_e32 v19, v19
	v_exp_f32_e32 v20, v20
	v_exp_f32_e32 v21, v21
	v_mad_i32_i24 v29, v27, s0, v29
	v_lshl_add_u64 v[26:27], s[40:41], 1, v[28:29]
	v_mov_b32_e32 v101, v63
	v_lshl_add_u64 v[148:149], v[26:27], 0, v[100:101]
	v_sub_f32_e32 v117, v116, v117
	v_lshlrev_b32_e32 v27, 16, v142
	v_fmamk_f32 v218, v40, 0xbf1b4598, v117
	v_lshlrev_b32_e32 v26, 16, v136
	v_lshlrev_b32_e32 v29, 16, v143
	v_mov_b32_e32 v28, v27
	v_add_f32_e32 v20, 1.0, v20
	v_add_f32_e32 v21, 1.0, v21
	v_fmamk_f32 v219, v36, 0xbf1b4598, v218
	v_pk_add_f32 v[26:27], v[26:27], v[28:29] neg_lo:[0,1] neg_hi:[0,1]
	v_pk_add_f32 v[36:37], v[18:19], -1.0 op_sel_hi:[1,0]
	v_rcp_f32_e32 v20, v20
	v_rcp_f32_e32 v21, v21
	v_pk_fma_f32 v[26:27], v[106:107], v[26:27], v[28:29] op_sel_hi:[0,1,1]
	v_pk_fma_f32 v[36:37], v[124:125], v[36:37], 1.0 op_sel_hi:[0,1,0]
	v_pk_mul_f32 v[36:37], v[26:27], v[36:37]
	v_lshlrev_b32_e32 v41, 16, v137
	v_pk_mul_f32 v[136:137], v[26:27], v[122:123] op_sel_hi:[1,0]
	v_lshlrev_b32_e32 v26, 16, v155
	v_lshlrev_b32_e32 v27, 16, v109
	v_mul_f32_e32 v22, 0xbfb8aa3b, v22
	v_mul_f32_e32 v23, 0xbfb8aa3b, v23
	v_lshlrev_b32_e32 v40, 16, v156
	v_lshlrev_b32_e32 v113, 16, v139
	v_mov_b32_e32 v112, v41
	v_pk_mov_b32 v[28:29], v[28:29], v[26:27] op_sel:[1,0]
	v_exp_f32_e32 v22, v22
	v_exp_f32_e32 v23, v23
	v_pk_add_f32 v[40:41], v[40:41], v[112:113] neg_lo:[0,1] neg_hi:[0,1]
	v_pk_add_f32 v[28:29], v[28:29], v[26:27] neg_lo:[0,1] neg_hi:[0,1]
	v_pk_fma_f32 v[142:143], v[58:59], v[40:41], v[112:113] op_sel_hi:[0,1,1]
	v_pk_fma_f32 v[26:27], v[106:107], v[28:29], v[26:27] op_sel_hi:[0,1,1]
	v_pk_add_f32 v[28:29], v[20:21], -1.0 op_sel_hi:[1,0]
	v_pk_mul_f32 v[40:41], v[142:143], v[36:37]
	v_pk_fma_f32 v[28:29], v[124:125], v[28:29], 1.0 op_sel_hi:[0,1,0]
	v_fma_f32 v156, v120, v40, 0
	v_fma_f32 v220, v120, v41, 0
	v_pk_mul_f32 v[40:41], v[26:27], v[28:29]
	v_lshlrev_b32_e32 v28, 16, v145
	v_lshlrev_b32_e32 v29, 16, v144
	v_add_f32_e32 v22, 1.0, v22
	v_add_f32_e32 v23, 1.0, v23
	v_pk_mov_b32 v[112:113], v[112:113], v[28:29] op_sel:[1,0]
	v_rcp_f32_e32 v22, v22
	v_rcp_f32_e32 v23, v23
	v_pk_add_f32 v[112:113], v[112:113], v[28:29] neg_lo:[0,1] neg_hi:[0,1]
	v_mov_b32_e32 v109, v60
	v_pk_fma_f32 v[144:145], v[58:59], v[112:113], v[28:29] op_sel_hi:[0,1,1]
	v_pk_mul_f32 v[28:29], v[144:145], v[40:41]
	v_pk_mul_f32 v[112:113], v[26:27], v[122:123] op_sel_hi:[1,0]
	v_fma_f32 v222, v120, v28, 0
	v_pk_add_f32 v[26:27], v[108:109], v[60:61] neg_lo:[0,1] neg_hi:[0,1]
	v_mov_b32_e32 v28, v107
	v_lshlrev_b32_e32 v109, 16, v140
	v_pk_fma_f32 v[106:107], v[28:29], v[26:27], v[60:61] op_sel_hi:[0,1,1]
	v_pk_add_f32 v[26:27], v[22:23], -1.0 op_sel_hi:[1,0]
	v_mov_b32_e32 v58, v125
	v_lshlrev_b32_e32 v108, 16, v141
	v_lshlrev_b32_e32 v125, 16, v154
	v_mov_b32_e32 v124, v109
	v_pk_fma_f32 v[26:27], v[58:59], v[26:27], 1.0 op_sel_hi:[0,1,0]
	v_pk_add_f32 v[108:109], v[108:109], v[124:125] neg_lo:[0,1] neg_hi:[0,1]
	v_mov_b32_e32 v60, v59
	v_mul_f32_e32 v24, 0xbfb8aa3b, v24
	v_mul_f32_e32 v25, 0xbfb8aa3b, v25
	v_pk_mul_f32 v[26:27], v[106:107], v[26:27]
	v_pk_fma_f32 v[140:141], v[60:61], v[108:109], v[124:125] op_sel_hi:[0,1,1]
	v_exp_f32_e32 v24, v24
	v_exp_f32_e32 v25, v25
	v_pk_mul_f32 v[108:109], v[140:141], v[26:27]
	v_mov_b32_e32 v122, v136
	v_fmac_f32_e32 v156, v121, v108
	v_mov_b32_e32 v108, v123
	v_pk_mul_f32 v[106:107], v[106:107], v[108:109] op_sel_hi:[1,0]
	v_add_f32_e32 v24, 1.0, v24
	v_mov_b32_e32 v123, v106
	v_add_f32_e32 v25, 1.0, v25
	v_pk_mul_f32 v[122:123], v[122:123], v[122:123]
	v_rcp_f32_e32 v24, v24
	v_rcp_f32_e32 v25, v25
	v_pk_mul_f32 v[32:33], v[38:39], v[38:39]
	v_fma_f32 v221, v120, v29, 0
	v_mov_b32_e32 v154, v137
	v_mov_b32_e32 v155, v107
	v_add_f32_e32 v29, v122, v123
	v_pk_mul_f32 v[154:155], v[154:155], v[154:155]
	v_add_f32_e32 v29, v29, v32
	v_pk_mul_f32 v[158:159], v[6:7], v[6:7]
	v_add_f32_e32 v224, v29, v33
	v_add_f32_e32 v29, v154, v155
	v_pk_mov_b32 v[32:33], v[60:61], v[104:105] op_sel:[1,0]
	v_add_f32_e32 v29, v29, v158
	v_pk_add_f32 v[32:33], v[32:33], v[104:105] neg_lo:[0,1] neg_hi:[0,1]
	v_mul_f32_e32 v10, 0xbfb8aa3b, v10
	v_mul_f32_e32 v11, 0xbfb8aa3b, v11
	v_add_f32_e32 v158, v29, v159
	v_pk_fma_f32 v[32:33], v[28:29], v[32:33], v[104:105] op_sel_hi:[0,1,1]
	v_pk_add_f32 v[28:29], v[24:25], -1.0 op_sel_hi:[1,0]
	v_exp_f32_e32 v10, v10
	v_exp_f32_e32 v11, v11
	v_pk_fma_f32 v[28:29], v[58:59], v[28:29], 1.0 op_sel_hi:[0,1,0]
	v_pk_mul_f32 v[122:123], v[32:33], v[108:109] op_sel_hi:[1,0]
	v_pk_mul_f32 v[28:29], v[32:33], v[28:29]
	v_mov_b32_e32 v32, v113
	v_mov_b32_e32 v33, v123
	v_pk_mul_f32 v[32:33], v[32:33], v[32:33]
	v_pk_mul_f32 v[160:161], v[16:17], v[16:17]
	v_add_f32_e32 v32, v32, v33
	v_add_f32_e32 v10, 1.0, v10
	v_add_f32_e32 v11, 1.0, v11
	v_add_f32_e32 v32, v32, v160
	v_rcp_f32_e32 v10, v10
	v_rcp_f32_e32 v11, v11
	v_add_f32_e32 v154, v32, v161
	v_mov_b32_e32 v32, v112
	v_mov_b32_e32 v33, v122
	v_mul_f32_e32 v12, 0xbfb8aa3b, v12
	v_mul_f32_e32 v13, 0xbfb8aa3b, v13
	v_pk_mul_f32 v[32:33], v[32:33], v[32:33]
	v_exp_f32_e32 v12, v12
	v_exp_f32_e32 v13, v13
	v_pk_mul_f32 v[30:31], v[8:9], v[8:9]
	v_lshlrev_b32_e32 v58, 16, v138
	v_lshlrev_b32_e32 v59, 16, v135
	v_add_f32_e32 v32, v32, v33
	v_pk_mov_b32 v[104:105], v[124:125], v[58:59] op_sel:[1,0]
	v_add_f32_e32 v30, v32, v30
	v_pk_add_f32 v[104:105], v[104:105], v[58:59] neg_lo:[0,1] neg_hi:[0,1]
	v_add_f32_e32 v155, v30, v31
	v_pk_add_f32 v[30:31], v[10:11], -1.0 op_sel_hi:[1,0]
	v_pk_fma_f32 v[138:139], v[60:61], v[104:105], v[58:59] op_sel_hi:[0,1,1]
	s_waitcnt lgkmcnt(1)
; DI float row16_sum(float v) { v += DPPF(v, 0xB1); v += DPPF(v, 0x4E); v += DPPF(v, 0x141); v += DPPF(v, 0x140); return v; }
; DI unsigned cvtpk(float lo, float hi) { const f2_t v = {lo, hi}; return __builtin_bit_cast(unsigned, __builtin_convertvector(v, bf2_t)); }
; DI void rwkv_r1_item(const Args& A, int l, LAS unsigned char* lds, int item, int& dh_staged, int tid, int wave, int lane) {
;     ...
;         for (int r = 0; r < 4; ++r) { const float x = w0v + wl[nt][r];
;             lw[nt][r] = -0.6065306597126334f * __builtin_amdgcn_rcpf(1.f + __expf(-x));
;             const float a = __builtin_amdgcn_rcpf(1.f + __expf(-(a0v + al[nt][r]))); alp[nt][r] = a;
;             const float k0 = ek[nt][r]; kap[nt][r] = k0 * kkw; ek[nt][r] = k0 * (1.f + (a - 1.f) * kaw);
;             ssq[r] += kap[nt][r] * kap[nt][r]; bsm[r] += er[nt][r] * ek[nt][r] * rkw; } }
; #pragma unroll
;     for (int r = 0; r < 4; ++r) {
;         ssq[r] = row16_sum(ssq[r]); bsm[r] = row16_sum(bsm[r]);
;         ssq[r] = __builtin_amdgcn_rsqf(fmaxf(ssq[r], 1e-24f)); }
;     { bf16* bon = (bf16*)(A.ws + WS_RKB);
; #pragma unroll
;       for (int nt = 0; nt < 4; ++nt)
; #pragma unroll
;           for (int r = 0; r < 4; ++r) { kap[nt][r] *= ssq[r]; MT[(4 * qd + r) * 72 + 16 * nt + fr] = (bf16)cvtpk(bsm[r] * ev[nt][r], 0.f); }
;       asm volatile("s_waitcnt lgkmcnt(0)" ::: "memory");
	v_pk_fma_f32 v[30:31], v[34:35], v[30:31], 1.0 op_sel_hi:[0,1,0]
	v_mov_b32_e32 v32, v130
	v_mov_b32_e32 v33, v126
	v_add_f32_e32 v12, 1.0, v12
	v_add_f32_e32 v13, 1.0, v13
	v_pk_mul_f32 v[58:59], v[138:139], v[28:29]
	v_pk_mul_f32 v[30:31], v[32:33], v[30:31]
	v_lshlrev_b32_e32 v33, 16, v132
	v_rcp_f32_e32 v12, v12
	v_rcp_f32_e32 v13, v13
	v_fmac_f32_e32 v221, v121, v59
	v_fmac_f32_e32 v222, v121, v58
	v_lshlrev_b32_e32 v32, 16, v133
	v_lshlrev_b32_e32 v59, 16, v134
	v_mov_b32_e32 v58, v33
	v_mul_f32_e32 v2, 0xbfb8aa3b, v2
	v_mul_f32_e32 v3, 0xbfb8aa3b, v3
	v_pk_add_f32 v[32:33], v[32:33], v[58:59] neg_lo:[0,1] neg_hi:[0,1]
	v_exp_f32_e32 v2, v2
	v_exp_f32_e32 v3, v3
	v_fmac_f32_e32 v220, v121, v109
	v_pk_fma_f32 v[120:121], v[110:111], v[32:33], v[58:59] op_sel_hi:[0,1,1]
	v_pk_mul_f32 v[32:33], v[120:121], v[30:31]
	v_mov_b32_e32 v60, v152
	s_waitcnt lgkmcnt(0)
	v_fmac_f32_e32 v156, v128, v32
	v_fmac_f32_e32 v220, v128, v33
	v_pk_add_f32 v[32:33], v[12:13], -1.0 op_sel_hi:[1,0]
	v_mov_b32_e32 v61, v150
	v_pk_fma_f32 v[32:33], v[34:35], v[32:33], 1.0 op_sel_hi:[0,1,0]
	v_add_f32_e32 v2, 1.0, v2
	v_add_f32_e32 v3, 1.0, v3
	v_pk_mul_f32 v[32:33], v[60:61], v[32:33]
	v_lshlrev_b32_e32 v60, 16, v97
	v_lshlrev_b32_e32 v61, 16, v95
	v_rcp_f32_e32 v2, v2
	v_rcp_f32_e32 v3, v3
	v_pk_mov_b32 v[58:59], v[58:59], v[60:61] op_sel:[1,0]
	v_mov_b32_e32 v124, v38
	v_pk_add_f32 v[58:59], v[58:59], v[60:61] neg_lo:[0,1] neg_hi:[0,1]
	v_mov_b32_e32 v38, v35
	v_pk_fma_f32 v[132:133], v[110:111], v[58:59], v[60:61] op_sel_hi:[0,1,1]
	v_pk_mul_f32 v[58:59], v[132:133], v[32:33]
	v_lshlrev_b32_e32 v61, 16, v103
	v_fmac_f32_e32 v221, v128, v59
	v_fmac_f32_e32 v222, v128, v58
	v_pk_add_f32 v[58:59], v[2:3], -1.0 op_sel_hi:[1,0]
	v_mov_b32_e32 v126, v131
	v_pk_fma_f32 v[34:35], v[38:39], v[58:59], 1.0 op_sel_hi:[0,1,0]
	v_lshlrev_b32_e32 v59, 16, v93
	v_lshlrev_b32_e32 v58, 16, v89
	v_mov_b32_e32 v60, v59
	v_pk_add_f32 v[58:59], v[58:59], v[60:61] neg_lo:[0,1] neg_hi:[0,1]
	v_mov_b32_e32 v104, v111
	v_pk_mul_f32 v[34:35], v[126:127], v[34:35]
	v_pk_fma_f32 v[126:127], v[104:105], v[58:59], v[60:61] op_sel_hi:[0,1,1]
	v_pk_mul_f32 v[58:59], v[126:127], v[34:35]
	v_mov_b32_e32 v125, v6
	v_fmac_f32_e32 v156, v129, v58
	v_fmac_f32_e32 v220, v129, v59
	v_mul_f32_e32 v4, 0xbfb8aa3b, v4
	v_add_f32_dpp v6, v156, v156 quad_perm:[1,0,3,2] row_mask:0xf bank_mask:0xf bound_ctrl:1
	v_add_f32_dpp v58, v220, v220 quad_perm:[1,0,3,2] row_mask:0xf bank_mask:0xf bound_ctrl:1
	v_mul_f32_e32 v5, 0xbfb8aa3b, v5
	v_add_f32_dpp v6, v6, v6 quad_perm:[2,3,0,1] row_mask:0xf bank_mask:0xf bound_ctrl:1
	v_add_f32_dpp v58, v58, v58 quad_perm:[2,3,0,1] row_mask:0xf bank_mask:0xf bound_ctrl:1
	v_exp_f32_e32 v4, v4
	v_add_f32_dpp v6, v6, v6 row_half_mirror row_mask:0xf bank_mask:0xf bound_ctrl:1
	v_add_f32_dpp v58, v58, v58 row_half_mirror row_mask:0xf bank_mask:0xf bound_ctrl:1
	v_exp_f32_e32 v5, v5
	v_add_f32_dpp v6, v6, v6 row_mirror row_mask:0xf bank_mask:0xf bound_ctrl:1
	v_mul_f32_e32 v59, v46, v6
	v_add_f32_dpp v58, v58, v58 row_mirror row_mask:0xf bank_mask:0xf bound_ctrl:1
	v_cvt_pk_bf16_f32 v59, v59, s0
	ds_write_b16 v205, v59 offset:28800
	v_mul_f32_e32 v59, v47, v58
	v_cvt_pk_bf16_f32 v59, v59, s0
	ds_write_b16 v206, v59 offset:28800
	v_mul_f32_e32 v59, v42, v6
	v_cvt_pk_bf16_f32 v59, v59, s0
	ds_write_b16 v205, v59 offset:28832
	v_mul_f32_e32 v59, v43, v58
	v_cvt_pk_bf16_f32 v59, v59, s0
	v_add_f32_e32 v4, 1.0, v4
	v_add_f32_e32 v5, 1.0, v5
	ds_write_b16 v206, v59 offset:28832
	v_mul_f32_e32 v59, v50, v6
	v_rcp_f32_e32 v4, v4
	v_rcp_f32_e32 v5, v5
	v_cvt_pk_bf16_f32 v59, v59, s0
	ds_write_b16 v205, v59 offset:28864
	v_mul_f32_e32 v59, v51, v58
	v_mul_f32_e32 v6, v54, v6
	v_cvt_pk_bf16_f32 v59, v59, s0
	v_cvt_pk_bf16_f32 v6, v6, s0
	ds_write_b16 v206, v59 offset:28864
	ds_write_b16 v205, v6 offset:28896
	v_mul_f32_e32 v6, v55, v58
	v_cvt_pk_bf16_f32 v6, v6, s0
	v_pk_add_f32 v[58:59], v[4:5], -1.0 op_sel_hi:[1,0]
	ds_write_b16 v206, v6 offset:28896
	v_mov_b32_e32 v6, v39
	v_pk_fma_f32 v[38:39], v[38:39], v[58:59], 1.0 op_sel_hi:[0,1,0]
	v_lshlrev_b32_e32 v58, 16, v99
	v_lshlrev_b32_e32 v59, 16, v91
	v_pk_mov_b32 v[60:61], v[60:61], v[58:59] op_sel:[1,0]
	v_mov_b32_e32 v150, v153
	v_pk_add_f32 v[60:61], v[60:61], v[58:59] neg_lo:[0,1] neg_hi:[0,1]
	v_pk_mul_f32 v[38:39], v[150:151], v[38:39]
	v_pk_fma_f32 v[130:131], v[104:105], v[60:61], v[58:59] op_sel_hi:[0,1,1]
	v_pk_mul_f32 v[58:59], v[130:131], v[38:39]
	v_sub_f32_e32 v223, v118, v119
	v_fmac_f32_e32 v221, v129, v59
	v_fmac_f32_e32 v222, v129, v58
	v_fmamk_f32 v157, v157, 0xbf1b4598, v223
	v_add_f32_dpp v59, v221, v221 quad_perm:[1,0,3,2] row_mask:0xf bank_mask:0xf bound_ctrl:1
	v_add_f32_dpp v58, v222, v222 quad_perm:[1,0,3,2] row_mask:0xf bank_mask:0xf bound_ctrl:1
	v_fmamk_f32 v162, v162, 0xbf1b4598, v157
	v_add_f32_dpp v59, v59, v59 quad_perm:[2,3,0,1] row_mask:0xf bank_mask:0xf bound_ctrl:1
	v_add_f32_dpp v58, v58, v58 quad_perm:[2,3,0,1] row_mask:0xf bank_mask:0xf bound_ctrl:1
	v_sub_f32_e32 v115, v114, v115
	v_add_f32_dpp v59, v59, v59 row_half_mirror row_mask:0xf bank_mask:0xf bound_ctrl:1
	v_add_f32_dpp v58, v58, v58 row_half_mirror row_mask:0xf bank_mask:0xf bound_ctrl:1
	v_fmamk_f32 v119, v163, 0xbf1b4598, v115
	v_add_f32_dpp v59, v59, v59 row_mirror row_mask:0xf bank_mask:0xf bound_ctrl:1
	v_mul_f32_e32 v60, v49, v59
	v_cvt_pk_bf16_f32 v60, v60, s0
	ds_write_b16 v206, v60 offset:29088
	v_mul_f32_e32 v60, v45, v59
	v_cvt_pk_bf16_f32 v60, v60, s0
	ds_write_b16 v206, v60 offset:29120
	v_mul_f32_e32 v60, v53, v59
	v_mul_f32_e32 v59, v57, v59
	v_cvt_pk_bf16_f32 v59, v59, s0
	v_add_f32_dpp v58, v58, v58 row_mirror row_mask:0xf bank_mask:0xf bound_ctrl:1
	ds_write_b16 v206, v59 offset:29184
	v_mul_f32_e32 v59, v48, v58
	v_cvt_pk_bf16_f32 v59, v59, s0
	ds_write_b16 v206, v59 offset:28944
	v_mul_f32_e32 v59, v44, v58
	v_cvt_pk_bf16_f32 v59, v59, s0
	ds_write_b16 v206, v59 offset:28976
	v_mul_f32_e32 v59, v52, v58
	v_mul_f32_e32 v58, v56, v58
	v_cvt_pk_bf16_f32 v60, v60, s0
	v_cvt_pk_bf16_f32 v59, v59, s0
	v_cvt_pk_bf16_f32 v58, v58, s0
	ds_write_b16 v206, v60 offset:29152
	ds_write_b16 v206, v59 offset:29008
	ds_write_b16 v206, v58 offset:29040
	s_waitcnt lgkmcnt(0)
; #define LAS __attribute__((address_space(3)))
; DI void rwkv_r1_item(const Args& A, int l, LAS unsigned char* lds, int item, int& dh_staged, int tid, int wave, int lane) {
;     ...
;       const int p = lane >> 2, c16 = (lane & 3) * 16; const LAS u32x4_t* sp = (const LAS u32x4_t*)(MT + p * 72 + c16); const u32x4_t w0 = sp[0], w1 = sp[1];
;       bf16* dst = bon + ((size_t)dir * NT + tok0 + sgn * p) * RW + hh * 64 + c16;
;       *(u32x4_t*)dst = w0; *(u32x4_t*)(dst + 8) = w1;
;       asm volatile("s_waitcnt lgkmcnt(0)" ::: "memory"); }
;     unsigned char* pkg = A.ws + WS_PKG + ((size_t)((dir * NB + b) * 6 + hh) * 128 + cc) * PKG_BYTES;
;     float lend[4];
;     u32x2_t btf[4], ktf[4];
; #pragma unroll
;     for (int nt = 0; nt < 4; ++nt) { float lam[4]; lam[0] = lw[nt][0]; lam[1] = lam[0] + lw[nt][1]; lam[2] = lam[1] + lw[nt][2]; lam[3] = lam[2] + lw[nt][3];
;         const float t1 = __shfl(lam[3], lane - 16), t2 = __shfl(lam[3], lane - 32), t3 = __shfl(lam[3], lane - 48);
;         const float off = (qd >= 1 ? t1 : 0.f) + (qd >= 2 ? t2 : 0.f) + (qd >= 3 ? t3 : 0.f);
; #pragma unroll
;         for (int r = 0; r < 4; ++r) lam[r] += off;
;         lend[nt] = __shfl(lam[3], 48 + fr);
;         float bt4[4], kt4[4];
;         float epv[4];
; #pragma unroll
;         for (int r = 0; r < 4; ++r) epv[r] = __expf(lam[r]);
;         float ep_prev = __shfl(epv[3], lane - 16); if (qd == 0) ep_prev = 1.f;
;         const float eendall = __expf(lend[nt]);
;         float ia[4], ir[4], ib[4], ik[4];
; #pragma unroll
;         for (int r = 0; r < 4; ++r) { const float ep = epv[r], epm = r ? epv[r - 1] : ep_prev, einv = __builtin_amdgcn_rcpf(ep), eend = eendall * einv;
;             const float bb = kap[nt][r] * alp[nt][r];
;             ia[r] = -kap[nt][r] * epm; ir[r] = er[nt][r] * ep; ib[r] = bb * einv; ik[r] = ek[nt][r] * einv;
;             bt4[r] = bb * eend; kt4[r] = ek[nt][r] * eend; }
; #pragma unroll
;         for (int r = 0; r < 4; r += 2) { const int o = (4 * qd + r) * 72 + 16 * nt + fr;
;             const unsigned pa_ = cvtpk(ia[r], ia[r + 1]), pr_ = cvtpk(ir[r], ir[r + 1]), pb_ = cvtpk(ib[r], ib[r + 1]), pk_ = cvtpk(ik[r], ik[r + 1]);
;             IMG[o] = (bf16)pa_; IMG[o + 72] = (bf16)(pa_ >> 16); IMG[1152 + o] = (bf16)pr_; IMG[1152 + o + 72] = (bf16)(pr_ >> 16);
	ds_read_b128 v[58:61], v178 offset:28800
	ds_read_b128 v[108:111], v178 offset:28816
	s_waitcnt lgkmcnt(1)
	global_store_dwordx4 v[148:149], v[58:61], off
	s_waitcnt lgkmcnt(0)
	global_store_dwordx4 v[148:149], v[108:111], off offset:16
	v_or_b32_e32 v58, v207, v146
	v_lshlrev_b32_e32 v58, 2, v58
	v_xor_b32_e32 v97, 0x80, v58
	v_or_b32_e32 v58, v207, v68
	v_lshlrev_b32_e32 v95, 2, v58
	ds_bpermute_b32 v58, v208, v219
	ds_bpermute_b32 v59, v97, v219
	ds_bpermute_b32 v60, v209, v219
	s_waitcnt lgkmcnt(0)
	v_fmamk_f32 v101, v215, 0xbf1b4598, v119
	s_waitcnt lgkmcnt(2)
	v_cndmask_b32_e64 v58, v58, 0, s[8:9]
	s_waitcnt lgkmcnt(1)
	v_cndmask_b32_e64 v59, 0, v59, s[12:13]
	v_add_f32_e32 v58, v58, v59
	s_waitcnt lgkmcnt(0)
	v_cndmask_b32_e64 v59, 0, v60, s[14:15]
	v_add_f32_e32 v58, v58, v59
	v_add_f32_e32 v59, v116, v58
	v_add_f32_e32 v60, v117, v58
	v_add_f32_e32 v61, v218, v58
	v_add_f32_e32 v89, v219, v58
	v_mul_f32_e32 v58, 0x3fb8aa3b, v59
	v_mul_f32_e32 v59, 0x3fb8aa3b, v60
	v_mul_f32_e32 v60, 0x3fb8aa3b, v61
	v_exp_f32_e32 v104, v60
	v_mul_f32_e32 v60, 0x3fb8aa3b, v89
	v_exp_f32_e32 v105, v60
	v_exp_f32_e32 v58, v58
	v_exp_f32_e32 v59, v59
	v_rcp_f32_e32 v108, v104
	ds_bpermute_b32 v60, v208, v105
	v_rcp_f32_e32 v109, v105
	v_rcp_f32_e32 v61, v59
	v_pk_mul_f32 v[116:117], v[142:143], v[58:59]
	ds_bpermute_b32 v91, v95, v89
	s_waitcnt lgkmcnt(1)
	v_cndmask_b32_e64 v110, v60, 1.0, s[8:9]
	v_rcp_f32_e32 v60, v58
	v_mov_b32_e32 v111, v58
	v_pk_mul_f32 v[142:143], v[144:145], v[104:105]
	v_mov_b32_e32 v144, v59
	v_pk_mul_f32 v[128:129], v[36:37], v[60:61]
	v_pk_mul_f32 v[58:59], v[40:41], v[108:109]
	v_cvt_pk_bf16_f32 v89, v116, v117
	v_cvt_pk_bf16_f32 v93, v128, v129
	ds_write_b16 v205, v89 offset:20736
	ds_write_b16_d16_hi v205, v89 offset:20880
	ds_write_b16 v205, v93 offset:25344
	ds_write_b16_d16_hi v205, v93 offset:25488
	v_cvt_pk_bf16_f32 v89, v142, v143
	v_cvt_pk_bf16_f32 v58, v58, v59
	ds_write_b16 v206, v89 offset:20880
	ds_write_b16_d16_hi v206, v89 offset:21024
	ds_write_b16 v206, v58 offset:25488
	ds_write_b16_d16_hi v206, v58 offset:25632
	ds_bpermute_b32 v58, v208, v162
	ds_bpermute_b32 v59, v97, v162
	ds_bpermute_b32 v89, v209, v162
	v_mov_b32_e32 v145, v104
	v_mov_b32_e32 v134, v8
	s_waitcnt lgkmcnt(2)
	v_cndmask_b32_e64 v58, v58, 0, s[8:9]
	s_waitcnt lgkmcnt(1)
	v_cndmask_b32_e64 v59, 0, v59, s[12:13]
	v_add_f32_e32 v58, v58, v59
	s_waitcnt lgkmcnt(0)
	v_cndmask_b32_e64 v59, 0, v89, s[14:15]
	v_add_f32_e32 v58, v58, v59
	v_add_f32_e32 v59, v118, v58
	v_add_f32_e32 v93, v223, v58
	v_mul_f32_e32 v59, 0x3fb8aa3b, v59
	v_exp_f32_e32 v142, v59
	v_mul_f32_e32 v59, 0x3fb8aa3b, v93
	v_add_f32_dpp v93, v224, v224 quad_perm:[1,0,3,2] row_mask:0xf bank_mask:0xf bound_ctrl:1
	v_add_f32_e32 v99, v157, v58
	v_add_f32_e32 v58, v162, v58
	v_add_f32_dpp v93, v93, v93 quad_perm:[2,3,0,1] row_mask:0xf bank_mask:0xf bound_ctrl:1
	ds_bpermute_b32 v89, v95, v58
	v_mul_f32_e32 v58, 0x3fb8aa3b, v58
	v_add_f32_dpp v93, v93, v93 row_half_mirror row_mask:0xf bank_mask:0xf bound_ctrl:1
	v_exp_f32_e32 v149, v58
	v_exp_f32_e32 v143, v59
	v_add_f32_dpp v93, v93, v93 row_mirror row_mask:0xf bank_mask:0xf bound_ctrl:1
	v_max_f32_e32 v93, 0x179abe15, v93
	v_rsq_f32_e32 v128, v93
	ds_bpermute_b32 v58, v208, v149
	v_add_f32_dpp v93, v158, v158 quad_perm:[1,0,3,2] row_mask:0xf bank_mask:0xf bound_ctrl:1
	v_mul_f32_e32 v59, 0x3fb8aa3b, v99
	v_exp_f32_e32 v148, v59
	v_add_f32_dpp v93, v93, v93 quad_perm:[2,3,0,1] row_mask:0xf bank_mask:0xf bound_ctrl:1
	s_waitcnt lgkmcnt(0)
	v_cndmask_b32_e64 v150, v58, 1.0, s[8:9]
	v_mov_b32_e32 v151, v142
	v_add_f32_dpp v93, v93, v93 row_half_mirror row_mask:0xf bank_mask:0xf bound_ctrl:1
	v_rcp_f32_e32 v58, v142
	v_rcp_f32_e32 v59, v143
	v_add_f32_dpp v93, v93, v93 row_mirror row_mask:0xf bank_mask:0xf bound_ctrl:1
	v_max_f32_e32 v93, 0x179abe15, v93
	v_rsq_f32_e32 v129, v93
	v_pk_mul_f32 v[140:141], v[140:141], v[142:143]
	v_pk_mul_f32 v[138:139], v[138:139], v[148:149]
	v_mov_b32_e32 v135, v16
	v_pk_mul_f32 v[104:105], v[136:137], v[128:129]
	v_pk_mul_f32 v[106:107], v[106:107], v[128:129]
	v_pk_mul_f32 v[116:117], v[18:19], v[104:105]
	v_pk_mul_f32 v[18:19], v[110:111], v[104:105] neg_lo:[0,1] neg_hi:[0,1]
	v_pk_mul_f32 v[104:105], v[116:117], v[60:61]
	v_cvt_pk_bf16_f32 v18, v18, v19
	v_cvt_pk_bf16_f32 v19, v104, v105
	ds_write_b16 v205, v18 offset:18432
	ds_write_b16_d16_hi v205, v18 offset:18576
	ds_write_b16 v205, v19 offset:23040
	ds_write_b16_d16_hi v205, v19 offset:23184
	v_add_f32_dpp v18, v154, v154 quad_perm:[1,0,3,2] row_mask:0xf bank_mask:0xf bound_ctrl:1
	v_pk_mul_f32 v[104:105], v[22:23], v[106:107]
	v_pk_mul_f32 v[22:23], v[150:151], v[106:107] neg_lo:[0,1] neg_hi:[0,1]
	v_add_f32_dpp v18, v18, v18 quad_perm:[2,3,0,1] row_mask:0xf bank_mask:0xf bound_ctrl:1
	v_rcp_f32_e32 v106, v148
	v_rcp_f32_e32 v107, v149
	v_add_f32_dpp v18, v18, v18 row_half_mirror row_mask:0xf bank_mask:0xf bound_ctrl:1
	v_pk_mul_f32 v[136:137], v[104:105], v[58:59]
	v_pk_mul_f32 v[150:151], v[26:27], v[58:59]
	v_add_f32_dpp v18, v18, v18 row_mirror row_mask:0xf bank_mask:0xf bound_ctrl:1
	v_max_f32_e32 v18, 0x179abe15, v18
	v_rsq_f32_e32 v19, v18
	v_cvt_pk_bf16_f32 v22, v22, v23
	v_add_f32_dpp v18, v155, v155 quad_perm:[1,0,3,2] row_mask:0xf bank_mask:0xf bound_ctrl:1
	v_cvt_pk_bf16_f32 v23, v140, v141
	v_cvt_pk_bf16_f32 v93, v136, v137
	v_add_f32_dpp v18, v18, v18 quad_perm:[2,3,0,1] row_mask:0xf bank_mask:0xf bound_ctrl:1
	v_cvt_pk_bf16_f32 v99, v150, v151
	v_sub_f32_e32 v15, v14, v15
	v_add_f32_dpp v18, v18, v18 row_half_mirror row_mask:0xf bank_mask:0xf bound_ctrl:1
	v_fmamk_f32 v16, v216, 0xbf1b4598, v15
	v_fmamk_f32 v8, v217, 0xbf1b4598, v16
; DI unsigned cvtpk(float lo, float hi) { const f2_t v = {lo, hi}; return __builtin_bit_cast(unsigned, __builtin_convertvector(v, bf2_t)); }
; DI void rwkv_r1_item(const Args& A, int l, LAS unsigned char* lds, int item, int& dh_staged, int tid, int wave, int lane) {
;     ...
;     for (int nt = 0; nt < 4; ++nt) { float lam[4]; lam[0] = lw[nt][0]; lam[1] = lam[0] + lw[nt][1]; lam[2] = lam[1] + lw[nt][2]; lam[3] = lam[2] + lw[nt][3];
;         const float t1 = __shfl(lam[3], lane - 16), t2 = __shfl(lam[3], lane - 32), t3 = __shfl(lam[3], lane - 48);
;         const float off = (qd >= 1 ? t1 : 0.f) + (qd >= 2 ? t2 : 0.f) + (qd >= 3 ? t3 : 0.f);
; #pragma unroll
;         for (int r = 0; r < 4; ++r) lam[r] += off;
;         lend[nt] = __shfl(lam[3], 48 + fr);
;         float bt4[4], kt4[4];
;         float epv[4];
; #pragma unroll
;         for (int r = 0; r < 4; ++r) epv[r] = __expf(lam[r]);
;         float ep_prev = __shfl(epv[3], lane - 16); if (qd == 0) ep_prev = 1.f;
;         const float eendall = __expf(lend[nt]);
;         float ia[4], ir[4], ib[4], ik[4];
; #pragma unroll
;         for (int r = 0; r < 4; ++r) { const float ep = epv[r], epm = r ? epv[r - 1] : ep_prev, einv = __builtin_amdgcn_rcpf(ep), eend = eendall * einv;
;             const float bb = kap[nt][r] * alp[nt][r];
;             ia[r] = -kap[nt][r] * epm; ir[r] = er[nt][r] * ep; ib[r] = bb * einv; ik[r] = ek[nt][r] * einv;
;             bt4[r] = bb * eend; kt4[r] = ek[nt][r] * eend; }
; #pragma unroll
;         for (int r = 0; r < 4; r += 2) { const int o = (4 * qd + r) * 72 + 16 * nt + fr;
;             const unsigned pa_ = cvtpk(ia[r], ia[r + 1]), pr_ = cvtpk(ir[r], ir[r + 1]), pb_ = cvtpk(ib[r], ib[r + 1]), pk_ = cvtpk(ik[r], ik[r + 1]);
;             IMG[o] = (bf16)pa_; IMG[o + 72] = (bf16)(pa_ >> 16); IMG[1152 + o] = (bf16)pr_; IMG[1152 + o + 72] = (bf16)(pr_ >> 16);
;             IMG[2304 + o] = (bf16)pb_; IMG[2304 + o + 72] = (bf16)(pb_ >> 16); IMG[3456 + o] = (bf16)pk_; IMG[3456 + o + 72] = (bf16)(pk_ >> 16); }
;         btf[nt].x = cvtpk(bt4[0], bt4[1]); btf[nt].y = cvtpk(bt4[2], bt4[3]); ktf[nt].x = cvtpk(kt4[0], kt4[1]); ktf[nt].y = cvtpk(kt4[2], kt4[3]); }
	v_add_f32_dpp v18, v18, v18 row_mirror row_mask:0xf bank_mask:0xf bound_ctrl:1
	v_max_f32_e32 v18, 0x179abe15, v18
	v_rsq_f32_e32 v18, v18
	v_pk_mul_f32 v[6:7], v[6:7], v[128:129]
	v_mov_b32_e32 v222, s96
	v_readlane_b32 s0, v234, 5
	v_pk_mul_f32 v[110:111], v[112:113], v[18:19]
	v_pk_mul_f32 v[112:113], v[122:123], v[18:19]
	v_pk_mul_f32 v[122:123], v[20:21], v[110:111]
	v_pk_mul_f32 v[20:21], v[144:145], v[110:111] neg_lo:[0,1] neg_hi:[0,1]
	v_pk_mul_f32 v[110:111], v[122:123], v[108:109]
	v_cvt_pk_bf16_f32 v20, v20, v21
	v_cvt_pk_bf16_f32 v21, v110, v111
	ds_write_b16 v206, v20 offset:18576
	ds_write_b16_d16_hi v206, v20 offset:18720
	ds_write_b16 v206, v21 offset:23184
	ds_write_b16_d16_hi v206, v21 offset:23328
	v_mov_b32_e32 v20, v143
	v_mov_b32_e32 v21, v148
	v_pk_mul_f32 v[110:111], v[24:25], v[112:113]
	v_pk_mul_f32 v[20:21], v[20:21], v[112:113] neg_lo:[0,1] neg_hi:[0,1]
	v_pk_mul_f32 v[24:25], v[110:111], v[106:107]
	v_pk_mul_f32 v[112:113], v[28:29], v[106:107]
	v_cvt_pk_bf16_f32 v20, v20, v21
	v_cvt_pk_bf16_f32 v21, v138, v139
	ds_write_b16 v205, v22 offset:18464
	ds_write_b16_d16_hi v205, v22 offset:18608
	ds_write_b16 v205, v23 offset:20768
	ds_write_b16_d16_hi v205, v23 offset:20912
	ds_write_b16 v205, v93 offset:23072
	ds_write_b16_d16_hi v205, v93 offset:23216
	ds_write_b16 v205, v99 offset:25376
	ds_write_b16_d16_hi v205, v99 offset:25520
	v_cvt_pk_bf16_f32 v22, v24, v25
	v_cvt_pk_bf16_f32 v23, v112, v113
	ds_write_b16 v206, v20 offset:18608
	ds_write_b16_d16_hi v206, v20 offset:18752
	ds_write_b16 v206, v21 offset:20912
	ds_write_b16_d16_hi v206, v21 offset:21056
	ds_write_b16 v206, v22 offset:23216
	ds_write_b16_d16_hi v206, v22 offset:23360
	ds_write_b16 v206, v23 offset:25520
	ds_write_b16_d16_hi v206, v23 offset:25664
	ds_bpermute_b32 v20, v208, v101
	ds_bpermute_b32 v21, v97, v101
	ds_bpermute_b32 v22, v209, v101
	v_pk_mul_f32 v[134:135], v[134:135], v[18:19]
	v_mov_b32_e32 v223, v180
	s_waitcnt lgkmcnt(2)
	v_cndmask_b32_e64 v20, v20, 0, s[8:9]
	s_waitcnt lgkmcnt(1)
	v_cndmask_b32_e64 v21, 0, v21, s[12:13]
	v_add_f32_e32 v20, v20, v21
	s_waitcnt lgkmcnt(0)
	v_cndmask_b32_e64 v21, 0, v22, s[14:15]
	v_add_f32_e32 v20, v20, v21
	v_add_f32_e32 v21, v114, v20
	v_add_f32_e32 v22, v115, v20
	v_add_f32_e32 v23, v119, v20
	v_add_f32_e32 v24, v101, v20
	v_mul_f32_e32 v20, 0x3fb8aa3b, v21
	v_mul_f32_e32 v21, 0x3fb8aa3b, v22
	v_mul_f32_e32 v22, 0x3fb8aa3b, v23
	v_mul_f32_e32 v23, 0x3fb8aa3b, v24
	v_exp_f32_e32 v23, v23
	ds_bpermute_b32 v93, v95, v24
	v_exp_f32_e32 v20, v20
	v_exp_f32_e32 v21, v21
	ds_bpermute_b32 v24, v208, v23
	v_exp_f32_e32 v22, v22
	v_rcp_f32_e32 v112, v20
	v_rcp_f32_e32 v113, v21
	v_pk_mul_f32 v[118:119], v[124:125], v[128:129]
	s_waitcnt lgkmcnt(0)
	v_cndmask_b32_e64 v24, v24, 1.0, s[8:9]
	v_mov_b32_e32 v25, v20
	v_pk_mul_f32 v[114:115], v[10:11], v[118:119]
	v_pk_mul_f32 v[10:11], v[24:25], v[118:119] neg_lo:[0,1] neg_hi:[0,1]
	v_rcp_f32_e32 v118, v22
	v_rcp_f32_e32 v119, v23
	v_pk_mul_f32 v[136:137], v[120:121], v[20:21]
	v_pk_mul_f32 v[120:121], v[12:13], v[134:135]
	v_mov_b32_e32 v12, v21
	v_mov_b32_e32 v13, v22
	v_pk_mul_f32 v[24:25], v[114:115], v[112:113]
	v_pk_mul_f32 v[124:125], v[30:31], v[112:113]
	v_pk_mul_f32 v[132:133], v[132:133], v[22:23]
	v_pk_mul_f32 v[12:13], v[12:13], v[134:135] neg_lo:[0,1] neg_hi:[0,1]
	v_cvt_pk_bf16_f32 v10, v10, v11
	v_cvt_pk_bf16_f32 v11, v136, v137
	v_pk_mul_f32 v[20:21], v[120:121], v[118:119]
	v_pk_mul_f32 v[22:23], v[32:33], v[118:119]
	v_cvt_pk_bf16_f32 v24, v24, v25
	v_cvt_pk_bf16_f32 v25, v124, v125
	ds_write_b16 v205, v10 offset:18496
	ds_write_b16_d16_hi v205, v10 offset:18640
	ds_write_b16 v205, v11 offset:20800
	ds_write_b16_d16_hi v205, v11 offset:20944
	ds_write_b16 v205, v24 offset:23104
	ds_write_b16_d16_hi v205, v24 offset:23248
	ds_write_b16 v205, v25 offset:25408
	ds_write_b16_d16_hi v205, v25 offset:25552
	v_cvt_pk_bf16_f32 v10, v12, v13
	v_cvt_pk_bf16_f32 v11, v132, v133
	v_cvt_pk_bf16_f32 v12, v20, v21
	v_cvt_pk_bf16_f32 v13, v22, v23
	ds_write_b16 v206, v10 offset:18640
	ds_write_b16_d16_hi v206, v10 offset:18784
	ds_write_b16 v206, v11 offset:20944
	ds_write_b16_d16_hi v206, v11 offset:21088
	ds_write_b16 v206, v12 offset:23248
	ds_write_b16_d16_hi v206, v12 offset:23392
	ds_write_b16 v206, v13 offset:25552
	ds_write_b16_d16_hi v206, v13 offset:25696
	ds_bpermute_b32 v10, v208, v8
	ds_bpermute_b32 v11, v97, v8
	ds_bpermute_b32 v12, v209, v8
	s_waitcnt lgkmcnt(2)
	v_cndmask_b32_e64 v10, v10, 0, s[8:9]
	s_waitcnt lgkmcnt(1)
	v_cndmask_b32_e64 v11, 0, v11, s[12:13]
	v_add_f32_e32 v10, v10, v11
	s_waitcnt lgkmcnt(0)
	v_cndmask_b32_e64 v11, 0, v12, s[14:15]
	v_add_f32_e32 v10, v10, v11
	v_add_f32_e32 v8, v8, v10
	v_add_f32_e32 v11, v14, v10
	v_add_f32_e32 v12, v15, v10
	v_add_f32_e32 v13, v16, v10
	ds_bpermute_b32 v95, v95, v8
	v_mul_f32_e32 v8, 0x3fb8aa3b, v8
	v_mul_f32_e32 v10, 0x3fb8aa3b, v11
	v_mul_f32_e32 v11, 0x3fb8aa3b, v12
	v_mul_f32_e32 v12, 0x3fb8aa3b, v13
	v_exp_f32_e32 v13, v8
	v_exp_f32_e32 v10, v10
	v_exp_f32_e32 v11, v11
	v_exp_f32_e32 v12, v12
	ds_bpermute_b32 v8, v208, v13
	v_rcp_f32_e32 v124, v10
	v_rcp_f32_e32 v125, v11
	v_rcp_f32_e32 v128, v12
	v_rcp_f32_e32 v129, v13
	v_mov_b32_e32 v16, v9
	s_waitcnt lgkmcnt(0)
; #define LAS __attribute__((address_space(3)))
; #define MFMA16(a, b, c) __builtin_amdgcn_mfma_f32_16x16x32_bf16((a), (b), (c), 0, 0, 0)
; DI void rwkv_r1_item(const Args& A, int l, LAS unsigned char* lds, int item, int& dh_staged, int tid, int wave, int lane) {
;     ...
;         for (int r = 0; r < 4; ++r) { const float ep = epv[r], epm = r ? epv[r - 1] : ep_prev, einv = __builtin_amdgcn_rcpf(ep), eend = eendall * einv;
;             const float bb = kap[nt][r] * alp[nt][r];
;             ia[r] = -kap[nt][r] * epm; ir[r] = er[nt][r] * ep; ib[r] = bb * einv; ik[r] = ek[nt][r] * einv;
;             bt4[r] = bb * eend; kt4[r] = ek[nt][r] * eend; }
; #pragma unroll
;         for (int r = 0; r < 4; r += 2) { const int o = (4 * qd + r) * 72 + 16 * nt + fr;
;             const unsigned pa_ = cvtpk(ia[r], ia[r + 1]), pr_ = cvtpk(ir[r], ir[r + 1]), pb_ = cvtpk(ib[r], ib[r + 1]), pk_ = cvtpk(ik[r], ik[r + 1]);
;             IMG[o] = (bf16)pa_; IMG[o + 72] = (bf16)(pa_ >> 16); IMG[1152 + o] = (bf16)pr_; IMG[1152 + o + 72] = (bf16)(pr_ >> 16);
;             IMG[2304 + o] = (bf16)pb_; IMG[2304 + o + 72] = (bf16)(pb_ >> 16); IMG[3456 + o] = (bf16)pk_; IMG[3456 + o + 72] = (bf16)(pk_ >> 16); }
;         btf[nt].x = cvtpk(bt4[0], bt4[1]); btf[nt].y = cvtpk(bt4[2], bt4[3]); ktf[nt].x = cvtpk(kt4[0], kt4[1]); ktf[nt].y = cvtpk(kt4[2], kt4[3]); }
;     asm volatile("s_waitcnt lgkmcnt(0)" ::: "memory");
;     f32x4 Lab = (f32x4){0.f, 0.f, 0.f, 0.f}, Lak = Lab, Mrb = Lab, Mrk = Lab;
; #pragma unroll
;     for (int ks = 0; ks < 2; ++ks) { const int o = fr * 72 + 32 * ks + 8 * qd;
;         const bf16x8_t aA = *(const LAS bf16x8_t*)(IMG + o), aR = *(const LAS bf16x8_t*)(IMG + 1152 + o), bB = *(const LAS bf16x8_t*)(IMG + 2304 + o), bK = *(const LAS bf16x8_t*)(IMG + 3456 + o);
;         Lab = MFMA16(aA, bB, Lab); Lak = MFMA16(aA, bK, Lak); Mrb = MFMA16(aR, bB, Mrb); Mrk = MFMA16(aR, bK, Mrk); }
; #pragma unroll
;     for (int r = 0; r < 4; ++r) { const int t = 4 * qd + r; if (!(fr < t)) { Lab[r] = 0.f; Lak[r] = 0.f; } if (!(fr <= t)) { Mrb[r] = 0.f; Mrk[r] = 0.f; } Lf[t * 17 + fr] = Lab[r]; }
;     asm volatile("s_waitcnt lgkmcnt(0)" ::: "memory");
;     float Tc[16];
; #pragma unroll
;     for (int t = 0; t < 16; ++t) { float acc = (t == fr) ? 1.f : 0.f;
; #pragma unroll
;         for (int s = 0; s < t; ++s) acc += Lf[t * 17 + s] * Tc[s];
;         Tc[t] = acc; }
	v_cndmask_b32_e64 v14, v8, 1.0, s[8:9]
	v_mov_b32_e32 v15, v10
	v_pk_mul_f32 v[8:9], v[16:17], v[18:19]
	v_pk_mul_f32 v[20:21], v[126:127], v[10:11]
	v_pk_mul_f32 v[126:127], v[2:3], v[6:7]
	v_pk_mul_f32 v[2:3], v[14:15], v[6:7] neg_lo:[0,1] neg_hi:[0,1]
	v_pk_mul_f32 v[22:23], v[130:131], v[12:13]
	v_pk_mul_f32 v[130:131], v[4:5], v[8:9]
	v_mov_b32_e32 v4, v11
	v_mov_b32_e32 v5, v12
	v_pk_mul_f32 v[6:7], v[126:127], v[124:125]
	v_pk_mul_f32 v[14:15], v[34:35], v[124:125]
	v_pk_mul_f32 v[4:5], v[4:5], v[8:9] neg_lo:[0,1] neg_hi:[0,1]
	v_cvt_pk_bf16_f32 v2, v2, v3
	v_pk_mul_f32 v[8:9], v[130:131], v[128:129]
	v_pk_mul_f32 v[10:11], v[38:39], v[128:129]
	v_cvt_pk_bf16_f32 v3, v20, v21
	v_cvt_pk_bf16_f32 v6, v6, v7
	v_cvt_pk_bf16_f32 v7, v14, v15
	ds_write_b16 v205, v2 offset:18528
	ds_write_b16_d16_hi v205, v2 offset:18672
	ds_write_b16 v205, v3 offset:20832
	ds_write_b16_d16_hi v205, v3 offset:20976
	ds_write_b16 v205, v6 offset:23136
	ds_write_b16_d16_hi v205, v6 offset:23280
	ds_write_b16 v205, v7 offset:25440
	ds_write_b16_d16_hi v205, v7 offset:25584
	v_cvt_pk_bf16_f32 v2, v4, v5
	v_cvt_pk_bf16_f32 v3, v22, v23
	v_cvt_pk_bf16_f32 v4, v8, v9
	v_cvt_pk_bf16_f32 v5, v10, v11
	ds_write_b16 v206, v2 offset:18672
	ds_write_b16_d16_hi v206, v2 offset:18816
	ds_write_b16 v206, v3 offset:20976
	ds_write_b16_d16_hi v206, v3 offset:21120
	ds_write_b16 v206, v4 offset:23280
	ds_write_b16_d16_hi v206, v4 offset:23424
	ds_write_b16 v206, v5 offset:25584
	ds_write_b16_d16_hi v206, v5 offset:25728
	s_waitcnt lgkmcnt(0)
	ds_read_b128 v[2:5], v179 offset:18432
	ds_read_b128 v[6:9], v179 offset:20736
	ds_read_b128 v[10:13], v179 offset:23040
	ds_read_b128 v[14:17], v179 offset:25344
	s_waitcnt lgkmcnt(1)
	v_mfma_f32_16x16x32_bf16 v[18:21], v[2:5], v[10:13], 0
	s_waitcnt lgkmcnt(0)
	v_mfma_f32_16x16x32_bf16 v[2:5], v[2:5], v[14:17], 0
	v_mfma_f32_16x16x32_bf16 v[10:13], v[6:9], v[10:13], 0
	v_mfma_f32_16x16x32_bf16 v[6:9], v[6:9], v[14:17], 0
	ds_read_b128 v[14:17], v179 offset:18496
	ds_read_b128 v[22:25], v179 offset:20800
	ds_read_b128 v[132:135], v179 offset:23104
	ds_read_b128 v[136:139], v179 offset:25408
	s_waitcnt lgkmcnt(1)
	v_mfma_f32_16x16x32_bf16 v[18:21], v[14:17], v[132:135], v[18:21]
	s_waitcnt lgkmcnt(0)
	v_mfma_f32_16x16x32_bf16 v[2:5], v[14:17], v[136:139], v[2:5]
	v_mov_b32_e32 v14, s1
	s_nop 4
	v_cndmask_b32_e64 v14, v14, v18, s[16:17]
	ds_write_b32 v210, v14 offset:27648
	v_cndmask_b32_e64 v14, v19, 0, s[18:19]
	v_cndmask_b32_e64 v15, 0, v20, s[22:23]
	v_add_u32_e32 v16, 0x6c00, v211
	ds_write2_b32 v16, v14, v15 offset1:17
	v_cndmask_b32_e64 v14, 0, v21, s[26:27]
	ds_write_b32 v211, v14 offset:27784
	s_waitcnt lgkmcnt(0)
	ds_read_b32 v14, v222 offset:27716
	v_add_u32_e32 v20, 0x6c00, v222
	ds_read2_b32 v[18:19], v20 offset0:53 offset1:89
	v_mfma_f32_16x16x32_bf16 v[10:13], v[22:25], v[132:135], v[10:13]
	ds_read2_b32 v[132:133], v20 offset0:197 offset1:233
	s_waitcnt lgkmcnt(2)
	v_fma_f32 v99, v180, v14, v181
	ds_read_b64 v[14:15], v222 offset:27784
	v_mfma_f32_16x16x32_bf16 v[6:9], v[22:25], v[136:139], v[6:9]
	s_waitcnt lgkmcnt(0)
	v_fma_f32 v101, v180, v14, v182
	v_mov_b32_e32 v14, s0
	v_fmac_f32_e32 v101, v15, v99
	ds_read2_b32 v[14:15], v14 offset1:1
	v_readlane_b32 s0, v234, 7
	s_waitcnt lgkmcnt(0)
	v_fma_f32 v97, v180, v14, v183
	v_fmac_f32_e32 v97, v99, v15
	ds_read_b128 v[14:17], v222 offset:27920
	v_fmac_f32_e32 v97, v101, v18
	s_waitcnt lgkmcnt(0)
	v_fma_f32 v103, v180, v14, v184
	v_mov_b32_e32 v14, s0
	v_fmac_f32_e32 v103, v99, v15
	ds_read2_b32 v[14:15], v14 offset1:1
	v_readlane_b32 s0, v234, 9
	v_fmac_f32_e32 v103, v101, v16
	v_fmac_f32_e32 v103, v97, v17
	s_waitcnt lgkmcnt(0)
	v_fma_f32 v216, v180, v14, v185
	v_mov_b32_e32 v14, s0
	v_fmac_f32_e32 v216, v99, v15
	ds_read2_b32 v[14:15], v14 offset1:1
	v_readlane_b32 s0, v234, 11
	s_waitcnt lgkmcnt(0)
	v_fmac_f32_e32 v216, v101, v14
	v_mov_b32_e32 v14, s0
	v_fmac_f32_e32 v216, v97, v15
	ds_read2_b64 v[14:17], v14 offset1:1
	v_readlane_b32 s0, v234, 13
	v_fmac_f32_e32 v216, v103, v19
	ds_read2_b32 v[18:19], v20 offset0:125 offset1:161
	s_waitcnt lgkmcnt(1)
	v_fma_f32 v217, v180, v14, v186
	v_fmac_f32_e32 v217, v99, v15
	ds_read_b64 v[14:15], v222 offset:28072
	v_fmac_f32_e32 v217, v101, v16
	v_fmac_f32_e32 v217, v97, v17
	s_waitcnt lgkmcnt(0)
	v_fmac_f32_e32 v217, v103, v14
	v_mov_b32_e32 v14, s0
	v_fmac_f32_e32 v217, v216, v15
	ds_read2_b32 v[14:15], v14 offset1:1
	v_readlane_b32 s0, v234, 15
	s_waitcnt lgkmcnt(0)
	v_fma_f32 v215, v180, v14, v187
	v_mov_b32_e32 v14, s0
	v_fmac_f32_e32 v215, v99, v15
	ds_read2_b32 v[14:15], v14 offset1:1
	v_readlane_b32 s0, v234, 16
	s_waitcnt lgkmcnt(0)
	v_fmac_f32_e32 v215, v101, v14
	v_mov_b32_e32 v14, s0
	v_fmac_f32_e32 v215, v97, v15
	ds_read2_b32 v[14:15], v14 offset1:1
	v_readlane_b32 s0, v234, 17
	s_waitcnt lgkmcnt(0)
	v_fmac_f32_e32 v215, v103, v14
	v_fmac_f32_e32 v215, v216, v15
	ds_read_b128 v[14:17], v222 offset:28192
	v_fmac_f32_e32 v215, v217, v18
	s_waitcnt lgkmcnt(0)
; DI void rwkv_r1_item(const Args& A, int l, LAS unsigned char* lds, int item, int& dh_staged, int tid, int wave, int lane) {
;     ...
;     float Tc[16];
; #pragma unroll
;     for (int t = 0; t < 16; ++t) { float acc = (t == fr) ? 1.f : 0.f;
; #pragma unroll
;         for (int s = 0; s < t; ++s) acc += Lf[t * 17 + s] * Tc[s];
;         Tc[t] = acc; }
;     f32x4 Tm;
; #pragma unroll
;     for (int r = 0; r < 4; ++r) Tm[r] = qd == 0 ? Tc[r] : (qd == 1 ? Tc[4 + r] : (qd == 2 ? Tc[8 + r] : Tc[12 + r]));
	v_fma_f32 v218, v180, v14, v188
	v_fmac_f32_e32 v218, v99, v15
	v_fmac_f32_e32 v218, v101, v16
	v_fmac_f32_e32 v218, v97, v17
	ds_read_b128 v[14:17], v222 offset:28208
	s_waitcnt lgkmcnt(0)
	v_fmac_f32_e32 v218, v103, v14
	v_mov_b32_e32 v14, s0
	v_fmac_f32_e32 v218, v216, v15
	ds_read2_b32 v[14:15], v14 offset1:1
	v_readlane_b32 s0, v234, 18
	v_fmac_f32_e32 v218, v217, v16
	v_fmac_f32_e32 v218, v215, v17
	s_waitcnt lgkmcnt(0)
	v_fma_f32 v219, v180, v14, v189
	v_mov_b32_e32 v14, s0
	v_fmac_f32_e32 v219, v99, v15
	ds_read2_b32 v[14:15], v14 offset1:1
	v_readlane_b32 s0, v234, 19
	s_waitcnt lgkmcnt(0)
	v_fmac_f32_e32 v219, v101, v14
	v_mov_b32_e32 v14, s0
	v_fmac_f32_e32 v219, v97, v15
	ds_read2_b32 v[14:15], v14 offset1:1
	v_readlane_b32 s0, v234, 20
	s_waitcnt lgkmcnt(0)
	v_fmac_f32_e32 v219, v103, v14
	v_mov_b32_e32 v14, s0
	v_fmac_f32_e32 v219, v216, v15
	ds_read2_b32 v[14:15], v14 offset1:1
	v_readlane_b32 s0, v234, 21
	s_waitcnt lgkmcnt(0)
	v_fmac_f32_e32 v219, v217, v14
	v_mov_b32_e32 v14, s0
	v_fmac_f32_e32 v219, v215, v15
	ds_read2_b64 v[14:17], v14 offset1:1
	v_readlane_b32 s0, v234, 22
	v_fmac_f32_e32 v219, v218, v19
	s_waitcnt lgkmcnt(0)
	v_fma_f32 v221, v180, v14, v190
	v_fmac_f32_e32 v221, v99, v15
	v_fmac_f32_e32 v221, v101, v16
	v_mov_b32_e32 v14, s0
	v_fmac_f32_e32 v221, v97, v17
	ds_read2_b64 v[14:17], v14 offset1:1
	v_readlane_b32 s0, v234, 23
	s_waitcnt lgkmcnt(0)
	v_fmac_f32_e32 v221, v103, v14
	v_fmac_f32_e32 v221, v216, v15
	ds_read_b64 v[14:15], v222 offset:28360
	v_fmac_f32_e32 v221, v217, v16
	v_fmac_f32_e32 v221, v215, v17
	s_waitcnt lgkmcnt(0)
	v_fmac_f32_e32 v221, v218, v14
	v_mov_b32_e32 v14, s0
	v_fmac_f32_e32 v221, v219, v15
	ds_read2_b32 v[14:15], v14 offset1:1
	v_readlane_b32 s0, v234, 24
	s_waitcnt lgkmcnt(0)
	v_fma_f32 v220, v180, v14, v191
	v_mov_b32_e32 v14, s0
	v_fmac_f32_e32 v220, v99, v15
	ds_read2_b32 v[14:15], v14 offset1:1
	v_readlane_b32 s0, v234, 25
	s_waitcnt lgkmcnt(0)
	v_fmac_f32_e32 v220, v101, v14
	v_mov_b32_e32 v14, s0
	v_fmac_f32_e32 v220, v97, v15
	ds_read2_b32 v[14:15], v14 offset1:1
	v_readlane_b32 s0, v234, 26
	s_waitcnt lgkmcnt(0)
	v_fmac_f32_e32 v220, v103, v14
	v_mov_b32_e32 v14, s0
	v_fmac_f32_e32 v220, v216, v15
	ds_read2_b32 v[14:15], v14 offset1:1
	v_readlane_b32 s0, v234, 27
	s_waitcnt lgkmcnt(0)
	v_fmac_f32_e32 v220, v217, v14
	v_mov_b32_e32 v14, s0
	v_fmac_f32_e32 v220, v215, v15
	ds_read2_b32 v[14:15], v14 offset1:1
	v_readlane_b32 s0, v234, 28
	s_waitcnt lgkmcnt(0)
	v_fmac_f32_e32 v220, v218, v14
	v_fmac_f32_e32 v220, v219, v15
	ds_read_b128 v[14:17], v222 offset:28464
	v_fmac_f32_e32 v220, v221, v132
	s_waitcnt lgkmcnt(0)
	v_fma_f32 v132, v180, v14, v192
	v_fmac_f32_e32 v132, v99, v15
	v_fmac_f32_e32 v132, v101, v16
	v_fmac_f32_e32 v132, v97, v17
	ds_read_b128 v[14:17], v222 offset:28480
	s_waitcnt lgkmcnt(0)
	v_fmac_f32_e32 v132, v103, v14
	v_fmac_f32_e32 v132, v216, v15
	v_fmac_f32_e32 v132, v217, v16
	v_fmac_f32_e32 v132, v215, v17
	ds_read_b128 v[14:17], v222 offset:28496
	s_waitcnt lgkmcnt(0)
	v_fmac_f32_e32 v132, v218, v14
	v_mov_b32_e32 v14, s0
	v_readlane_b32 s0, v234, 29
	ds_read2_b32 v[144:145], v14 offset1:1
	v_fmac_f32_e32 v132, v219, v15
	v_mov_b32_e32 v14, s0
	v_readlane_b32 s0, v234, 30
	ds_read2_b32 v[142:143], v14 offset1:1
	v_fmac_f32_e32 v132, v221, v16
	v_mov_b32_e32 v14, s0
	v_readlane_b32 s0, v234, 31
	ds_read2_b32 v[140:141], v14 offset1:1
	v_fmac_f32_e32 v132, v220, v17
	v_mov_b32_e32 v14, s0
	v_readlane_b32 s0, v234, 32
	ds_read2_b32 v[138:139], v14 offset1:1
	s_nop 0
	v_mov_b32_e32 v14, s0
	v_readlane_b32 s0, v234, 33
	ds_read2_b32 v[136:137], v14 offset1:1
	s_nop 0
	v_mov_b32_e32 v14, s0
	v_readlane_b32 s0, v234, 34
	ds_read2_b32 v[134:135], v14 offset1:1
	s_nop 0
	v_mov_b32_e32 v14, s0
	v_readlane_b32 s0, v234, 35
	ds_read2_b64 v[22:25], v14 offset1:1
	s_nop 0
	v_mov_b32_e32 v14, s0
	v_readlane_b32 s0, v234, 36
	ds_read2_b64 v[18:21], v14 offset1:1
	s_nop 0
	v_mov_b32_e32 v14, s0
	v_readlane_b32 s0, v234, 37
	ds_read2_b64 v[14:17], v14 offset1:1
	ds_read_b64 v[162:163], v222 offset:28648
	v_mov_b32_e32 v148, s0
	v_readlane_b32 s0, v234, 38
	ds_read2_b32 v[160:161], v148 offset1:1
	s_nop 0
	v_mov_b32_e32 v148, s0
	v_readlane_b32 s0, v234, 39
	ds_read2_b32 v[158:159], v148 offset1:1
	s_nop 0
	v_mov_b32_e32 v148, s0
	v_readlane_b32 s0, v234, 40
	ds_read2_b32 v[156:157], v148 offset1:1
	s_nop 0
	v_mov_b32_e32 v148, s0
	v_readlane_b32 s0, v234, 42
	ds_read2_b32 v[154:155], v148 offset1:1
	s_nop 0
	v_mov_b32_e32 v148, s0
	v_readlane_b32 s0, v234, 44
	ds_read2_b32 v[152:153], v148 offset1:1
	s_nop 0
	v_mov_b32_e32 v148, s0
	v_readlane_b32 s0, v234, 46
	ds_read2_b32 v[150:151], v148 offset1:1
	s_nop 0
	v_mov_b32_e32 v148, s0
	ds_read2_b32 v[148:149], v148 offset1:1
	ds_read_b32 v222, v222 offset:28724
	s_and_saveexec_b64 s[40:41], s[10:11]
	s_cbranch_execz .LBB0_366
	v_cmp_lt_i32_e32 vcc, 1, v168
	s_mov_b64 s[42:43], 0
	s_and_saveexec_b64 s[44:45], vcc
	s_xor_b64 s[44:45], exec, s[44:45]
	s_cbranch_execnz .LBB0_401
	s_or_saveexec_b64 s[44:45], s[44:45]
	v_mov_b32_e32 v223, v218
	s_xor_b64 exec, exec, s[44:45]
	s_cbranch_execnz .LBB0_404

; DI unsigned cvtpk(float lo, float hi) { const f2_t v = {lo, hi}; return __builtin_bit_cast(unsigned, __builtin_convertvector(v, bf2_t)); }
; DI void rwkv_r1_item(const Args& A, int l, LAS unsigned char* lds, int item, int& dh_staged, int tid, int wave, int lane) {
;     ...
;     const int sgn = dir ? -1 : 1; const int tok0 = b * SEQ + (dir ? SEQ - 1 - 16 * cc : 16 * cc);
;     const float* mu = A.in[I_MU] + (size_t)(l * 2 + dir) * 1280;
;     float er[4][4], ek[4][4], ev[4][4];
;     u32x4_t ld[7];
; #pragma unroll
;     for (int i = 0; i < 7; ++i) { const int idx = lane + 64 * i; const int ri = idx / 24, pc = idx % 24; const bool ok = (idx < 17 * 24) && (ri > 0 || cc > 0);
;         ld[i] = (u32x4_t){0u, 0u, 0u, 0u};
;         if (ok) ld[i] = *(const u32x4_t*)(Z + (size_t)(tok0 + sgn * (ri - 1)) * ZLD + ZRKV + (pc >> 3) * RW + hh * 64 + (pc & 7) * 8); }
;     uint4 zcw[2], zca[2], zpw[2], zpa[2];
;     { const int zwd = dir ? ZWDB : ZWDF, zad = dir ? ZADB : ZADF; const bool hasp = !(cc == 0 && fr == 0);
;       const bf16* zc = Z + (size_t)(tok0 + sgn * fr) * ZLD; const bf16* zq = Z + (size_t)(tok0 + sgn * (fr - 1)) * ZLD;
; #pragma unroll
;       for (int ks = 0; ks < 2; ++ks) { zcw[ks] = *(const uint4*)(zc + zwd + 32 * ks + 8 * qd); zca[ks] = *(const uint4*)(zc + zad + 32 * ks + 8 * qd);
;           zpw[ks] = make_uint4(0u, 0u, 0u, 0u); zpa[ks] = make_uint4(0u, 0u, 0u, 0u);
;           if (hasp) { zpw[ks] = *(const uint4*)(zq + zwd + 32 * ks + 8 * qd); zpa[ks] = *(const uint4*)(zq + zad + 32 * ks + 8 * qd); } } }
;     if (dh_staged != dir * 6 + hh) { dh_staged = dir * 6 + hh;
;     const int ch = tid & 63, i0 = (tid >> 6) * 8; const float* w2 = A.in[I_W2] + ((size_t)(l * 2 + dir) * 64 + i0) * RW + hh * 64 + ch; const float* a2 = A.in[I_A2] + ((size_t)(l * 2 + dir) * 64 + i0) * RW + hh * 64 + ch;
;     u32x4_t pw, pa; pw.x = cvtpk(w2[0], w2[RW]); pw.y = cvtpk(w2[2 * RW], w2[3 * RW]); pw.z = cvtpk(w2[4 * RW], w2[5 * RW]); pw.w = cvtpk(w2[6 * RW], w2[7 * RW]);
;     pa.x = cvtpk(a2[0], a2[RW]); pa.y = cvtpk(a2[2 * RW], a2[3 * RW]); pa.z = cvtpk(a2[4 * RW], a2[5 * RW]); pa.w = cvtpk(a2[6 * RW], a2[7 * RW]);
;     float prmv; { const int pi = tid >> 6, pc = hh * 64 + (tid & 63); const float* mu_ = A.in[I_MU] + (size_t)(l * 2 + dir) * 1280;
.LBB0_1807:
	s_or_b64 exec, exec, s[42:43]
	s_ashr_i32 s0, s46, 3
	s_add_i32 s42, s0, s47
	s_add_i32 s46, s42, 2
	v_readlane_b32 s12, v235, 17
	s_mul_i32 s43, s46, 0x1400
	v_readlane_b32 s22, v235, 27
	s_mul_hi_i32 s0, s46, 0x1400
	v_readlane_b32 s23, v235, 28
	s_add_u32 s44, s22, s43
	s_addc_u32 s45, s23, s0
	v_lshlrev_b32_e32 v252, 2, v64
	v_mov_b32_e32 v253, v63
	v_add_u32_e32 v254, 0x1200, v252
	v_mov_b32_e32 v255, v63
	v_add_u32_e32 v252, s85, v252
	v_lshl_add_u64 v[252:253], s[44:45], 0, v[252:253]
	v_lshl_add_u64 v[254:255], s[44:45], 0, v[254:255]
	global_load_dwordx4 v[236:239], v[252:253], off offset:512
	global_load_dwordx4 v[240:243], v[254:255], off offset:16
	global_load_dwordx4 v[244:247], v[252:253], off offset:768
	global_load_dwordx4 v[248:251], v[254:255], off offset:272
	s_mul_i32 s0, s42, 6
	s_add_i32 s0, s0, s84
	s_cmp_eq_u32 s64, s0
	v_lshlrev_b32_e32 v102, 2, v146
	v_readlane_b32 s13, v235, 18
	v_readlane_b32 s14, v235, 19
	v_readlane_b32 s15, v235, 20
	v_readlane_b32 s16, v235, 21
	v_readlane_b32 s17, v235, 22
	v_readlane_b32 s18, v235, 23
	v_readlane_b32 s19, v235, 24
	v_readlane_b32 s20, v235, 25
	v_readlane_b32 s21, v235, 26
	v_readlane_b32 s24, v235, 29
	v_readlane_b32 s25, v235, 30
	v_readlane_b32 s26, v235, 31
	v_readlane_b32 s27, v235, 32
	s_cbranch_scc1 .LBB0_1818
	s_ashr_i32 s47, s46, 31
	v_readlane_b32 s12, v235, 17
	s_lshl_b64 s[48:49], s[46:47], 6
	v_readlane_b32 s26, v235, 31
	v_readlane_b32 s27, v235, 32
	v_or_b32_e32 v89, s48, v66
	s_movk_i32 s43, 0x600
	v_mov_b64_e32 v[104:105], s[26:27]
	v_readlane_b32 s13, v235, 18
	v_readlane_b32 s14, v235, 19
	v_readlane_b32 s15, v235, 20
	v_readlane_b32 s16, v235, 21
	v_readlane_b32 s17, v235, 22
	v_readlane_b32 s18, v235, 23
	v_readlane_b32 s19, v235, 24
	v_readlane_b32 s20, v235, 25
	v_readlane_b32 s21, v235, 26
	v_readlane_b32 s22, v235, 27
	v_readlane_b32 s23, v235, 28
	v_readlane_b32 s24, v235, 29
	v_readlane_b32 s25, v235, 30
	v_mad_u64_u32 v[104:105], s[64:65], v89, s43, v[104:105]
	v_mad_i32_i24 v105, s49, v216, v105
	s_lshl_b64 s[64:65], s[2:3], 2
	v_readlane_b32 s12, v235, 36
	v_lshl_add_u64 v[104:105], v[104:105], 0, s[64:65]
	v_mov_b32_e32 v103, v63
	v_readlane_b32 s14, v235, 38
	v_readlane_b32 s15, v235, 39
	v_lshl_add_u64 v[104:105], v[104:105], 0, v[102:103]
	v_add_co_u32_e32 v108, vcc, s85, v104
	v_mov_b64_e32 v[106:107], s[14:15]
	v_mad_u64_u32 v[106:107], s[66:67], v89, s43, v[106:107]
	v_mad_i32_i24 v107, s49, v216, v107
	v_addc_co_u32_e32 v109, vcc, 0, v105, vcc
	v_lshl_add_u64 v[106:107], v[106:107], 0, s[64:65]
	global_load_dword v89, v[104:105], off
	global_load_dword v91, v[104:105], off offset:1536
	global_load_dword v93, v[104:105], off offset:3072
	v_add_co_u32_e32 v104, vcc, 0x2000, v104
	v_lshl_add_u64 v[106:107], v[106:107], 0, v[102:103]
	s_nop 0
	v_addc_co_u32_e32 v105, vcc, 0, v105, vcc
	global_load_dword v95, v[108:109], off offset:512
	global_load_dword v97, v[108:109], off offset:2048
	global_load_dword v99, v[108:109], off offset:3584
	global_load_dword v101, v[104:105], off offset:1024
	global_load_dword v103, v[104:105], off offset:2560
	s_nop 0
	global_load_dword v108, v[106:107], off
	global_load_dword v109, v[106:107], off offset:1536
	global_load_dword v110, v[106:107], off offset:3072
	v_add_co_u32_e32 v104, vcc, 0x1000, v106
	v_readlane_b32 s13, v235, 37
	s_nop 0
	v_addc_co_u32_e32 v105, vcc, 0, v107, vcc
	global_load_dword v111, v[104:105], off offset:512
	global_load_dword v112, v[104:105], off offset:2048
	global_load_dword v113, v[104:105], off offset:3584
	v_add_co_u32_e32 v104, vcc, 0x2000, v106
	v_readlane_b32 s12, v234, 40
	s_nop 0
	v_addc_co_u32_e32 v105, vcc, 0, v107, vcc
	global_load_dword v114, v[104:105], off offset:1024
	global_load_dword v115, v[104:105], off offset:2560
	v_or_b32_e32 v104, s2, v146
	v_readlane_b32 s13, v234, 41
	v_readlane_b32 s16, v235, 40
	v_readlane_b32 s17, v235, 41
	v_readlane_b32 s18, v235, 42
	v_readlane_b32 s19, v235, 43
	v_readlane_b32 s20, v235, 44
	v_readlane_b32 s21, v235, 45
	v_readlane_b32 s22, v235, 46
	v_readlane_b32 s23, v235, 47
	v_readlane_b32 s24, v235, 48
	v_readlane_b32 s25, v235, 49
	v_readlane_b32 s26, v235, 50
	v_readlane_b32 s27, v235, 51
	s_and_saveexec_b64 s[48:49], s[12:13]
	s_xor_b64 s[48:49], exec, s[48:49]
	s_cbranch_execz .LBB0_1815
	v_ashrrev_i32_e32 v105, 31, v104
	v_cmp_lt_i32_e32 vcc, 4, v171
	s_mov_b64 s[64:65], 0
	s_mov_b64 s[66:67], 0
	s_and_saveexec_b64 s[68:69], vcc
	s_xor_b64 s[68:69], exec, s[68:69]
	s_cbranch_execnz .LBB0_1868
	s_andn2_saveexec_b64 s[68:69], s[68:69]
	s_cbranch_execnz .LBB0_1875

; #define LAS __attribute__((address_space(3)))
; DI float bf2f(unsigned v) { return __uint_as_float(v << 16); }
; DI void rwkv_r1_item(const Args& A, int l, LAS unsigned char* lds, int item, int& dh_staged, int tid, int wave, int lane) {
;     ...
;     { LAS bf16* stg = IMG; constexpr int SLD = 200;
; #pragma unroll
;       for (int i = 0; i < 7; ++i) { const int idx = lane + 64 * i; const int ri = idx / 24, pc = idx % 24; if (idx < 17 * 24) *(LAS u32x4_t*)(stg + ri * SLD + pc * 8) = ld[i]; }
;       asm volatile("s_waitcnt lgkmcnt(0)" ::: "memory");
; #pragma unroll
;       for (int nt = 0; nt < 4; ++nt) { const LAS bf16* sp = stg + (4 * qd) * SLD + 16 * nt + fr;
;           float qr = bf2f(sp[0]), qk = bf2f(sp[64]), qv = bf2f(sp[128]);
;           const float mr = prm[16 * nt + fr], mk = prm[64 + 16 * nt + fr], mv = prm[128 + 16 * nt + fr];
; #pragma unroll
;           for (int r = 0; r < 4; ++r) { const float cr = bf2f(sp[(r + 1) * SLD]), ck = bf2f(sp[(r + 1) * SLD + 64]), cv = bf2f(sp[(r + 1) * SLD + 128]);
;               er[nt][r] = cr + mr * (qr - cr); ek[nt][r] = ck + mk * (qk - ck); ev[nt][r] = cv + mv * (qv - cv); qr = cr; qk = ck; qv = cv; } }
.LBB0_1818:
	s_waitcnt vmcnt(9)
	ds_write_b128 v200, v[34:37] offset:18432
	s_waitcnt vmcnt(8)
	ds_write_b128 v201, v[38:41] offset:18432
	s_waitcnt vmcnt(7)
	ds_write_b128 v202, v[42:45] offset:18432
	s_waitcnt vmcnt(6)
	ds_write_b128 v203, v[46:49] offset:18432
	s_waitcnt vmcnt(5)
	ds_write_b128 v204, v[50:53] offset:18432
	s_waitcnt vmcnt(4)
	ds_write_b128 v205, v[54:57] offset:18432
	s_and_saveexec_b64 s[46:47], s[6:7]
	ds_write_b128 v206, v[58:61] offset:24832
	s_or_b64 exec, exec, s[46:47]
	s_waitcnt lgkmcnt(0)
	ds_read2_b32 v[58:59], v176 offset1:16
	ds_read2_b32 v[106:107], v176 offset0:64 offset1:80
	ds_read2_b32 v[34:35], v176 offset0:128 offset1:144
	ds_read_u16 v36, v175 offset:19488
	ds_read_u16 v37, v175 offset:19888
	ds_read_u16 v38, v175 offset:20288
	s_waitcnt vmcnt(3)
	v_lshlrev_b32_e32 v218, 16, v26
	v_and_b32_e32 v219, 0xffff0000, v26
	s_waitcnt lgkmcnt(2)
	v_lshlrev_b32_e32 v36, 16, v36
	s_waitcnt lgkmcnt(1)
	v_lshlrev_b32_e32 v37, 16, v37
	s_waitcnt lgkmcnt(0)
	v_lshlrev_b32_e32 v39, 16, v38
	ds_read_u16 v38, v175 offset:18688
	ds_read_u16 v40, v175 offset:19088
	v_lshlrev_b32_e32 v160, 16, v27
	v_and_b32_e32 v158, 0xffff0000, v27
	v_lshlrev_b32_e32 v217, 16, v30
	v_and_b32_e32 v220, 0xffff0000, v30
	s_waitcnt lgkmcnt(0)
	v_lshlrev_b32_e32 v41, 16, v40
	v_lshlrev_b32_e32 v40, 16, v38
	v_pk_mov_b32 v[42:43], v[40:41], v[36:37] op_sel:[1,0]
	v_mov_b32_e32 v38, v37
	v_pk_add_f32 v[40:41], v[40:41], v[42:43] neg_lo:[0,1] neg_hi:[0,1]
	v_pk_add_f32 v[36:37], v[36:37], v[38:39] neg_lo:[0,1] neg_hi:[0,1]
	v_pk_fma_f32 v[46:47], v[34:35], v[40:41], v[42:43] op_sel_hi:[0,1,1]
	v_pk_fma_f32 v[48:49], v[34:35], v[36:37], v[38:39] op_sel_hi:[0,1,1]
	ds_read_u16 v34, v175 offset:18592
	v_lshlrev_b32_e32 v161, 16, v31
	v_and_b32_e32 v159, 0xffff0000, v31
	v_lshlrev_b32_e32 v157, 16, v32
	v_and_b32_e32 v129, 0xffff0000, v32
	s_waitcnt lgkmcnt(0)
	v_lshlrev_b32_e32 v108, 16, v34
	ds_read_u16 v34, v175 offset:18992
	ds_read_u16 v36, v175 offset:19392
	v_lshlrev_b32_e32 v125, 16, v33
	v_and_b32_e32 v123, 0xffff0000, v33
	s_waitcnt vmcnt(2)
	v_lshlrev_b32_e32 v118, 16, v22
	s_waitcnt lgkmcnt(1)
	v_lshlrev_b32_e32 v60, 16, v34
	s_waitcnt lgkmcnt(0)
	v_lshlrev_b32_e32 v61, 16, v36
	ds_read_u16 v34, v175 offset:20192
	ds_read_u16 v36, v175 offset:19792
	v_and_b32_e32 v119, 0xffff0000, v22
	v_lshlrev_b32_e32 v114, 16, v23
	v_and_b32_e32 v115, 0xffff0000, v23
	s_waitcnt lgkmcnt(1)
	v_lshlrev_b32_e32 v105, 16, v34
	ds_read_u16 v34, v175 offset:19520
	ds_read_u16 v37, v175 offset:19920
	ds_read_u16 v38, v175 offset:20320
	s_waitcnt lgkmcnt(3)
	v_lshlrev_b32_e32 v104, 16, v36
	v_lshlrev_b32_e32 v30, 16, v25
	s_waitcnt lgkmcnt(2)
	v_lshlrev_b32_e32 v36, 16, v34
	s_waitcnt lgkmcnt(1)
	v_lshlrev_b32_e32 v37, 16, v37
	s_waitcnt lgkmcnt(0)
	v_lshlrev_b32_e32 v39, 16, v38
	ds_read_u16 v34, v175 offset:18720
	ds_read_u16 v38, v175 offset:19120
	v_and_b32_e32 v31, 0xffff0000, v25
	v_lshlrev_b32_e32 v120, 16, v18
	v_and_b32_e32 v121, 0xffff0000, v18
	s_waitcnt lgkmcnt(1)
	v_lshlrev_b32_e32 v40, 16, v34
	s_waitcnt lgkmcnt(0)
	v_lshlrev_b32_e32 v41, 16, v38
	v_pk_mov_b32 v[42:43], v[40:41], v[36:37] op_sel:[1,0]
	v_mov_b32_e32 v38, v37
	v_pk_add_f32 v[40:41], v[40:41], v[42:43] neg_lo:[0,1] neg_hi:[0,1]
	v_mov_b32_e32 v34, v35
	v_pk_add_f32 v[36:37], v[36:37], v[38:39] neg_lo:[0,1] neg_hi:[0,1]
	v_pk_fma_f32 v[42:43], v[34:35], v[40:41], v[42:43] op_sel_hi:[0,1,1]
	v_pk_fma_f32 v[44:45], v[34:35], v[36:37], v[38:39] op_sel_hi:[0,1,1]
	ds_read2_b32 v[110:111], v176 offset0:32 offset1:48
	ds_read2_b32 v[112:113], v176 offset0:96 offset1:112
	ds_read2_b32 v[34:35], v176 offset0:160 offset1:176
	ds_read_u16 v36, v175 offset:19552
	ds_read_u16 v37, v175 offset:19952
	ds_read_u16 v38, v175 offset:20352
	v_lshlrev_b32_e32 v116, 16, v19
	v_and_b32_e32 v117, 0xffff0000, v19
	s_waitcnt lgkmcnt(2)
	v_lshlrev_b32_e32 v36, 16, v36
	s_waitcnt lgkmcnt(1)
	v_lshlrev_b32_e32 v37, 16, v37
	s_waitcnt lgkmcnt(0)
	v_lshlrev_b32_e32 v39, 16, v38
	ds_read_u16 v38, v175 offset:18752
	ds_read_u16 v40, v175 offset:19152
	v_lshlrev_b32_e32 v32, 16, v21
	v_and_b32_e32 v33, 0xffff0000, v21
	v_lshlrev_b32_e32 v153, 16, v28
	v_and_b32_e32 v128, 0xffff0000, v28
	s_waitcnt lgkmcnt(0)
	v_lshlrev_b32_e32 v41, 16, v40
	v_lshlrev_b32_e32 v40, 16, v38
	v_pk_mov_b32 v[50:51], v[40:41], v[36:37] op_sel:[1,0]
	v_mov_b32_e32 v38, v37
	v_pk_add_f32 v[40:41], v[40:41], v[50:51] neg_lo:[0,1] neg_hi:[0,1]
	v_pk_add_f32 v[36:37], v[36:37], v[38:39] neg_lo:[0,1] neg_hi:[0,1]
	v_pk_fma_f32 v[50:51], v[34:35], v[40:41], v[50:51] op_sel_hi:[0,1,1]
	v_pk_fma_f32 v[52:53], v[34:35], v[36:37], v[38:39] op_sel_hi:[0,1,1]
	ds_read_u16 v34, v175 offset:19584
	ds_read_u16 v37, v175 offset:19984
	ds_read_u16 v38, v175 offset:20384
	v_sub_f32_e32 v28, v217, v218
	v_lshlrev_b32_e32 v124, 16, v29
	s_waitcnt lgkmcnt(2)
	v_lshlrev_b32_e32 v36, 16, v34
	s_waitcnt lgkmcnt(1)
	v_lshlrev_b32_e32 v37, 16, v37
	s_waitcnt lgkmcnt(0)
; DI float bf2f(unsigned v) { return __uint_as_float(v << 16); }
; DI void rwkv_r1_item(const Args& A, int l, LAS unsigned char* lds, int item, int& dh_staged, int tid, int wave, int lane) {
;     ...
;           float qr = bf2f(sp[0]), qk = bf2f(sp[64]), qv = bf2f(sp[128]);
;           const float mr = prm[16 * nt + fr], mk = prm[64 + 16 * nt + fr], mv = prm[128 + 16 * nt + fr];
; #pragma unroll
;           for (int r = 0; r < 4; ++r) { const float cr = bf2f(sp[(r + 1) * SLD]), ck = bf2f(sp[(r + 1) * SLD + 64]), cv = bf2f(sp[(r + 1) * SLD + 128]);
;               er[nt][r] = cr + mr * (qr - cr); ek[nt][r] = ck + mk * (qk - ck); ev[nt][r] = cv + mv * (qv - cv); qr = cr; qk = ck; qv = cv; } }
;       asm volatile("s_waitcnt lgkmcnt(0)" ::: "memory"); }
;     bf16x8_t thA[2], adA[2];
;     {
; #pragma unroll
;       for (int ks = 0; ks < 2; ++ks) { float cw[8], pw[8], ca[8], pa[8];
;           unpack8(zcw[ks], cw); unpack8(zca[ks], ca); unpack8(zpw[ks], pw); unpack8(zpa[ks], pa);
;           const float* muw = mu + 1152 + 32 * ks + 8 * qd; const float* mua = mu + 1216 + 32 * ks + 8 * qd;
; #pragma unroll
;           for (int e = 0; e < 8; ++e) { const float xw = cw[e] + muw[e] * (pw[e] - cw[e]); cw[e] = 1.f - 2.f * __builtin_amdgcn_rcpf(1.f + __expf(2.f * xw)); ca[e] = ca[e] + mua[e] * (pa[e] - ca[e]); }
	v_lshlrev_b32_e32 v39, 16, v38
	ds_read_u16 v34, v175 offset:18784
	ds_read_u16 v38, v175 offset:19184
	ds_read_u16 v127, v175 offset:19024
	ds_read_u16 v152, v175 offset:19056
	ds_read_u16 v126, v175 offset:19424
	ds_read_u16 v151, v175 offset:19456
	ds_read_u16 v130, v175 offset:18624
	ds_read_u16 v131, v175 offset:18656
	ds_read_u16 v148, v175 offset:19824
	ds_read_u16 v150, v175 offset:19856
	ds_read_u16 v101, v175 offset:20224
	ds_read_u16 v149, v175 offset:20256
	ds_read_u16 v136, v175 offset:18560
	ds_read_u16 v142, v175 offset:18960
	ds_read_u16 v143, v175 offset:19360
	ds_read_u16 v137, v175 offset:18832
	ds_read_u16 v139, v175 offset:19232
	ds_read_u16 v109, v175 offset:20160
	ds_read_u16 v155, v175 offset:19760
	ds_read_u16 v144, v175 offset:20032
	ds_read_u16 v145, v175 offset:19632
	ds_read_u16 v156, v175 offset:18432
	ds_read_u16 v141, v175 offset:18464
	ds_read_u16 v140, v175 offset:18864
	ds_read_u16 v154, v175 offset:19264
	ds_read_u16 v135, v175 offset:20064
	ds_read_u16 v138, v175 offset:19664
	ds_read_u16 v133, v175 offset:18496
	ds_read_u16 v132, v175 offset:18896
	ds_read_u16 v134, v175 offset:19296
	ds_read_u16 v95, v175 offset:20096
	ds_read_u16 v97, v175 offset:19696
	ds_read_u16 v89, v175 offset:18528
	ds_read_u16 v93, v175 offset:18928
	ds_read_u16 v103, v175 offset:19328
	ds_read_u16 v91, v175 offset:20128
	ds_read_u16 v99, v175 offset:19728
	s_waitcnt lgkmcnt(0)
	v_and_b32_e32 v122, 0xffff0000, v29
	s_waitcnt lgkmcnt(14)
	v_lshlrev_b32_e32 v40, 16, v34
	v_lshlrev_b32_e32 v41, 16, v38
	v_pk_mov_b32 v[54:55], v[40:41], v[36:37] op_sel:[1,0]
	v_mov_b32_e32 v38, v37
	v_pk_add_f32 v[40:41], v[40:41], v[54:55] neg_lo:[0,1] neg_hi:[0,1]
	v_mov_b32_e32 v34, v35
	v_pk_add_f32 v[36:37], v[36:37], v[38:39] neg_lo:[0,1] neg_hi:[0,1]
	v_pk_fma_f32 v[54:55], v[34:35], v[40:41], v[54:55] op_sel_hi:[0,1,1]
	v_pk_fma_f32 v[56:57], v[34:35], v[36:37], v[38:39] op_sel_hi:[0,1,1]
	v_lshlrev_b32_e32 v34, 2, v64
	v_mov_b32_e32 v35, v63
	v_lshl_add_u64 v[162:163], s[44:45], 0, v[34:35]
	v_add_co_u32_e32 v26, vcc, s85, v162
	s_mov_b64 s[44:45], 0x1200
	s_nop 0
	v_addc_co_u32_e32 v27, vcc, 0, v163, vcc
	v_lshl_add_u64 v[36:37], v[162:163], 0, s[44:45]
	v_lshlrev_b32_e32 v38, 16, v24
	v_and_b32_e32 v39, 0xffff0000, v24
	v_lshlrev_b32_e32 v40, 16, v20
	v_and_b32_e32 v41, 0xffff0000, v20
	s_waitcnt vmcnt(0)
	v_mov_b32_e32 v22, v236
	v_mov_b32_e32 v23, v237
	v_mov_b32_e32 v24, v238
	v_mov_b32_e32 v25, v239
	v_mov_b32_e32 v18, v240
	v_mov_b32_e32 v19, v241
	v_mov_b32_e32 v20, v242
	v_mov_b32_e32 v21, v243
	s_mov_b64 s[44:45], 0x1300
	v_lshl_add_u64 v[34:35], v[162:163], 0, s[44:45]
	v_pk_add_f32 v[116:117], v[116:117], v[114:115] neg_lo:[0,1] neg_hi:[0,1]
	v_pk_add_f32 v[120:121], v[120:121], v[118:119] neg_lo:[0,1] neg_hi:[0,1]
	s_ashr_i32 s43, s42, 31
	s_lshl_b64 s[44:45], s[42:43], 14
	s_ashr_i32 s0, s70, 31
	s_add_u32 s44, s70, s44
	v_readlane_b32 s12, v235, 63
	s_addc_u32 s45, s0, s45
	v_readlane_b32 s13, v234, 0
	s_movk_i32 s0, 0x300
	s_waitcnt vmcnt(1)
	v_fmac_f32_e32 v218, v28, v22
	v_sub_f32_e32 v28, v220, v219
	v_fmac_f32_e32 v219, v28, v23
	v_add_f32_e32 v22, v218, v218
	v_add_f32_e32 v23, v219, v219
	v_mov_b32_e32 v26, v244
	v_mov_b32_e32 v27, v245
	v_mov_b32_e32 v28, v246
	v_mov_b32_e32 v29, v247
	s_nop 0
	v_mov_b32_e32 v218, v248
	v_mov_b32_e32 v219, v249
	v_mov_b32_e32 v220, v250
	v_mov_b32_e32 v221, v251
	v_mul_f32_e32 v22, 0x3fb8aa3b, v22
	v_mul_f32_e32 v23, 0x3fb8aa3b, v23
	v_exp_f32_e32 v22, v22
	v_exp_f32_e32 v23, v23
	v_add_f32_e32 v22, 1.0, v22
	v_add_f32_e32 v23, 1.0, v23
	v_rcp_f32_e32 v22, v22
	v_rcp_f32_e32 v23, v23
	s_waitcnt vmcnt(1)
	v_pk_fma_f32 v[28:29], v[116:117], v[28:29], v[114:115]
	v_sub_f32_e32 v114, v157, v153
	v_fmac_f32_e32 v153, v114, v18
	v_sub_f32_e32 v114, v129, v128
	v_fmac_f32_e32 v128, v114, v19
	v_add_f32_e32 v18, v153, v153
	v_add_f32_e32 v19, v128, v128
	v_mul_f32_e32 v18, 0x3fb8aa3b, v18
	v_mul_f32_e32 v19, 0x3fb8aa3b, v19
	v_exp_f32_e32 v18, v18
	v_exp_f32_e32 v19, v19
	v_pk_fma_f32 v[26:27], v[120:121], v[26:27], v[118:119]
	v_sub_f32_e32 v118, v161, v160
	v_add_f32_e32 v18, 1.0, v18
	v_add_f32_e32 v19, 1.0, v19
	v_rcp_f32_e32 v18, v18
	v_rcp_f32_e32 v19, v19
	v_fmac_f32_e32 v160, v118, v24
	v_sub_f32_e32 v118, v159, v158
	v_fmac_f32_e32 v158, v118, v25
	v_pk_fma_f32 v[114:115], v[18:19], 2.0, 1.0 op_sel_hi:[1,0,0] neg_lo:[1,0,0] neg_hi:[1,0,0]
	v_pk_add_f32 v[18:19], v[40:41], v[38:39] neg_lo:[0,1] neg_hi:[0,1]
	v_add_f32_e32 v24, v160, v160
	s_waitcnt vmcnt(0)
; #define LAS __attribute__((address_space(3)))
; DI unsigned cvtpk(float lo, float hi) { const f2_t v = {lo, hi}; return __builtin_bit_cast(unsigned, __builtin_convertvector(v, bf2_t)); }
; DI void rwkv_r1_item(const Args& A, int l, LAS unsigned char* lds, int item, int& dh_staged, int tid, int wave, int lane) {
;     ...
;       for (int ks = 0; ks < 2; ++ks) { float cw[8], pw[8], ca[8], pa[8];
;           unpack8(zcw[ks], cw); unpack8(zca[ks], ca); unpack8(zpw[ks], pw); unpack8(zpa[ks], pa);
;           const float* muw = mu + 1152 + 32 * ks + 8 * qd; const float* mua = mu + 1216 + 32 * ks + 8 * qd;
; #pragma unroll
;           for (int e = 0; e < 8; ++e) { const float xw = cw[e] + muw[e] * (pw[e] - cw[e]); cw[e] = 1.f - 2.f * __builtin_amdgcn_rcpf(1.f + __expf(2.f * xw)); ca[e] = ca[e] + mua[e] * (pa[e] - ca[e]); }
;           union { unsigned u[4]; bf16x8_t v; } x, y;
; #pragma unroll
;           for (int e = 0; e < 4; ++e) { x.u[e] = cvtpk(cw[2 * e], cw[2 * e + 1]); y.u[e] = cvtpk(ca[2 * e], ca[2 * e + 1]); }
;           thA[ks] = x.v; adA[ks] = y.v; } }
;     f32x4 wl[4], al[4];
; #pragma unroll
;     for (int nt = 0; nt < 4; ++nt) { wl[nt] = (f32x4){0.f, 0.f, 0.f, 0.f}; al[nt] = (f32x4){0.f, 0.f, 0.f, 0.f};
; #pragma unroll
;         for (int ks = 0; ks < 2; ++ks) { const bf16x8_t bw = *(const LAS bf16x8_t*)(W2T + (16 * nt + fr) * 72 + 32 * ks + 8 * qd); const bf16x8_t ba = *(const LAS bf16x8_t*)(A2T + (16 * nt + fr) * 72 + 32 * ks + 8 * qd);
	v_pk_fma_f32 v[38:39], v[18:19], v[218:219], v[38:39]
	v_sub_f32_e32 v18, v125, v124
	v_sub_f32_e32 v19, v123, v122
	v_fmac_f32_e32 v124, v18, v20
	v_fmac_f32_e32 v122, v19, v21
	v_add_f32_e32 v18, v124, v124
	v_add_f32_e32 v19, v122, v122
	v_add_f32_e32 v25, v158, v158
	v_mul_f32_e32 v18, 0x3fb8aa3b, v18
	v_mul_f32_e32 v19, 0x3fb8aa3b, v19
	v_mul_f32_e32 v24, 0x3fb8aa3b, v24
	v_mul_f32_e32 v25, 0x3fb8aa3b, v25
	v_exp_f32_e32 v18, v18
	v_exp_f32_e32 v19, v19
	v_exp_f32_e32 v24, v24
	v_exp_f32_e32 v25, v25
	v_add_f32_e32 v18, 1.0, v18
	v_add_f32_e32 v19, 1.0, v19
	v_add_f32_e32 v24, 1.0, v24
	v_add_f32_e32 v25, 1.0, v25
	v_rcp_f32_e32 v18, v18
	v_rcp_f32_e32 v19, v19
	v_rcp_f32_e32 v24, v24
	v_rcp_f32_e32 v25, v25
	v_pk_fma_f32 v[22:23], v[22:23], 2.0, 1.0 op_sel_hi:[1,0,0] neg_lo:[1,0,0] neg_hi:[1,0,0]
	v_pk_fma_f32 v[40:41], v[18:19], 2.0, 1.0 op_sel_hi:[1,0,0] neg_lo:[1,0,0] neg_hi:[1,0,0]
	v_pk_add_f32 v[18:19], v[32:33], v[30:31] neg_lo:[0,1] neg_hi:[0,1]
	v_pk_fma_f32 v[24:25], v[24:25], 2.0, 1.0 op_sel_hi:[1,0,0] neg_lo:[1,0,0] neg_hi:[1,0,0]
	v_pk_fma_f32 v[30:31], v[18:19], v[220:221], v[30:31]
	v_cvt_pk_bf16_f32 v22, v22, v23
	v_cvt_pk_bf16_f32 v18, v26, v27
	v_cvt_pk_bf16_f32 v23, v24, v25
	v_cvt_pk_bf16_f32 v19, v28, v29
	v_cvt_pk_bf16_f32 v24, v114, v115
	v_cvt_pk_bf16_f32 v20, v38, v39
	v_cvt_pk_bf16_f32 v21, v30, v31
	v_lshlrev_b32_e32 v157, 16, v10
	v_and_b32_e32 v158, 0xffff0000, v10
	v_lshlrev_b32_e32 v128, 16, v11
	v_and_b32_e32 v124, 0xffff0000, v11
	v_lshlrev_b32_e32 v123, 16, v16
	v_and_b32_e32 v121, 0xffff0000, v16
	v_lshlrev_b32_e32 v119, 16, v17
	v_and_b32_e32 v117, 0xffff0000, v17
	v_lshlrev_b32_e32 v28, 16, v8
	v_and_b32_e32 v29, 0xffff0000, v8
	v_lshlrev_b32_e32 v16, 16, v9
	v_and_b32_e32 v17, 0xffff0000, v9
	v_lshlrev_b32_e32 v114, 16, v2
	v_and_b32_e32 v115, 0xffff0000, v2
	v_lshlrev_b32_e32 v38, 16, v3
	v_and_b32_e32 v39, 0xffff0000, v3
	v_lshlrev_b32_e32 v30, 16, v4
	v_and_b32_e32 v31, 0xffff0000, v4
	v_lshlrev_b32_e32 v26, 16, v5
	v_and_b32_e32 v27, 0xffff0000, v5
	global_load_dwordx4 v[2:5], v[36:37], off offset:144
	global_load_dwordx4 v[8:11], v[36:37], off offset:128
	v_lshlrev_b32_e32 v153, 16, v14
	v_and_b32_e32 v14, 0xffff0000, v14
	v_cvt_pk_bf16_f32 v25, v40, v41
	v_lshlrev_b32_e32 v40, 16, v6
	v_and_b32_e32 v41, 0xffff0000, v6
	v_lshlrev_b32_e32 v32, 16, v7
	v_and_b32_e32 v33, 0xffff0000, v7
	v_sub_f32_e32 v6, v153, v157
	v_sub_f32_e32 v7, v14, v158
	v_lshlrev_b32_e32 v129, 16, v15
	v_and_b32_e32 v125, 0xffff0000, v15
	v_lshlrev_b32_e32 v122, 16, v12
	v_and_b32_e32 v120, 0xffff0000, v12
	v_lshlrev_b32_e32 v118, 16, v13
	v_and_b32_e32 v116, 0xffff0000, v13
	s_waitcnt vmcnt(0)
	v_fmac_f32_e32 v157, v6, v8
	v_fmac_f32_e32 v158, v7, v9
	v_add_f32_e32 v6, v157, v157
	v_add_f32_e32 v7, v158, v158
	v_mul_f32_e32 v6, 0x3fb8aa3b, v6
	v_mul_f32_e32 v7, 0x3fb8aa3b, v7
	v_exp_f32_e32 v6, v6
	v_exp_f32_e32 v7, v7
	v_add_f32_e32 v6, 1.0, v6
	v_add_f32_e32 v7, 1.0, v7
	v_rcp_f32_e32 v6, v6
	v_rcp_f32_e32 v7, v7
	s_nop 0
	v_pk_fma_f32 v[36:37], v[6:7], 2.0, 1.0 op_sel_hi:[1,0,0] neg_lo:[1,0,0] neg_hi:[1,0,0]
	global_load_dwordx4 v[6:9], v[34:35], off offset:144
	global_load_dwordx4 v[12:15], v[34:35], off offset:128
	v_pk_add_f32 v[34:35], v[114:115], v[40:41] neg_lo:[0,1] neg_hi:[0,1]
	s_waitcnt vmcnt(0)
	v_pk_fma_f32 v[12:13], v[34:35], v[12:13], v[40:41]
	v_sub_f32_e32 v34, v129, v128
	v_fmac_f32_e32 v128, v34, v10
	v_sub_f32_e32 v34, v125, v124
	v_fmac_f32_e32 v124, v34, v11
	v_pk_add_f32 v[34:35], v[38:39], v[32:33] neg_lo:[0,1] neg_hi:[0,1]
	v_add_f32_e32 v10, v128, v128
	v_pk_fma_f32 v[14:15], v[34:35], v[14:15], v[32:33]
	v_sub_f32_e32 v32, v123, v122
	v_fmac_f32_e32 v122, v32, v2
	v_sub_f32_e32 v32, v121, v120
	v_fmac_f32_e32 v120, v32, v3
	v_add_f32_e32 v2, v122, v122
	v_add_f32_e32 v3, v120, v120
	v_mul_f32_e32 v2, 0x3fb8aa3b, v2
	v_mul_f32_e32 v3, 0x3fb8aa3b, v3
	v_exp_f32_e32 v2, v2
	v_exp_f32_e32 v3, v3
	v_add_f32_e32 v11, v124, v124
	v_mul_f32_e32 v10, 0x3fb8aa3b, v10
	v_add_f32_e32 v2, 1.0, v2
	v_add_f32_e32 v3, 1.0, v3
	v_rcp_f32_e32 v2, v2
	v_rcp_f32_e32 v3, v3
	v_mul_f32_e32 v11, 0x3fb8aa3b, v11
	v_exp_f32_e32 v10, v10
	v_exp_f32_e32 v11, v11
	v_pk_fma_f32 v[32:33], v[2:3], 2.0, 1.0 op_sel_hi:[1,0,0] neg_lo:[1,0,0] neg_hi:[1,0,0]
	v_pk_add_f32 v[2:3], v[30:31], v[28:29] neg_lo:[0,1] neg_hi:[0,1]
	v_add_f32_e32 v10, 1.0, v10
	v_pk_fma_f32 v[28:29], v[2:3], v[6:7], v[28:29]
	v_sub_f32_e32 v2, v119, v118
	v_sub_f32_e32 v3, v117, v116
	v_fmac_f32_e32 v118, v2, v4
	v_fmac_f32_e32 v116, v3, v5
	v_add_f32_e32 v2, v118, v118
	v_add_f32_e32 v3, v116, v116
	v_mul_f32_e32 v2, 0x3fb8aa3b, v2
	v_mul_f32_e32 v3, 0x3fb8aa3b, v3
	v_exp_f32_e32 v2, v2
	v_exp_f32_e32 v3, v3
	v_add_f32_e32 v11, 1.0, v11
	v_rcp_f32_e32 v10, v10
	v_add_f32_e32 v2, 1.0, v2
	v_add_f32_e32 v3, 1.0, v3
	v_rcp_f32_e32 v2, v2
	v_rcp_f32_e32 v3, v3
	v_rcp_f32_e32 v11, v11
	v_cvt_pk_bf16_f32 v6, v36, v37
	v_cvt_pk_bf16_f32 v4, v28, v29
	v_pk_fma_f32 v[30:31], v[2:3], 2.0, 1.0 op_sel_hi:[1,0,0] neg_lo:[1,0,0] neg_hi:[1,0,0]
	v_pk_add_f32 v[2:3], v[26:27], v[16:17] neg_lo:[0,1] neg_hi:[0,1]
	v_pk_fma_f32 v[10:11], v[10:11], 2.0, 1.0 op_sel_hi:[1,0,0] neg_lo:[1,0,0] neg_hi:[1,0,0]
	v_pk_fma_f32 v[16:17], v[2:3], v[8:9], v[16:17]
	v_cvt_pk_bf16_f32 v2, v12, v13
	v_cvt_pk_bf16_f32 v7, v10, v11
	v_cvt_pk_bf16_f32 v3, v14, v15
	v_cvt_pk_bf16_f32 v5, v16, v17
	ds_read_b128 v[10:13], v177
	ds_read_b128 v[14:17], v177 offset:9216
	v_cvt_pk_bf16_f32 v8, v32, v33
	v_cvt_pk_bf16_f32 v9, v30, v31
	ds_read_b128 v[26:29], v177 offset:64
	ds_read_b128 v[30:33], v177 offset:9280
	s_waitcnt lgkmcnt(3)
; #define LAS __attribute__((address_space(3)))
; #define MFMA16(a, b, c) __builtin_amdgcn_mfma_f32_16x16x32_bf16((a), (b), (c), 0, 0, 0)
; DI void rwkv_r1_item(const Args& A, int l, LAS unsigned char* lds, int item, int& dh_staged, int tid, int wave, int lane) {
;     ...
;     f32x4 wl[4], al[4];
; #pragma unroll
;     for (int nt = 0; nt < 4; ++nt) { wl[nt] = (f32x4){0.f, 0.f, 0.f, 0.f}; al[nt] = (f32x4){0.f, 0.f, 0.f, 0.f};
; #pragma unroll
;         for (int ks = 0; ks < 2; ++ks) { const bf16x8_t bw = *(const LAS bf16x8_t*)(W2T + (16 * nt + fr) * 72 + 32 * ks + 8 * qd); const bf16x8_t ba = *(const LAS bf16x8_t*)(A2T + (16 * nt + fr) * 72 + 32 * ks + 8 * qd);
;             wl[nt] = MFMA16(thA[ks], bw, wl[nt]); al[nt] = MFMA16(adA[ks], ba, al[nt]); } }
;     float lw[4][4], alp[4][4], kap[4][4]; float ssq[4] = {0.f, 0.f, 0.f, 0.f}, bsm[4] = {0.f, 0.f, 0.f, 0.f};
; #pragma unroll
;     for (int nt = 0; nt < 4; ++nt) { const int ch = hh * 64 + 16 * nt + fr;
;         const float w0v = prm[192 + 16 * nt + fr], a0v = prm[256 + 16 * nt + fr], kkw = prm[320 + 16 * nt + fr], kaw = prm[384 + 16 * nt + fr], rkw = prm[448 + 16 * nt + fr];
; #pragma unroll
;         for (int r = 0; r < 4; ++r) { const float x = w0v + wl[nt][r];
;             lw[nt][r] = -0.6065306597126334f * __builtin_amdgcn_rcpf(1.f + __expf(-x));
;             const float a = __builtin_amdgcn_rcpf(1.f + __expf(-(a0v + al[nt][r]))); alp[nt][r] = a;
	v_mfma_f32_16x16x32_bf16 v[10:13], v[22:25], v[10:13], 0
	v_add_u32_e32 v128, 0x400, v176
	s_waitcnt lgkmcnt(2)
	v_mfma_f32_16x16x32_bf16 v[14:17], v[18:21], v[14:17], 0
	s_waitcnt lgkmcnt(1)
	v_mfma_f32_16x16x32_bf16 v[38:41], v[6:9], v[26:29], v[10:13]
	s_waitcnt lgkmcnt(0)
	v_mfma_f32_16x16x32_bf16 v[34:37], v[2:5], v[30:33], v[14:17]
	s_nop 0
	ds_read_b128 v[10:13], v177 offset:2304
	s_nop 1
	ds_read_b128 v[14:17], v177 offset:11520
	ds_read_b128 v[26:29], v177 offset:2368
	ds_read_b128 v[114:117], v177 offset:11584
	s_waitcnt lgkmcnt(3)
	v_mfma_f32_16x16x32_bf16 v[10:13], v[22:25], v[10:13], 0
	s_waitcnt lgkmcnt(2)
	v_mfma_f32_16x16x32_bf16 v[14:17], v[18:21], v[14:17], 0
	s_waitcnt lgkmcnt(1)
	v_mfma_f32_16x16x32_bf16 v[30:33], v[6:9], v[26:29], v[10:13]
	s_waitcnt lgkmcnt(0)
	v_mfma_f32_16x16x32_bf16 v[26:29], v[2:5], v[114:117], v[14:17]
	s_nop 1
	ds_read_b128 v[10:13], v177 offset:4608
	s_nop 0
	ds_read_b128 v[14:17], v177 offset:13824
	s_waitcnt lgkmcnt(0)
	v_mfma_f32_16x16x32_bf16 v[114:117], v[18:21], v[14:17], 0
	ds_read_b128 v[14:17], v177 offset:4672
	ds_read_b128 v[118:121], v177 offset:13888
	v_mfma_f32_16x16x32_bf16 v[10:13], v[22:25], v[10:13], 0
	s_waitcnt lgkmcnt(1)
	v_mfma_f32_16x16x32_bf16 v[14:17], v[6:9], v[14:17], v[10:13]
	s_waitcnt lgkmcnt(0)
	v_mfma_f32_16x16x32_bf16 v[10:13], v[2:5], v[118:121], v[114:117]
	s_nop 2
	ds_read_b128 v[114:117], v178
	ds_read_b128 v[118:121], v178 offset:9216
	s_waitcnt lgkmcnt(1)
	v_mfma_f32_16x16x32_bf16 v[22:25], v[22:25], v[114:117], 0
	s_waitcnt lgkmcnt(0)
	v_mfma_f32_16x16x32_bf16 v[18:21], v[18:21], v[118:121], 0
	ds_read_b128 v[114:117], v178 offset:64
	ds_read_b128 v[118:121], v178 offset:9280
	s_waitcnt lgkmcnt(1)
	v_mfma_f32_16x16x32_bf16 v[6:9], v[6:9], v[114:117], v[22:25]
	ds_read2_b32 v[114:115], v176 offset0:192 offset1:208
	s_waitcnt lgkmcnt(0)
	s_nop 0
	v_add_f32_e32 v22, v30, v115
	v_mfma_f32_16x16x32_bf16 v[2:5], v[2:5], v[118:121], v[18:21]
	v_mul_f32_e32 v22, 0xbfb8aa3b, v22
	v_exp_f32_e32 v22, v22
	v_add_f32_e32 v23, v31, v115
	v_add_f32_e32 v18, v38, v114
	v_add_f32_e32 v19, v39, v114
	v_mul_f32_e32 v18, 0xbfb8aa3b, v18
	v_mul_f32_e32 v19, 0xbfb8aa3b, v19
	v_exp_f32_e32 v18, v18
	v_exp_f32_e32 v19, v19
	v_mul_f32_e32 v23, 0xbfb8aa3b, v23
	ds_read2_b32 v[24:25], v128 offset1:16
	ds_read2_b32 v[122:123], v128 offset0:64 offset1:80
	ds_read2_b32 v[124:125], v128 offset0:128 offset1:144
	ds_read2_b32 v[120:121], v128 offset0:192 offset1:208
	v_add_f32_e32 v18, 1.0, v18
	v_add_f32_e32 v19, 1.0, v19
	v_rcp_f32_e32 v20, v18
	v_rcp_f32_e32 v21, v19
	v_exp_f32_e32 v23, v23
	v_add_f32_e32 v22, 1.0, v22
	s_waitcnt lgkmcnt(3)
	v_add_f32_e32 v18, v34, v24
	v_pk_mul_f32 v[116:117], v[20:21], s[40:41]
	v_add_f32_e32 v20, v40, v114
	v_add_f32_e32 v21, v41, v114
	v_mul_f32_e32 v20, 0xbfb8aa3b, v20
	v_mul_f32_e32 v21, 0xbfb8aa3b, v21
	v_exp_f32_e32 v20, v20
	v_exp_f32_e32 v21, v21
	v_add_f32_e32 v19, v35, v24
	v_rcp_f32_e32 v30, v22
	v_add_f32_e32 v20, 1.0, v20
	v_add_f32_e32 v21, 1.0, v21
	v_rcp_f32_e32 v40, v20
	v_add_f32_e32 v20, v36, v24
	v_rcp_f32_e32 v36, v21
	v_add_f32_e32 v21, v37, v24
	v_add_f32_e32 v22, v26, v25
	v_add_f32_e32 v24, v32, v115
	v_add_f32_e32 v26, v33, v115
	v_mul_f32_e32 v24, 0xbfb8aa3b, v24
	v_mul_f32_e32 v26, 0xbfb8aa3b, v26
	v_add_f32_e32 v23, 1.0, v23
	v_exp_f32_e32 v24, v24
	v_exp_f32_e32 v26, v26
	v_rcp_f32_e32 v31, v23
	v_add_f32_e32 v23, v27, v25
	v_add_f32_e32 v24, 1.0, v24
	v_add_f32_e32 v26, 1.0, v26
	v_pk_mul_f32 v[118:119], v[30:31], s[40:41]
	v_rcp_f32_e32 v157, v24
	v_add_f32_e32 v24, v28, v25
	v_rcp_f32_e32 v162, v26
	v_add_f32_e32 v25, v29, v25
	ds_read2_b32 v[28:29], v176 offset0:224 offset1:240
	ds_read2_b32 v[30:31], v128 offset0:32 offset1:48
	ds_read2_b32 v[26:27], v128 offset0:96 offset1:112
	ds_read2_b32 v[34:35], v128 offset0:160 offset1:176
	ds_read2_b32 v[128:129], v128 offset0:224 offset1:240
	s_waitcnt lgkmcnt(4)
	v_add_f32_e32 v14, v14, v28
	v_add_f32_e32 v15, v15, v28
	v_mul_f32_e32 v14, 0xbfb8aa3b, v14
	v_mul_f32_e32 v15, 0xbfb8aa3b, v15
	v_exp_f32_e32 v14, v14
	v_exp_f32_e32 v15, v15
	v_add_f32_e32 v8, v8, v29
	v_add_f32_e32 v6, v6, v29
	v_add_f32_e32 v14, 1.0, v14
	v_add_f32_e32 v15, 1.0, v15
	v_rcp_f32_e32 v14, v14
	v_rcp_f32_e32 v15, v15
	v_add_f32_e32 v7, v7, v29
	v_mul_f32_e32 v8, 0xbfb8aa3b, v8
	v_mul_f32_e32 v6, 0xbfb8aa3b, v6
	v_pk_mul_f32 v[114:115], v[14:15], s[40:41]
	v_add_f32_e32 v14, v16, v28
	v_mul_f32_e32 v14, 0xbfb8aa3b, v14
	v_exp_f32_e32 v14, v14
	v_mul_f32_e32 v7, 0xbfb8aa3b, v7
	v_exp_f32_e32 v8, v8
	v_exp_f32_e32 v6, v6
	v_exp_f32_e32 v7, v7
	v_add_f32_e32 v14, 1.0, v14
	v_rcp_f32_e32 v163, v14
	v_add_f32_e32 v14, v17, v28
	v_mul_f32_e32 v14, 0xbfb8aa3b, v14
	v_add_f32_e32 v8, 1.0, v8
	v_exp_f32_e32 v14, v14
	v_add_f32_e32 v6, 1.0, v6
	v_add_f32_e32 v7, 1.0, v7
	v_rcp_f32_e32 v218, v8
	v_add_f32_e32 v8, v9, v29
	v_rcp_f32_e32 v6, v6
	v_rcp_f32_e32 v7, v7
	v_mul_f32_e32 v8, 0xbfb8aa3b, v8
	v_exp_f32_e32 v8, v8
	v_add_f32_e32 v14, 1.0, v14
	v_rcp_f32_e32 v217, v14
	v_pk_mul_f32 v[14:15], v[6:7], s[40:41]
	v_lshlrev_b32_e32 v7, 16, v152
	v_lshlrev_b32_e32 v6, 16, v127
	v_lshlrev_b32_e32 v17, 16, v151
	v_lshlrev_b32_e32 v16, 16, v126
	v_pk_add_f32 v[32:33], v[6:7], v[16:17] neg_lo:[0,1] neg_hi:[0,1]
	v_add_f32_e32 v8, 1.0, v8
	v_pk_fma_f32 v[126:127], v[112:113], v[32:33], v[16:17]
	v_lshlrev_b32_e32 v33, 16, v131
	v_lshlrev_b32_e32 v32, 16, v130
	v_rcp_f32_e32 v219, v8
	v_lshlrev_b32_e32 v9, 16, v150
	v_lshlrev_b32_e32 v8, 16, v148
	v_lshlrev_b32_e32 v29, 16, v149
	v_lshlrev_b32_e32 v28, 16, v101
	v_mul_f32_e32 v18, 0xbfb8aa3b, v18
	v_mul_f32_e32 v19, 0xbfb8aa3b, v19
	s_waitcnt lgkmcnt(3)
; #define LAS __attribute__((address_space(3)))
; DI float row16_sum(float v) { v += DPPF(v, 0xB1); v += DPPF(v, 0x4E); v += DPPF(v, 0x141); v += DPPF(v, 0x140); return v; }
; DI unsigned cvtpk(float lo, float hi) { const f2_t v = {lo, hi}; return __builtin_bit_cast(unsigned, __builtin_convertvector(v, bf2_t)); }
; DI void rwkv_r1_item(const Args& A, int l, LAS unsigned char* lds, int item, int& dh_staged, int tid, int wave, int lane) {
;     ...
;     for (int nt = 0; nt < 4; ++nt) { const int ch = hh * 64 + 16 * nt + fr;
;         const float w0v = prm[192 + 16 * nt + fr], a0v = prm[256 + 16 * nt + fr], kkw = prm[320 + 16 * nt + fr], kaw = prm[384 + 16 * nt + fr], rkw = prm[448 + 16 * nt + fr];
; #pragma unroll
;         for (int r = 0; r < 4; ++r) { const float x = w0v + wl[nt][r];
;             lw[nt][r] = -0.6065306597126334f * __builtin_amdgcn_rcpf(1.f + __expf(-x));
;             const float a = __builtin_amdgcn_rcpf(1.f + __expf(-(a0v + al[nt][r]))); alp[nt][r] = a;
;             const float k0 = ek[nt][r]; kap[nt][r] = k0 * kkw; ek[nt][r] = k0 * (1.f + (a - 1.f) * kaw);
;             ssq[r] += kap[nt][r] * kap[nt][r]; bsm[r] += er[nt][r] * ek[nt][r] * rkw; } }
; #pragma unroll
;     for (int r = 0; r < 4; ++r) {
;         ssq[r] = row16_sum(ssq[r]); bsm[r] = row16_sum(bsm[r]);
;         ssq[r] = __builtin_amdgcn_rsqf(fmaxf(ssq[r], 1e-24f)); }
;     { bf16* bon = (bf16*)(A.ws + WS_RKB);
; #pragma unroll
;       for (int nt = 0; nt < 4; ++nt)
; #pragma unroll
;           for (int r = 0; r < 4; ++r) { kap[nt][r] *= ssq[r]; MT[(4 * qd + r) * 72 + 16 * nt + fr] = (bf16)cvtpk(bsm[r] * ev[nt][r], 0.f); }
;       asm volatile("s_waitcnt lgkmcnt(0)" ::: "memory");
;       const int p = lane >> 2, c16 = (lane & 3) * 16; const LAS u32x4_t* sp = (const LAS u32x4_t*)(MT + p * 72 + c16); const u32x4_t w0 = sp[0], w1 = sp[1];
;       bf16* dst = bon + ((size_t)dir * NT + tok0 + sgn * p) * RW + hh * 64 + c16;
	v_add_f32_e32 v10, v10, v30
	v_add_f32_e32 v11, v11, v30
	v_add_f32_e32 v12, v12, v30
	v_add_f32_e32 v13, v13, v30
	v_add_f32_e32 v2, v2, v31
	v_add_f32_e32 v3, v3, v31
	v_pk_add_f32 v[32:33], v[32:33], v[6:7] neg_lo:[0,1] neg_hi:[0,1]
	v_add_f32_e32 v4, v4, v31
	v_add_f32_e32 v5, v5, v31
	v_pk_add_f32 v[30:31], v[8:9], v[28:29] neg_lo:[0,1] neg_hi:[0,1]
	v_pk_add_f32 v[16:17], v[16:17], v[8:9] neg_lo:[0,1] neg_hi:[0,1]
	v_exp_f32_e32 v18, v18
	v_exp_f32_e32 v19, v19
	v_pk_fma_f32 v[130:131], v[112:113], v[32:33], v[6:7]
	v_pk_fma_f32 v[150:151], v[112:113], v[30:31], v[28:29]
	v_pk_fma_f32 v[152:153], v[112:113], v[16:17], v[8:9]
	s_waitcnt lgkmcnt(2)
	v_pk_mul_f32 v[38:39], v[130:131], v[26:27]
	v_pk_mul_f32 v[6:7], v[126:127], v[26:27]
	v_pk_mul_f32 v[8:9], v[152:153], v[26:27]
	v_pk_mul_f32 v[16:17], v[150:151], v[26:27]
	v_mul_i32_i24_e32 v26, s71, v179
	v_ashrrev_i32_e32 v27, 31, v26
	v_lshl_add_u64 v[26:27], s[44:45], 0, v[26:27]
	v_mov_b64_e32 v[28:29], s[12:13]
	v_add_f32_e32 v18, 1.0, v18
	v_add_f32_e32 v19, 1.0, v19
	v_mul_f32_e32 v20, 0xbfb8aa3b, v20
	v_mul_f32_e32 v21, 0xbfb8aa3b, v21
	v_mad_u64_u32 v[28:29], s[44:45], v26, s0, v[28:29]
	v_rcp_f32_e32 v18, v18
	v_rcp_f32_e32 v19, v19
	v_exp_f32_e32 v20, v20
	v_exp_f32_e32 v21, v21
	v_mad_i32_i24 v29, v27, s0, v29
	v_lshl_add_u64 v[26:27], s[2:3], 1, v[28:29]
	v_mov_b32_e32 v101, v63
	v_lshl_add_u64 v[148:149], v[26:27], 0, v[100:101]
	v_sub_f32_e32 v117, v116, v117
	v_lshlrev_b32_e32 v27, 16, v142
	v_fmamk_f32 v220, v40, 0xbf1b4598, v117
	v_lshlrev_b32_e32 v26, 16, v136
	v_lshlrev_b32_e32 v29, 16, v143
	v_mov_b32_e32 v28, v27
	v_add_f32_e32 v20, 1.0, v20
	v_add_f32_e32 v21, 1.0, v21
	v_fmamk_f32 v221, v36, 0xbf1b4598, v220
	v_pk_add_f32 v[26:27], v[26:27], v[28:29] neg_lo:[0,1] neg_hi:[0,1]
	v_pk_add_f32 v[36:37], v[18:19], -1.0 op_sel_hi:[1,0]
	v_rcp_f32_e32 v20, v20
	v_rcp_f32_e32 v21, v21
	v_pk_fma_f32 v[26:27], v[106:107], v[26:27], v[28:29] op_sel_hi:[0,1,1]
	v_pk_fma_f32 v[36:37], v[124:125], v[36:37], 1.0 op_sel_hi:[0,1,0]
	v_pk_mul_f32 v[36:37], v[26:27], v[36:37]
	v_lshlrev_b32_e32 v41, 16, v137
	v_pk_mul_f32 v[136:137], v[26:27], v[122:123] op_sel_hi:[1,0]
	v_lshlrev_b32_e32 v26, 16, v155
	v_lshlrev_b32_e32 v27, 16, v109
	v_mul_f32_e32 v22, 0xbfb8aa3b, v22
	v_mul_f32_e32 v23, 0xbfb8aa3b, v23
	v_lshlrev_b32_e32 v40, 16, v156
	v_lshlrev_b32_e32 v113, 16, v139
	v_mov_b32_e32 v112, v41
	v_pk_mov_b32 v[28:29], v[28:29], v[26:27] op_sel:[1,0]
	v_exp_f32_e32 v22, v22
	v_exp_f32_e32 v23, v23
	v_pk_add_f32 v[40:41], v[40:41], v[112:113] neg_lo:[0,1] neg_hi:[0,1]
	v_pk_add_f32 v[28:29], v[28:29], v[26:27] neg_lo:[0,1] neg_hi:[0,1]
	v_pk_fma_f32 v[142:143], v[58:59], v[40:41], v[112:113] op_sel_hi:[0,1,1]
	v_pk_fma_f32 v[26:27], v[106:107], v[28:29], v[26:27] op_sel_hi:[0,1,1]
	v_pk_add_f32 v[28:29], v[20:21], -1.0 op_sel_hi:[1,0]
	v_pk_mul_f32 v[40:41], v[142:143], v[36:37]
	v_pk_fma_f32 v[28:29], v[124:125], v[28:29], 1.0 op_sel_hi:[0,1,0]
	v_fma_f32 v156, v120, v40, 0
	v_fma_f32 v222, v120, v41, 0
	v_pk_mul_f32 v[40:41], v[26:27], v[28:29]
	v_lshlrev_b32_e32 v28, 16, v145
	v_lshlrev_b32_e32 v29, 16, v144
	v_add_f32_e32 v22, 1.0, v22
	v_add_f32_e32 v23, 1.0, v23
	v_pk_mov_b32 v[112:113], v[112:113], v[28:29] op_sel:[1,0]
	v_rcp_f32_e32 v22, v22
	v_rcp_f32_e32 v23, v23
	v_pk_add_f32 v[112:113], v[112:113], v[28:29] neg_lo:[0,1] neg_hi:[0,1]
	v_mov_b32_e32 v109, v60
	v_pk_fma_f32 v[144:145], v[58:59], v[112:113], v[28:29] op_sel_hi:[0,1,1]
	v_pk_mul_f32 v[28:29], v[144:145], v[40:41]
	v_pk_mul_f32 v[112:113], v[26:27], v[122:123] op_sel_hi:[1,0]
	v_fma_f32 v224, v120, v28, 0
	v_pk_add_f32 v[26:27], v[108:109], v[60:61] neg_lo:[0,1] neg_hi:[0,1]
	v_mov_b32_e32 v28, v107
	v_lshlrev_b32_e32 v109, 16, v140
	v_pk_fma_f32 v[106:107], v[28:29], v[26:27], v[60:61] op_sel_hi:[0,1,1]
	v_pk_add_f32 v[26:27], v[22:23], -1.0 op_sel_hi:[1,0]
	v_mov_b32_e32 v58, v125
	v_lshlrev_b32_e32 v108, 16, v141
	v_lshlrev_b32_e32 v125, 16, v154
	v_mov_b32_e32 v124, v109
	v_pk_fma_f32 v[26:27], v[58:59], v[26:27], 1.0 op_sel_hi:[0,1,0]
	v_pk_add_f32 v[108:109], v[108:109], v[124:125] neg_lo:[0,1] neg_hi:[0,1]
	v_mov_b32_e32 v60, v59
	v_mul_f32_e32 v24, 0xbfb8aa3b, v24
	v_mul_f32_e32 v25, 0xbfb8aa3b, v25
	v_pk_mul_f32 v[26:27], v[106:107], v[26:27]
	v_pk_fma_f32 v[140:141], v[60:61], v[108:109], v[124:125] op_sel_hi:[0,1,1]
	v_exp_f32_e32 v24, v24
	v_exp_f32_e32 v25, v25
	v_pk_mul_f32 v[108:109], v[140:141], v[26:27]
	v_mov_b32_e32 v122, v136
	v_fmac_f32_e32 v156, v121, v108
	v_mov_b32_e32 v108, v123
	v_pk_mul_f32 v[106:107], v[106:107], v[108:109] op_sel_hi:[1,0]
	v_add_f32_e32 v24, 1.0, v24
	v_mov_b32_e32 v123, v106
	v_add_f32_e32 v25, 1.0, v25
	v_pk_mul_f32 v[122:123], v[122:123], v[122:123]
	v_rcp_f32_e32 v24, v24
	v_rcp_f32_e32 v25, v25
	v_pk_mul_f32 v[32:33], v[38:39], v[38:39]
	v_fma_f32 v223, v120, v29, 0
	v_mov_b32_e32 v154, v137
	v_mov_b32_e32 v155, v107
	v_add_f32_e32 v29, v122, v123
	v_pk_mul_f32 v[154:155], v[154:155], v[154:155]
	v_add_f32_e32 v29, v29, v32
	v_pk_mul_f32 v[158:159], v[6:7], v[6:7]
	v_add_f32_e32 v226, v29, v33
	v_add_f32_e32 v29, v154, v155
	v_pk_mov_b32 v[32:33], v[60:61], v[104:105] op_sel:[1,0]
	v_add_f32_e32 v29, v29, v158
	v_pk_add_f32 v[32:33], v[32:33], v[104:105] neg_lo:[0,1] neg_hi:[0,1]
	v_mul_f32_e32 v10, 0xbfb8aa3b, v10
	v_mul_f32_e32 v11, 0xbfb8aa3b, v11
	v_add_f32_e32 v158, v29, v159
	v_pk_fma_f32 v[32:33], v[28:29], v[32:33], v[104:105] op_sel_hi:[0,1,1]
	v_pk_add_f32 v[28:29], v[24:25], -1.0 op_sel_hi:[1,0]
	v_exp_f32_e32 v10, v10
	v_exp_f32_e32 v11, v11
	v_pk_fma_f32 v[28:29], v[58:59], v[28:29], 1.0 op_sel_hi:[0,1,0]
	v_pk_mul_f32 v[122:123], v[32:33], v[108:109] op_sel_hi:[1,0]
	v_pk_mul_f32 v[28:29], v[32:33], v[28:29]
	v_mov_b32_e32 v32, v113
	v_mov_b32_e32 v33, v123
	v_pk_mul_f32 v[32:33], v[32:33], v[32:33]
	v_pk_mul_f32 v[160:161], v[16:17], v[16:17]
	v_add_f32_e32 v32, v32, v33
	v_add_f32_e32 v10, 1.0, v10
	v_add_f32_e32 v11, 1.0, v11
	v_add_f32_e32 v32, v32, v160
	v_rcp_f32_e32 v10, v10
	v_rcp_f32_e32 v11, v11
	v_add_f32_e32 v154, v32, v161
	v_mov_b32_e32 v32, v112
	v_mov_b32_e32 v33, v122
	v_mul_f32_e32 v12, 0xbfb8aa3b, v12
	v_mul_f32_e32 v13, 0xbfb8aa3b, v13
	v_pk_mul_f32 v[32:33], v[32:33], v[32:33]
	v_exp_f32_e32 v12, v12
	v_exp_f32_e32 v13, v13
	v_pk_mul_f32 v[30:31], v[8:9], v[8:9]
	v_lshlrev_b32_e32 v58, 16, v138
	v_lshlrev_b32_e32 v59, 16, v135
	v_add_f32_e32 v32, v32, v33
	v_pk_mov_b32 v[104:105], v[124:125], v[58:59] op_sel:[1,0]
	v_add_f32_e32 v30, v32, v30
	v_pk_add_f32 v[104:105], v[104:105], v[58:59] neg_lo:[0,1] neg_hi:[0,1]
	v_add_f32_e32 v155, v30, v31
	v_pk_add_f32 v[30:31], v[10:11], -1.0 op_sel_hi:[1,0]
	v_pk_fma_f32 v[138:139], v[60:61], v[104:105], v[58:59] op_sel_hi:[0,1,1]
	s_waitcnt lgkmcnt(1)
; DI float row16_sum(float v) { v += DPPF(v, 0xB1); v += DPPF(v, 0x4E); v += DPPF(v, 0x141); v += DPPF(v, 0x140); return v; }
; DI unsigned cvtpk(float lo, float hi) { const f2_t v = {lo, hi}; return __builtin_bit_cast(unsigned, __builtin_convertvector(v, bf2_t)); }
; DI void rwkv_r1_item(const Args& A, int l, LAS unsigned char* lds, int item, int& dh_staged, int tid, int wave, int lane) {
;     ...
;         for (int r = 0; r < 4; ++r) { const float x = w0v + wl[nt][r];
;             lw[nt][r] = -0.6065306597126334f * __builtin_amdgcn_rcpf(1.f + __expf(-x));
;             const float a = __builtin_amdgcn_rcpf(1.f + __expf(-(a0v + al[nt][r]))); alp[nt][r] = a;
;             const float k0 = ek[nt][r]; kap[nt][r] = k0 * kkw; ek[nt][r] = k0 * (1.f + (a - 1.f) * kaw);
;             ssq[r] += kap[nt][r] * kap[nt][r]; bsm[r] += er[nt][r] * ek[nt][r] * rkw; } }
; #pragma unroll
;     for (int r = 0; r < 4; ++r) {
;         ssq[r] = row16_sum(ssq[r]); bsm[r] = row16_sum(bsm[r]);
;         ssq[r] = __builtin_amdgcn_rsqf(fmaxf(ssq[r], 1e-24f)); }
;     { bf16* bon = (bf16*)(A.ws + WS_RKB);
; #pragma unroll
;       for (int nt = 0; nt < 4; ++nt)
; #pragma unroll
;           for (int r = 0; r < 4; ++r) { kap[nt][r] *= ssq[r]; MT[(4 * qd + r) * 72 + 16 * nt + fr] = (bf16)cvtpk(bsm[r] * ev[nt][r], 0.f); }
;       asm volatile("s_waitcnt lgkmcnt(0)" ::: "memory");
	v_pk_fma_f32 v[30:31], v[34:35], v[30:31], 1.0 op_sel_hi:[0,1,0]
	v_mov_b32_e32 v32, v130
	v_mov_b32_e32 v33, v126
	v_add_f32_e32 v12, 1.0, v12
	v_add_f32_e32 v13, 1.0, v13
	v_pk_mul_f32 v[58:59], v[138:139], v[28:29]
	v_pk_mul_f32 v[30:31], v[32:33], v[30:31]
	v_lshlrev_b32_e32 v33, 16, v132
	v_rcp_f32_e32 v12, v12
	v_rcp_f32_e32 v13, v13
	v_fmac_f32_e32 v223, v121, v59
	v_fmac_f32_e32 v224, v121, v58
	v_lshlrev_b32_e32 v32, 16, v133
	v_lshlrev_b32_e32 v59, 16, v134
	v_mov_b32_e32 v58, v33
	v_mul_f32_e32 v2, 0xbfb8aa3b, v2
	v_mul_f32_e32 v3, 0xbfb8aa3b, v3
	v_pk_add_f32 v[32:33], v[32:33], v[58:59] neg_lo:[0,1] neg_hi:[0,1]
	v_exp_f32_e32 v2, v2
	v_exp_f32_e32 v3, v3
	v_fmac_f32_e32 v222, v121, v109
	v_pk_fma_f32 v[120:121], v[110:111], v[32:33], v[58:59] op_sel_hi:[0,1,1]
	v_pk_mul_f32 v[32:33], v[120:121], v[30:31]
	v_mov_b32_e32 v60, v152
	s_waitcnt lgkmcnt(0)
	v_fmac_f32_e32 v156, v128, v32
	v_fmac_f32_e32 v222, v128, v33
	v_pk_add_f32 v[32:33], v[12:13], -1.0 op_sel_hi:[1,0]
	v_mov_b32_e32 v61, v150
	v_pk_fma_f32 v[32:33], v[34:35], v[32:33], 1.0 op_sel_hi:[0,1,0]
	v_add_f32_e32 v2, 1.0, v2
	v_add_f32_e32 v3, 1.0, v3
	v_pk_mul_f32 v[32:33], v[60:61], v[32:33]
	v_lshlrev_b32_e32 v60, 16, v97
	v_lshlrev_b32_e32 v61, 16, v95
	v_rcp_f32_e32 v2, v2
	v_rcp_f32_e32 v3, v3
	v_pk_mov_b32 v[58:59], v[58:59], v[60:61] op_sel:[1,0]
	v_mov_b32_e32 v124, v38
	v_pk_add_f32 v[58:59], v[58:59], v[60:61] neg_lo:[0,1] neg_hi:[0,1]
	v_mov_b32_e32 v38, v35
	v_pk_fma_f32 v[132:133], v[110:111], v[58:59], v[60:61] op_sel_hi:[0,1,1]
	v_pk_mul_f32 v[58:59], v[132:133], v[32:33]
	v_lshlrev_b32_e32 v61, 16, v103
	v_fmac_f32_e32 v223, v128, v59
	v_fmac_f32_e32 v224, v128, v58
	v_pk_add_f32 v[58:59], v[2:3], -1.0 op_sel_hi:[1,0]
	v_mov_b32_e32 v126, v131
	v_pk_fma_f32 v[34:35], v[38:39], v[58:59], 1.0 op_sel_hi:[0,1,0]
	v_lshlrev_b32_e32 v59, 16, v93
	v_lshlrev_b32_e32 v58, 16, v89
	v_mov_b32_e32 v60, v59
	v_pk_add_f32 v[58:59], v[58:59], v[60:61] neg_lo:[0,1] neg_hi:[0,1]
	v_mov_b32_e32 v104, v111
	v_pk_mul_f32 v[34:35], v[126:127], v[34:35]
	v_pk_fma_f32 v[126:127], v[104:105], v[58:59], v[60:61] op_sel_hi:[0,1,1]
	v_pk_mul_f32 v[58:59], v[126:127], v[34:35]
	v_mov_b32_e32 v125, v6
	v_fmac_f32_e32 v156, v129, v58
	v_fmac_f32_e32 v222, v129, v59
	v_mul_f32_e32 v4, 0xbfb8aa3b, v4
	v_add_f32_dpp v6, v156, v156 quad_perm:[1,0,3,2] row_mask:0xf bank_mask:0xf bound_ctrl:1
	v_add_f32_dpp v58, v222, v222 quad_perm:[1,0,3,2] row_mask:0xf bank_mask:0xf bound_ctrl:1
	v_mul_f32_e32 v5, 0xbfb8aa3b, v5
	v_add_f32_dpp v6, v6, v6 quad_perm:[2,3,0,1] row_mask:0xf bank_mask:0xf bound_ctrl:1
	v_add_f32_dpp v58, v58, v58 quad_perm:[2,3,0,1] row_mask:0xf bank_mask:0xf bound_ctrl:1
	v_exp_f32_e32 v4, v4
	v_add_f32_dpp v6, v6, v6 row_half_mirror row_mask:0xf bank_mask:0xf bound_ctrl:1
	v_add_f32_dpp v58, v58, v58 row_half_mirror row_mask:0xf bank_mask:0xf bound_ctrl:1
	v_exp_f32_e32 v5, v5
	v_add_f32_dpp v6, v6, v6 row_mirror row_mask:0xf bank_mask:0xf bound_ctrl:1
	v_mul_f32_e32 v59, v46, v6
	v_add_f32_dpp v58, v58, v58 row_mirror row_mask:0xf bank_mask:0xf bound_ctrl:1
	v_cvt_pk_bf16_f32 v59, v59, s0
	ds_write_b16 v207, v59 offset:28800
	v_mul_f32_e32 v59, v47, v58
	v_cvt_pk_bf16_f32 v59, v59, s0
	ds_write_b16 v208, v59 offset:28800
	v_mul_f32_e32 v59, v42, v6
	v_cvt_pk_bf16_f32 v59, v59, s0
	ds_write_b16 v207, v59 offset:28832
	v_mul_f32_e32 v59, v43, v58
	v_cvt_pk_bf16_f32 v59, v59, s0
	v_add_f32_e32 v4, 1.0, v4
	v_add_f32_e32 v5, 1.0, v5
	ds_write_b16 v208, v59 offset:28832
	v_mul_f32_e32 v59, v50, v6
	v_rcp_f32_e32 v4, v4
	v_rcp_f32_e32 v5, v5
	v_cvt_pk_bf16_f32 v59, v59, s0
	ds_write_b16 v207, v59 offset:28864
	v_mul_f32_e32 v59, v51, v58
	v_mul_f32_e32 v6, v54, v6
	v_cvt_pk_bf16_f32 v59, v59, s0
	v_cvt_pk_bf16_f32 v6, v6, s0
	ds_write_b16 v208, v59 offset:28864
	ds_write_b16 v207, v6 offset:28896
	v_mul_f32_e32 v6, v55, v58
	v_cvt_pk_bf16_f32 v6, v6, s0
	v_pk_add_f32 v[58:59], v[4:5], -1.0 op_sel_hi:[1,0]
	ds_write_b16 v208, v6 offset:28896
	v_mov_b32_e32 v6, v39
	v_pk_fma_f32 v[38:39], v[38:39], v[58:59], 1.0 op_sel_hi:[0,1,0]
	v_lshlrev_b32_e32 v58, 16, v99
	v_lshlrev_b32_e32 v59, 16, v91
	v_pk_mov_b32 v[60:61], v[60:61], v[58:59] op_sel:[1,0]
	v_mov_b32_e32 v150, v153
	v_pk_add_f32 v[60:61], v[60:61], v[58:59] neg_lo:[0,1] neg_hi:[0,1]
	v_pk_mul_f32 v[38:39], v[150:151], v[38:39]
	v_pk_fma_f32 v[130:131], v[104:105], v[60:61], v[58:59] op_sel_hi:[0,1,1]
	v_pk_mul_f32 v[58:59], v[130:131], v[38:39]
	v_sub_f32_e32 v225, v118, v119
	v_fmac_f32_e32 v223, v129, v59
	v_fmac_f32_e32 v224, v129, v58
	v_fmamk_f32 v157, v157, 0xbf1b4598, v225
	v_add_f32_dpp v59, v223, v223 quad_perm:[1,0,3,2] row_mask:0xf bank_mask:0xf bound_ctrl:1
	v_add_f32_dpp v58, v224, v224 quad_perm:[1,0,3,2] row_mask:0xf bank_mask:0xf bound_ctrl:1
	v_fmamk_f32 v162, v162, 0xbf1b4598, v157
	v_add_f32_dpp v59, v59, v59 quad_perm:[2,3,0,1] row_mask:0xf bank_mask:0xf bound_ctrl:1
	v_add_f32_dpp v58, v58, v58 quad_perm:[2,3,0,1] row_mask:0xf bank_mask:0xf bound_ctrl:1
	v_sub_f32_e32 v115, v114, v115
	v_add_f32_dpp v59, v59, v59 row_half_mirror row_mask:0xf bank_mask:0xf bound_ctrl:1
	v_add_f32_dpp v58, v58, v58 row_half_mirror row_mask:0xf bank_mask:0xf bound_ctrl:1
	v_fmamk_f32 v119, v163, 0xbf1b4598, v115
	v_add_f32_dpp v59, v59, v59 row_mirror row_mask:0xf bank_mask:0xf bound_ctrl:1
	v_mul_f32_e32 v60, v49, v59
	v_cvt_pk_bf16_f32 v60, v60, s0
	ds_write_b16 v208, v60 offset:29088
	v_mul_f32_e32 v60, v45, v59
	v_cvt_pk_bf16_f32 v60, v60, s0
	ds_write_b16 v208, v60 offset:29120
	v_mul_f32_e32 v60, v53, v59
	v_mul_f32_e32 v59, v57, v59
	v_cvt_pk_bf16_f32 v59, v59, s0
	v_add_f32_dpp v58, v58, v58 row_mirror row_mask:0xf bank_mask:0xf bound_ctrl:1
	ds_write_b16 v208, v59 offset:29184
	v_mul_f32_e32 v59, v48, v58
	v_cvt_pk_bf16_f32 v59, v59, s0
	ds_write_b16 v208, v59 offset:28944
	v_mul_f32_e32 v59, v44, v58
	v_cvt_pk_bf16_f32 v59, v59, s0
	ds_write_b16 v208, v59 offset:28976
	v_mul_f32_e32 v59, v52, v58
	v_mul_f32_e32 v58, v56, v58
	v_cvt_pk_bf16_f32 v60, v60, s0
	v_cvt_pk_bf16_f32 v59, v59, s0
	v_cvt_pk_bf16_f32 v58, v58, s0
	ds_write_b16 v208, v60 offset:29152
	ds_write_b16 v208, v59 offset:29008
	ds_write_b16 v208, v58 offset:29040
	s_waitcnt lgkmcnt(0)
; #define LAS __attribute__((address_space(3)))
; DI void rwkv_r1_item(const Args& A, int l, LAS unsigned char* lds, int item, int& dh_staged, int tid, int wave, int lane) {
;     ...
;       const int p = lane >> 2, c16 = (lane & 3) * 16; const LAS u32x4_t* sp = (const LAS u32x4_t*)(MT + p * 72 + c16); const u32x4_t w0 = sp[0], w1 = sp[1];
;       bf16* dst = bon + ((size_t)dir * NT + tok0 + sgn * p) * RW + hh * 64 + c16;
;       *(u32x4_t*)dst = w0; *(u32x4_t*)(dst + 8) = w1;
;       asm volatile("s_waitcnt lgkmcnt(0)" ::: "memory"); }
;     unsigned char* pkg = A.ws + WS_PKG + ((size_t)((dir * NB + b) * 6 + hh) * 128 + cc) * PKG_BYTES;
;     float lend[4];
;     u32x2_t btf[4], ktf[4];
; #pragma unroll
;     for (int nt = 0; nt < 4; ++nt) { float lam[4]; lam[0] = lw[nt][0]; lam[1] = lam[0] + lw[nt][1]; lam[2] = lam[1] + lw[nt][2]; lam[3] = lam[2] + lw[nt][3];
;         const float t1 = __shfl(lam[3], lane - 16), t2 = __shfl(lam[3], lane - 32), t3 = __shfl(lam[3], lane - 48);
;         const float off = (qd >= 1 ? t1 : 0.f) + (qd >= 2 ? t2 : 0.f) + (qd >= 3 ? t3 : 0.f);
; #pragma unroll
;         for (int r = 0; r < 4; ++r) lam[r] += off;
;         lend[nt] = __shfl(lam[3], 48 + fr);
;         float bt4[4], kt4[4];
;         float epv[4];
; #pragma unroll
;         for (int r = 0; r < 4; ++r) epv[r] = __expf(lam[r]);
;         float ep_prev = __shfl(epv[3], lane - 16); if (qd == 0) ep_prev = 1.f;
;         const float eendall = __expf(lend[nt]);
;         float ia[4], ir[4], ib[4], ik[4];
; #pragma unroll
;         for (int r = 0; r < 4; ++r) { const float ep = epv[r], epm = r ? epv[r - 1] : ep_prev, einv = __builtin_amdgcn_rcpf(ep), eend = eendall * einv;
;             const float bb = kap[nt][r] * alp[nt][r];
;             ia[r] = -kap[nt][r] * epm; ir[r] = er[nt][r] * ep; ib[r] = bb * einv; ik[r] = ek[nt][r] * einv;
;             bt4[r] = bb * eend; kt4[r] = ek[nt][r] * eend; }
; #pragma unroll
;         for (int r = 0; r < 4; r += 2) { const int o = (4 * qd + r) * 72 + 16 * nt + fr;
;             const unsigned pa_ = cvtpk(ia[r], ia[r + 1]), pr_ = cvtpk(ir[r], ir[r + 1]), pb_ = cvtpk(ib[r], ib[r + 1]), pk_ = cvtpk(ik[r], ik[r + 1]);
;             IMG[o] = (bf16)pa_; IMG[o + 72] = (bf16)(pa_ >> 16); IMG[1152 + o] = (bf16)pr_; IMG[1152 + o + 72] = (bf16)(pr_ >> 16);
	ds_read_b128 v[58:61], v180 offset:28800
	ds_read_b128 v[108:111], v180 offset:28816
	s_waitcnt lgkmcnt(1)
	global_store_dwordx4 v[148:149], v[58:61], off
	s_waitcnt lgkmcnt(0)
	global_store_dwordx4 v[148:149], v[108:111], off offset:16
	v_or_b32_e32 v58, v209, v146
	v_lshlrev_b32_e32 v58, 2, v58
	v_xor_b32_e32 v97, 0x80, v58
	v_or_b32_e32 v58, v209, v68
	v_lshlrev_b32_e32 v95, 2, v58
	ds_bpermute_b32 v58, v210, v221
	ds_bpermute_b32 v59, v97, v221
	ds_bpermute_b32 v60, v211, v221
	s_waitcnt lgkmcnt(0)
	v_fmamk_f32 v101, v217, 0xbf1b4598, v119
	s_waitcnt lgkmcnt(2)
	v_cndmask_b32_e64 v58, v58, 0, s[10:11]
	s_waitcnt lgkmcnt(1)
	v_cndmask_b32_e64 v59, 0, v59, s[80:81]
	v_add_f32_e32 v58, v58, v59
	s_waitcnt lgkmcnt(0)
	v_cndmask_b32_e64 v59, 0, v60, s[82:83]
	v_add_f32_e32 v58, v58, v59
	v_add_f32_e32 v59, v116, v58
	v_add_f32_e32 v60, v117, v58
	v_add_f32_e32 v61, v220, v58
	v_add_f32_e32 v89, v221, v58
	v_mul_f32_e32 v58, 0x3fb8aa3b, v59
	v_mul_f32_e32 v59, 0x3fb8aa3b, v60
	v_mul_f32_e32 v60, 0x3fb8aa3b, v61
	v_exp_f32_e32 v104, v60
	v_mul_f32_e32 v60, 0x3fb8aa3b, v89
	v_exp_f32_e32 v105, v60
	v_exp_f32_e32 v58, v58
	v_exp_f32_e32 v59, v59
	v_rcp_f32_e32 v108, v104
	ds_bpermute_b32 v60, v210, v105
	v_rcp_f32_e32 v109, v105
	v_rcp_f32_e32 v61, v59
	v_pk_mul_f32 v[116:117], v[142:143], v[58:59]
	ds_bpermute_b32 v91, v95, v89
	s_waitcnt lgkmcnt(1)
	v_cndmask_b32_e64 v110, v60, 1.0, s[10:11]
	v_rcp_f32_e32 v60, v58
	v_mov_b32_e32 v111, v58
	v_pk_mul_f32 v[142:143], v[144:145], v[104:105]
	v_mov_b32_e32 v144, v59
	v_pk_mul_f32 v[128:129], v[36:37], v[60:61]
	v_pk_mul_f32 v[58:59], v[40:41], v[108:109]
	v_cvt_pk_bf16_f32 v89, v116, v117
	v_cvt_pk_bf16_f32 v93, v128, v129
	ds_write_b16 v207, v89 offset:20736
	ds_write_b16_d16_hi v207, v89 offset:20880
	ds_write_b16 v207, v93 offset:25344
	ds_write_b16_d16_hi v207, v93 offset:25488
	v_cvt_pk_bf16_f32 v89, v142, v143
	v_cvt_pk_bf16_f32 v58, v58, v59
	ds_write_b16 v208, v89 offset:20880
	ds_write_b16_d16_hi v208, v89 offset:21024
	ds_write_b16 v208, v58 offset:25488
	ds_write_b16_d16_hi v208, v58 offset:25632
	ds_bpermute_b32 v58, v210, v162
	ds_bpermute_b32 v59, v97, v162
	ds_bpermute_b32 v89, v211, v162
	v_mov_b32_e32 v145, v104
	v_mov_b32_e32 v134, v8
	s_waitcnt lgkmcnt(2)
	v_cndmask_b32_e64 v58, v58, 0, s[10:11]
	s_waitcnt lgkmcnt(1)
	v_cndmask_b32_e64 v59, 0, v59, s[80:81]
	v_add_f32_e32 v58, v58, v59
	s_waitcnt lgkmcnt(0)
	v_cndmask_b32_e64 v59, 0, v89, s[82:83]
	v_add_f32_e32 v58, v58, v59
	v_add_f32_e32 v59, v118, v58
	v_add_f32_e32 v93, v225, v58
	v_mul_f32_e32 v59, 0x3fb8aa3b, v59
	v_exp_f32_e32 v142, v59
	v_mul_f32_e32 v59, 0x3fb8aa3b, v93
	v_add_f32_dpp v93, v226, v226 quad_perm:[1,0,3,2] row_mask:0xf bank_mask:0xf bound_ctrl:1
	v_add_f32_e32 v99, v157, v58
	v_add_f32_e32 v58, v162, v58
	v_add_f32_dpp v93, v93, v93 quad_perm:[2,3,0,1] row_mask:0xf bank_mask:0xf bound_ctrl:1
	ds_bpermute_b32 v89, v95, v58
	v_mul_f32_e32 v58, 0x3fb8aa3b, v58
	v_add_f32_dpp v93, v93, v93 row_half_mirror row_mask:0xf bank_mask:0xf bound_ctrl:1
	v_exp_f32_e32 v149, v58
	v_exp_f32_e32 v143, v59
	v_add_f32_dpp v93, v93, v93 row_mirror row_mask:0xf bank_mask:0xf bound_ctrl:1
	v_max_f32_e32 v93, 0x179abe15, v93
	v_rsq_f32_e32 v128, v93
	ds_bpermute_b32 v58, v210, v149
	v_add_f32_dpp v93, v158, v158 quad_perm:[1,0,3,2] row_mask:0xf bank_mask:0xf bound_ctrl:1
	v_mul_f32_e32 v59, 0x3fb8aa3b, v99
	v_exp_f32_e32 v148, v59
	v_add_f32_dpp v93, v93, v93 quad_perm:[2,3,0,1] row_mask:0xf bank_mask:0xf bound_ctrl:1
	s_waitcnt lgkmcnt(0)
	v_cndmask_b32_e64 v150, v58, 1.0, s[10:11]
	v_mov_b32_e32 v151, v142
	v_add_f32_dpp v93, v93, v93 row_half_mirror row_mask:0xf bank_mask:0xf bound_ctrl:1
	v_rcp_f32_e32 v58, v142
	v_rcp_f32_e32 v59, v143
	v_add_f32_dpp v93, v93, v93 row_mirror row_mask:0xf bank_mask:0xf bound_ctrl:1
	v_max_f32_e32 v93, 0x179abe15, v93
	v_rsq_f32_e32 v129, v93
	v_pk_mul_f32 v[140:141], v[140:141], v[142:143]
	v_pk_mul_f32 v[138:139], v[138:139], v[148:149]
	v_mov_b32_e32 v135, v16
	v_pk_mul_f32 v[104:105], v[136:137], v[128:129]
	v_pk_mul_f32 v[106:107], v[106:107], v[128:129]
	v_pk_mul_f32 v[116:117], v[18:19], v[104:105]
	v_pk_mul_f32 v[18:19], v[110:111], v[104:105] neg_lo:[0,1] neg_hi:[0,1]
	v_pk_mul_f32 v[104:105], v[116:117], v[60:61]
	v_cvt_pk_bf16_f32 v18, v18, v19
	v_cvt_pk_bf16_f32 v19, v104, v105
	ds_write_b16 v207, v18 offset:18432
	ds_write_b16_d16_hi v207, v18 offset:18576
	ds_write_b16 v207, v19 offset:23040
	ds_write_b16_d16_hi v207, v19 offset:23184
	v_add_f32_dpp v18, v154, v154 quad_perm:[1,0,3,2] row_mask:0xf bank_mask:0xf bound_ctrl:1
	v_pk_mul_f32 v[104:105], v[22:23], v[106:107]
	v_pk_mul_f32 v[22:23], v[150:151], v[106:107] neg_lo:[0,1] neg_hi:[0,1]
	v_add_f32_dpp v18, v18, v18 quad_perm:[2,3,0,1] row_mask:0xf bank_mask:0xf bound_ctrl:1
	v_rcp_f32_e32 v106, v148
	v_rcp_f32_e32 v107, v149
	v_add_f32_dpp v18, v18, v18 row_half_mirror row_mask:0xf bank_mask:0xf bound_ctrl:1
	v_pk_mul_f32 v[136:137], v[104:105], v[58:59]
	v_pk_mul_f32 v[150:151], v[26:27], v[58:59]
	v_add_f32_dpp v18, v18, v18 row_mirror row_mask:0xf bank_mask:0xf bound_ctrl:1
	v_max_f32_e32 v18, 0x179abe15, v18
	v_rsq_f32_e32 v19, v18
	v_cvt_pk_bf16_f32 v22, v22, v23
	v_add_f32_dpp v18, v155, v155 quad_perm:[1,0,3,2] row_mask:0xf bank_mask:0xf bound_ctrl:1
	v_cvt_pk_bf16_f32 v23, v140, v141
	v_cvt_pk_bf16_f32 v93, v136, v137
	v_add_f32_dpp v18, v18, v18 quad_perm:[2,3,0,1] row_mask:0xf bank_mask:0xf bound_ctrl:1
	v_cvt_pk_bf16_f32 v99, v150, v151
	v_sub_f32_e32 v15, v14, v15
	v_add_f32_dpp v18, v18, v18 row_half_mirror row_mask:0xf bank_mask:0xf bound_ctrl:1
	v_fmamk_f32 v16, v218, 0xbf1b4598, v15
; DI unsigned cvtpk(float lo, float hi) { const f2_t v = {lo, hi}; return __builtin_bit_cast(unsigned, __builtin_convertvector(v, bf2_t)); }
; DI void rwkv_r1_item(const Args& A, int l, LAS unsigned char* lds, int item, int& dh_staged, int tid, int wave, int lane) {
;     ...
;     for (int nt = 0; nt < 4; ++nt) { float lam[4]; lam[0] = lw[nt][0]; lam[1] = lam[0] + lw[nt][1]; lam[2] = lam[1] + lw[nt][2]; lam[3] = lam[2] + lw[nt][3];
;         const float t1 = __shfl(lam[3], lane - 16), t2 = __shfl(lam[3], lane - 32), t3 = __shfl(lam[3], lane - 48);
;         const float off = (qd >= 1 ? t1 : 0.f) + (qd >= 2 ? t2 : 0.f) + (qd >= 3 ? t3 : 0.f);
; #pragma unroll
;         for (int r = 0; r < 4; ++r) lam[r] += off;
;         lend[nt] = __shfl(lam[3], 48 + fr);
;         float bt4[4], kt4[4];
;         float epv[4];
; #pragma unroll
;         for (int r = 0; r < 4; ++r) epv[r] = __expf(lam[r]);
;         float ep_prev = __shfl(epv[3], lane - 16); if (qd == 0) ep_prev = 1.f;
;         const float eendall = __expf(lend[nt]);
;         float ia[4], ir[4], ib[4], ik[4];
; #pragma unroll
;         for (int r = 0; r < 4; ++r) { const float ep = epv[r], epm = r ? epv[r - 1] : ep_prev, einv = __builtin_amdgcn_rcpf(ep), eend = eendall * einv;
;             const float bb = kap[nt][r] * alp[nt][r];
;             ia[r] = -kap[nt][r] * epm; ir[r] = er[nt][r] * ep; ib[r] = bb * einv; ik[r] = ek[nt][r] * einv;
;             bt4[r] = bb * eend; kt4[r] = ek[nt][r] * eend; }
; #pragma unroll
;         for (int r = 0; r < 4; r += 2) { const int o = (4 * qd + r) * 72 + 16 * nt + fr;
;             const unsigned pa_ = cvtpk(ia[r], ia[r + 1]), pr_ = cvtpk(ir[r], ir[r + 1]), pb_ = cvtpk(ib[r], ib[r + 1]), pk_ = cvtpk(ik[r], ik[r + 1]);
;             IMG[o] = (bf16)pa_; IMG[o + 72] = (bf16)(pa_ >> 16); IMG[1152 + o] = (bf16)pr_; IMG[1152 + o + 72] = (bf16)(pr_ >> 16);
;             IMG[2304 + o] = (bf16)pb_; IMG[2304 + o + 72] = (bf16)(pb_ >> 16); IMG[3456 + o] = (bf16)pk_; IMG[3456 + o + 72] = (bf16)(pk_ >> 16); }
;         btf[nt].x = cvtpk(bt4[0], bt4[1]); btf[nt].y = cvtpk(bt4[2], bt4[3]); ktf[nt].x = cvtpk(kt4[0], kt4[1]); ktf[nt].y = cvtpk(kt4[2], kt4[3]); }
	v_fmamk_f32 v8, v219, 0xbf1b4598, v16
	v_add_f32_dpp v18, v18, v18 row_mirror row_mask:0xf bank_mask:0xf bound_ctrl:1
	v_max_f32_e32 v18, 0x179abe15, v18
	v_rsq_f32_e32 v18, v18
	v_pk_mul_f32 v[6:7], v[6:7], v[128:129]
	v_mov_b32_e32 v224, s76
	v_readlane_b32 s0, v234, 5
	v_pk_mul_f32 v[110:111], v[112:113], v[18:19]
	v_pk_mul_f32 v[112:113], v[122:123], v[18:19]
	v_pk_mul_f32 v[122:123], v[20:21], v[110:111]
	v_pk_mul_f32 v[20:21], v[144:145], v[110:111] neg_lo:[0,1] neg_hi:[0,1]
	v_pk_mul_f32 v[110:111], v[122:123], v[108:109]
	v_cvt_pk_bf16_f32 v20, v20, v21
	v_cvt_pk_bf16_f32 v21, v110, v111
	ds_write_b16 v208, v20 offset:18576
	ds_write_b16_d16_hi v208, v20 offset:18720
	ds_write_b16 v208, v21 offset:23184
	ds_write_b16_d16_hi v208, v21 offset:23328
	v_mov_b32_e32 v20, v143
	v_mov_b32_e32 v21, v148
	v_pk_mul_f32 v[110:111], v[24:25], v[112:113]
	v_pk_mul_f32 v[20:21], v[20:21], v[112:113] neg_lo:[0,1] neg_hi:[0,1]
	v_pk_mul_f32 v[24:25], v[110:111], v[106:107]
	v_pk_mul_f32 v[112:113], v[28:29], v[106:107]
	v_cvt_pk_bf16_f32 v20, v20, v21
	v_cvt_pk_bf16_f32 v21, v138, v139
	ds_write_b16 v207, v22 offset:18464
	ds_write_b16_d16_hi v207, v22 offset:18608
	ds_write_b16 v207, v23 offset:20768
	ds_write_b16_d16_hi v207, v23 offset:20912
	ds_write_b16 v207, v93 offset:23072
	ds_write_b16_d16_hi v207, v93 offset:23216
	ds_write_b16 v207, v99 offset:25376
	ds_write_b16_d16_hi v207, v99 offset:25520
	v_cvt_pk_bf16_f32 v22, v24, v25
	v_cvt_pk_bf16_f32 v23, v112, v113
	ds_write_b16 v208, v20 offset:18608
	ds_write_b16_d16_hi v208, v20 offset:18752
	ds_write_b16 v208, v21 offset:20912
	ds_write_b16_d16_hi v208, v21 offset:21056
	ds_write_b16 v208, v22 offset:23216
	ds_write_b16_d16_hi v208, v22 offset:23360
	ds_write_b16 v208, v23 offset:25520
	ds_write_b16_d16_hi v208, v23 offset:25664
	ds_bpermute_b32 v20, v210, v101
	ds_bpermute_b32 v21, v97, v101
	ds_bpermute_b32 v22, v211, v101
	v_pk_mul_f32 v[134:135], v[134:135], v[18:19]
	v_mov_b32_e32 v225, v182
	s_waitcnt lgkmcnt(2)
	v_cndmask_b32_e64 v20, v20, 0, s[10:11]
	s_waitcnt lgkmcnt(1)
	v_cndmask_b32_e64 v21, 0, v21, s[80:81]
	v_add_f32_e32 v20, v20, v21
	s_waitcnt lgkmcnt(0)
	v_cndmask_b32_e64 v21, 0, v22, s[82:83]
	v_add_f32_e32 v20, v20, v21
	v_add_f32_e32 v21, v114, v20
	v_add_f32_e32 v22, v115, v20
	v_add_f32_e32 v23, v119, v20
	v_add_f32_e32 v24, v101, v20
	v_mul_f32_e32 v20, 0x3fb8aa3b, v21
	v_mul_f32_e32 v21, 0x3fb8aa3b, v22
	v_mul_f32_e32 v22, 0x3fb8aa3b, v23
	v_mul_f32_e32 v23, 0x3fb8aa3b, v24
	v_exp_f32_e32 v23, v23
	ds_bpermute_b32 v93, v95, v24
	v_exp_f32_e32 v20, v20
	v_exp_f32_e32 v21, v21
	ds_bpermute_b32 v24, v210, v23
	v_exp_f32_e32 v22, v22
	v_rcp_f32_e32 v112, v20
	v_rcp_f32_e32 v113, v21
	v_pk_mul_f32 v[118:119], v[124:125], v[128:129]
	s_waitcnt lgkmcnt(0)
	v_cndmask_b32_e64 v24, v24, 1.0, s[10:11]
	v_mov_b32_e32 v25, v20
	v_pk_mul_f32 v[114:115], v[10:11], v[118:119]
	v_pk_mul_f32 v[10:11], v[24:25], v[118:119] neg_lo:[0,1] neg_hi:[0,1]
	v_rcp_f32_e32 v118, v22
	v_rcp_f32_e32 v119, v23
	v_pk_mul_f32 v[136:137], v[120:121], v[20:21]
	v_pk_mul_f32 v[120:121], v[12:13], v[134:135]
	v_mov_b32_e32 v12, v21
	v_mov_b32_e32 v13, v22
	v_pk_mul_f32 v[24:25], v[114:115], v[112:113]
	v_pk_mul_f32 v[124:125], v[30:31], v[112:113]
	v_pk_mul_f32 v[132:133], v[132:133], v[22:23]
	v_pk_mul_f32 v[12:13], v[12:13], v[134:135] neg_lo:[0,1] neg_hi:[0,1]
	v_cvt_pk_bf16_f32 v10, v10, v11
	v_cvt_pk_bf16_f32 v11, v136, v137
	v_pk_mul_f32 v[20:21], v[120:121], v[118:119]
	v_pk_mul_f32 v[22:23], v[32:33], v[118:119]
	v_cvt_pk_bf16_f32 v24, v24, v25
	v_cvt_pk_bf16_f32 v25, v124, v125
	ds_write_b16 v207, v10 offset:18496
	ds_write_b16_d16_hi v207, v10 offset:18640
	ds_write_b16 v207, v11 offset:20800
	ds_write_b16_d16_hi v207, v11 offset:20944
	ds_write_b16 v207, v24 offset:23104
	ds_write_b16_d16_hi v207, v24 offset:23248
	ds_write_b16 v207, v25 offset:25408
	ds_write_b16_d16_hi v207, v25 offset:25552
	v_cvt_pk_bf16_f32 v10, v12, v13
	v_cvt_pk_bf16_f32 v11, v132, v133
	v_cvt_pk_bf16_f32 v12, v20, v21
	v_cvt_pk_bf16_f32 v13, v22, v23
	ds_write_b16 v208, v10 offset:18640
	ds_write_b16_d16_hi v208, v10 offset:18784
	ds_write_b16 v208, v11 offset:20944
	ds_write_b16_d16_hi v208, v11 offset:21088
	ds_write_b16 v208, v12 offset:23248
	ds_write_b16_d16_hi v208, v12 offset:23392
	ds_write_b16 v208, v13 offset:25552
	ds_write_b16_d16_hi v208, v13 offset:25696
	ds_bpermute_b32 v10, v210, v8
	ds_bpermute_b32 v11, v97, v8
	ds_bpermute_b32 v12, v211, v8
	s_waitcnt lgkmcnt(2)
	v_cndmask_b32_e64 v10, v10, 0, s[10:11]
	s_waitcnt lgkmcnt(1)
	v_cndmask_b32_e64 v11, 0, v11, s[80:81]
	v_add_f32_e32 v10, v10, v11
	s_waitcnt lgkmcnt(0)
	v_cndmask_b32_e64 v11, 0, v12, s[82:83]
	v_add_f32_e32 v10, v10, v11
	v_add_f32_e32 v8, v8, v10
	v_add_f32_e32 v11, v14, v10
	v_add_f32_e32 v12, v15, v10
	v_add_f32_e32 v13, v16, v10
	ds_bpermute_b32 v95, v95, v8
	v_mul_f32_e32 v8, 0x3fb8aa3b, v8
	v_mul_f32_e32 v10, 0x3fb8aa3b, v11
	v_mul_f32_e32 v11, 0x3fb8aa3b, v12
	v_mul_f32_e32 v12, 0x3fb8aa3b, v13
	v_exp_f32_e32 v13, v8
	v_exp_f32_e32 v10, v10
	v_exp_f32_e32 v11, v11
	v_exp_f32_e32 v12, v12
	ds_bpermute_b32 v8, v210, v13
	v_rcp_f32_e32 v124, v10
	v_rcp_f32_e32 v125, v11
	v_rcp_f32_e32 v128, v12
	v_rcp_f32_e32 v129, v13
	v_mov_b32_e32 v16, v9
	s_waitcnt lgkmcnt(0)
; #define LAS __attribute__((address_space(3)))
; #define MFMA16(a, b, c) __builtin_amdgcn_mfma_f32_16x16x32_bf16((a), (b), (c), 0, 0, 0)
; DI void rwkv_r1_item(const Args& A, int l, LAS unsigned char* lds, int item, int& dh_staged, int tid, int wave, int lane) {
;     ...
;         for (int r = 0; r < 4; ++r) { const float ep = epv[r], epm = r ? epv[r - 1] : ep_prev, einv = __builtin_amdgcn_rcpf(ep), eend = eendall * einv;
;             const float bb = kap[nt][r] * alp[nt][r];
;             ia[r] = -kap[nt][r] * epm; ir[r] = er[nt][r] * ep; ib[r] = bb * einv; ik[r] = ek[nt][r] * einv;
;             bt4[r] = bb * eend; kt4[r] = ek[nt][r] * eend; }
; #pragma unroll
;         for (int r = 0; r < 4; r += 2) { const int o = (4 * qd + r) * 72 + 16 * nt + fr;
;             const unsigned pa_ = cvtpk(ia[r], ia[r + 1]), pr_ = cvtpk(ir[r], ir[r + 1]), pb_ = cvtpk(ib[r], ib[r + 1]), pk_ = cvtpk(ik[r], ik[r + 1]);
;             IMG[o] = (bf16)pa_; IMG[o + 72] = (bf16)(pa_ >> 16); IMG[1152 + o] = (bf16)pr_; IMG[1152 + o + 72] = (bf16)(pr_ >> 16);
;             IMG[2304 + o] = (bf16)pb_; IMG[2304 + o + 72] = (bf16)(pb_ >> 16); IMG[3456 + o] = (bf16)pk_; IMG[3456 + o + 72] = (bf16)(pk_ >> 16); }
;         btf[nt].x = cvtpk(bt4[0], bt4[1]); btf[nt].y = cvtpk(bt4[2], bt4[3]); ktf[nt].x = cvtpk(kt4[0], kt4[1]); ktf[nt].y = cvtpk(kt4[2], kt4[3]); }
;     asm volatile("s_waitcnt lgkmcnt(0)" ::: "memory");
;     f32x4 Lab = (f32x4){0.f, 0.f, 0.f, 0.f}, Lak = Lab, Mrb = Lab, Mrk = Lab;
; #pragma unroll
;     for (int ks = 0; ks < 2; ++ks) { const int o = fr * 72 + 32 * ks + 8 * qd;
;         const bf16x8_t aA = *(const LAS bf16x8_t*)(IMG + o), aR = *(const LAS bf16x8_t*)(IMG + 1152 + o), bB = *(const LAS bf16x8_t*)(IMG + 2304 + o), bK = *(const LAS bf16x8_t*)(IMG + 3456 + o);
;         Lab = MFMA16(aA, bB, Lab); Lak = MFMA16(aA, bK, Lak); Mrb = MFMA16(aR, bB, Mrb); Mrk = MFMA16(aR, bK, Mrk); }
; #pragma unroll
;     for (int r = 0; r < 4; ++r) { const int t = 4 * qd + r; if (!(fr < t)) { Lab[r] = 0.f; Lak[r] = 0.f; } if (!(fr <= t)) { Mrb[r] = 0.f; Mrk[r] = 0.f; } Lf[t * 17 + fr] = Lab[r]; }
;     asm volatile("s_waitcnt lgkmcnt(0)" ::: "memory");
;     float Tc[16];
; #pragma unroll
;     for (int t = 0; t < 16; ++t) { float acc = (t == fr) ? 1.f : 0.f;
; #pragma unroll
;         for (int s = 0; s < t; ++s) acc += Lf[t * 17 + s] * Tc[s];
;         Tc[t] = acc; }
	v_cndmask_b32_e64 v14, v8, 1.0, s[10:11]
	v_mov_b32_e32 v15, v10
	v_pk_mul_f32 v[8:9], v[16:17], v[18:19]
	v_pk_mul_f32 v[20:21], v[126:127], v[10:11]
	v_pk_mul_f32 v[126:127], v[2:3], v[6:7]
	v_pk_mul_f32 v[2:3], v[14:15], v[6:7] neg_lo:[0,1] neg_hi:[0,1]
	v_pk_mul_f32 v[22:23], v[130:131], v[12:13]
	v_pk_mul_f32 v[130:131], v[4:5], v[8:9]
	v_mov_b32_e32 v4, v11
	v_mov_b32_e32 v5, v12
	v_pk_mul_f32 v[6:7], v[126:127], v[124:125]
	v_pk_mul_f32 v[14:15], v[34:35], v[124:125]
	v_pk_mul_f32 v[4:5], v[4:5], v[8:9] neg_lo:[0,1] neg_hi:[0,1]
	v_cvt_pk_bf16_f32 v2, v2, v3
	v_pk_mul_f32 v[8:9], v[130:131], v[128:129]
	v_pk_mul_f32 v[10:11], v[38:39], v[128:129]
	v_cvt_pk_bf16_f32 v3, v20, v21
	v_cvt_pk_bf16_f32 v6, v6, v7
	v_cvt_pk_bf16_f32 v7, v14, v15
	ds_write_b16 v207, v2 offset:18528
	ds_write_b16_d16_hi v207, v2 offset:18672
	ds_write_b16 v207, v3 offset:20832
	ds_write_b16_d16_hi v207, v3 offset:20976
	ds_write_b16 v207, v6 offset:23136
	ds_write_b16_d16_hi v207, v6 offset:23280
	ds_write_b16 v207, v7 offset:25440
	ds_write_b16_d16_hi v207, v7 offset:25584
	v_cvt_pk_bf16_f32 v2, v4, v5
	v_cvt_pk_bf16_f32 v3, v22, v23
	v_cvt_pk_bf16_f32 v4, v8, v9
	v_cvt_pk_bf16_f32 v5, v10, v11
	ds_write_b16 v208, v2 offset:18672
	ds_write_b16_d16_hi v208, v2 offset:18816
	ds_write_b16 v208, v3 offset:20976
	ds_write_b16_d16_hi v208, v3 offset:21120
	ds_write_b16 v208, v4 offset:23280
	ds_write_b16_d16_hi v208, v4 offset:23424
	ds_write_b16 v208, v5 offset:25584
	ds_write_b16_d16_hi v208, v5 offset:25728
	s_waitcnt lgkmcnt(0)
	ds_read_b128 v[2:5], v181 offset:18432
	ds_read_b128 v[6:9], v181 offset:20736
	ds_read_b128 v[10:13], v181 offset:23040
	ds_read_b128 v[14:17], v181 offset:25344
	s_waitcnt lgkmcnt(1)
	v_mfma_f32_16x16x32_bf16 v[18:21], v[2:5], v[10:13], 0
	s_waitcnt lgkmcnt(0)
	v_mfma_f32_16x16x32_bf16 v[2:5], v[2:5], v[14:17], 0
	v_mfma_f32_16x16x32_bf16 v[10:13], v[6:9], v[10:13], 0
	v_mfma_f32_16x16x32_bf16 v[6:9], v[6:9], v[14:17], 0
	ds_read_b128 v[14:17], v181 offset:18496
	ds_read_b128 v[22:25], v181 offset:20800
	ds_read_b128 v[132:135], v181 offset:23104
	ds_read_b128 v[136:139], v181 offset:25408
	s_waitcnt lgkmcnt(1)
	v_mfma_f32_16x16x32_bf16 v[18:21], v[14:17], v[132:135], v[18:21]
	s_waitcnt lgkmcnt(0)
	v_mfma_f32_16x16x32_bf16 v[2:5], v[14:17], v[136:139], v[2:5]
	v_mov_b32_e32 v14, s1
	s_nop 4
	v_cndmask_b32_e64 v14, v14, v18, s[96:97]
	ds_write_b32 v212, v14 offset:27648
	v_cndmask_b32_e64 v14, v19, 0, s[38:39]
	v_cndmask_b32_e64 v15, 0, v20, s[4:5]
	v_add_u32_e32 v16, 0x6c00, v213
	ds_write2_b32 v16, v14, v15 offset1:17
	v_cndmask_b32_e64 v14, 0, v21, s[28:29]
	ds_write_b32 v213, v14 offset:27784
	s_waitcnt lgkmcnt(0)
	ds_read_b32 v14, v224 offset:27716
	v_add_u32_e32 v20, 0x6c00, v224
	ds_read2_b32 v[18:19], v20 offset0:53 offset1:89
	v_mfma_f32_16x16x32_bf16 v[10:13], v[22:25], v[132:135], v[10:13]
	ds_read2_b32 v[132:133], v20 offset0:197 offset1:233
	s_waitcnt lgkmcnt(2)
	v_fma_f32 v99, v182, v14, v183
	ds_read_b64 v[14:15], v224 offset:27784
	v_mfma_f32_16x16x32_bf16 v[6:9], v[22:25], v[136:139], v[6:9]
	s_waitcnt lgkmcnt(0)
	v_fma_f32 v101, v182, v14, v184
	v_mov_b32_e32 v14, s0
	v_fmac_f32_e32 v101, v15, v99
	ds_read2_b32 v[14:15], v14 offset1:1
	v_readlane_b32 s0, v234, 7
	s_waitcnt lgkmcnt(0)
	v_fma_f32 v97, v182, v14, v185
	v_fmac_f32_e32 v97, v99, v15
	ds_read_b128 v[14:17], v224 offset:27920
	v_fmac_f32_e32 v97, v101, v18
	s_waitcnt lgkmcnt(0)
	v_fma_f32 v103, v182, v14, v186
	v_mov_b32_e32 v14, s0
	v_fmac_f32_e32 v103, v99, v15
	ds_read2_b32 v[14:15], v14 offset1:1
	v_readlane_b32 s0, v234, 9
	v_fmac_f32_e32 v103, v101, v16
	v_fmac_f32_e32 v103, v97, v17
	s_waitcnt lgkmcnt(0)
	v_fma_f32 v218, v182, v14, v187
	v_mov_b32_e32 v14, s0
	v_fmac_f32_e32 v218, v99, v15
	ds_read2_b32 v[14:15], v14 offset1:1
	v_readlane_b32 s0, v234, 11
	s_waitcnt lgkmcnt(0)
	v_fmac_f32_e32 v218, v101, v14
	v_mov_b32_e32 v14, s0
	v_fmac_f32_e32 v218, v97, v15
	ds_read2_b64 v[14:17], v14 offset1:1
	v_readlane_b32 s0, v234, 13
	v_fmac_f32_e32 v218, v103, v19
	ds_read2_b32 v[18:19], v20 offset0:125 offset1:161
	s_waitcnt lgkmcnt(1)
	v_fma_f32 v219, v182, v14, v188
	v_fmac_f32_e32 v219, v99, v15
	ds_read_b64 v[14:15], v224 offset:28072
	v_fmac_f32_e32 v219, v101, v16
	v_fmac_f32_e32 v219, v97, v17
	s_waitcnt lgkmcnt(0)
	v_fmac_f32_e32 v219, v103, v14
	v_mov_b32_e32 v14, s0
	v_fmac_f32_e32 v219, v218, v15
	ds_read2_b32 v[14:15], v14 offset1:1
	v_readlane_b32 s0, v234, 15
	s_waitcnt lgkmcnt(0)
	v_fma_f32 v217, v182, v14, v189
	v_mov_b32_e32 v14, s0
	v_fmac_f32_e32 v217, v99, v15
	ds_read2_b32 v[14:15], v14 offset1:1
	v_readlane_b32 s0, v234, 16
	s_waitcnt lgkmcnt(0)
	v_fmac_f32_e32 v217, v101, v14
	v_mov_b32_e32 v14, s0
	v_fmac_f32_e32 v217, v97, v15
	ds_read2_b32 v[14:15], v14 offset1:1
	v_readlane_b32 s0, v234, 17
	s_waitcnt lgkmcnt(0)
	v_fmac_f32_e32 v217, v103, v14
	v_fmac_f32_e32 v217, v218, v15
	ds_read_b128 v[14:17], v224 offset:28192
	v_fmac_f32_e32 v217, v219, v18
	s_waitcnt lgkmcnt(0)
; DI void rwkv_r1_item(const Args& A, int l, LAS unsigned char* lds, int item, int& dh_staged, int tid, int wave, int lane) {
;     ...
;     float Tc[16];
; #pragma unroll
;     for (int t = 0; t < 16; ++t) { float acc = (t == fr) ? 1.f : 0.f;
; #pragma unroll
;         for (int s = 0; s < t; ++s) acc += Lf[t * 17 + s] * Tc[s];
;         Tc[t] = acc; }
;     f32x4 Tm;
; #pragma unroll
;     for (int r = 0; r < 4; ++r) Tm[r] = qd == 0 ? Tc[r] : (qd == 1 ? Tc[4 + r] : (qd == 2 ? Tc[8 + r] : Tc[12 + r]));
	v_fma_f32 v220, v182, v14, v190
	v_fmac_f32_e32 v220, v99, v15
	v_fmac_f32_e32 v220, v101, v16
	v_fmac_f32_e32 v220, v97, v17
	ds_read_b128 v[14:17], v224 offset:28208
	s_waitcnt lgkmcnt(0)
	v_fmac_f32_e32 v220, v103, v14
	v_mov_b32_e32 v14, s0
	v_fmac_f32_e32 v220, v218, v15
	ds_read2_b32 v[14:15], v14 offset1:1
	v_readlane_b32 s0, v234, 18
	v_fmac_f32_e32 v220, v219, v16
	v_fmac_f32_e32 v220, v217, v17
	s_waitcnt lgkmcnt(0)
	v_fma_f32 v221, v182, v14, v191
	v_mov_b32_e32 v14, s0
	v_fmac_f32_e32 v221, v99, v15
	ds_read2_b32 v[14:15], v14 offset1:1
	v_readlane_b32 s0, v234, 19
	s_waitcnt lgkmcnt(0)
	v_fmac_f32_e32 v221, v101, v14
	v_mov_b32_e32 v14, s0
	v_fmac_f32_e32 v221, v97, v15
	ds_read2_b32 v[14:15], v14 offset1:1
	v_readlane_b32 s0, v234, 20
	s_waitcnt lgkmcnt(0)
	v_fmac_f32_e32 v221, v103, v14
	v_mov_b32_e32 v14, s0
	v_fmac_f32_e32 v221, v218, v15
	ds_read2_b32 v[14:15], v14 offset1:1
	v_readlane_b32 s0, v234, 21
	s_waitcnt lgkmcnt(0)
	v_fmac_f32_e32 v221, v219, v14
	v_mov_b32_e32 v14, s0
	v_fmac_f32_e32 v221, v217, v15
	ds_read2_b64 v[14:17], v14 offset1:1
	v_readlane_b32 s0, v234, 22
	v_fmac_f32_e32 v221, v220, v19
	s_waitcnt lgkmcnt(0)
	v_fma_f32 v223, v182, v14, v192
	v_fmac_f32_e32 v223, v99, v15
	v_fmac_f32_e32 v223, v101, v16
	v_mov_b32_e32 v14, s0
	v_fmac_f32_e32 v223, v97, v17
	ds_read2_b64 v[14:17], v14 offset1:1
	v_readlane_b32 s0, v234, 23
	s_waitcnt lgkmcnt(0)
	v_fmac_f32_e32 v223, v103, v14
	v_fmac_f32_e32 v223, v218, v15
	ds_read_b64 v[14:15], v224 offset:28360
	v_fmac_f32_e32 v223, v219, v16
	v_fmac_f32_e32 v223, v217, v17
	s_waitcnt lgkmcnt(0)
	v_fmac_f32_e32 v223, v220, v14
	v_mov_b32_e32 v14, s0
	v_fmac_f32_e32 v223, v221, v15
	ds_read2_b32 v[14:15], v14 offset1:1
	v_readlane_b32 s0, v234, 24
	s_waitcnt lgkmcnt(0)
	v_fma_f32 v222, v182, v14, v193
	v_mov_b32_e32 v14, s0
	v_fmac_f32_e32 v222, v99, v15
	ds_read2_b32 v[14:15], v14 offset1:1
	v_readlane_b32 s0, v234, 25
	s_waitcnt lgkmcnt(0)
	v_fmac_f32_e32 v222, v101, v14
	v_mov_b32_e32 v14, s0
	v_fmac_f32_e32 v222, v97, v15
	ds_read2_b32 v[14:15], v14 offset1:1
	v_readlane_b32 s0, v234, 26
	s_waitcnt lgkmcnt(0)
	v_fmac_f32_e32 v222, v103, v14
	v_mov_b32_e32 v14, s0
	v_fmac_f32_e32 v222, v218, v15
	ds_read2_b32 v[14:15], v14 offset1:1
	v_readlane_b32 s0, v234, 27
	s_waitcnt lgkmcnt(0)
	v_fmac_f32_e32 v222, v219, v14
	v_mov_b32_e32 v14, s0
	v_fmac_f32_e32 v222, v217, v15
	ds_read2_b32 v[14:15], v14 offset1:1
	v_readlane_b32 s0, v234, 28
	s_waitcnt lgkmcnt(0)
	v_fmac_f32_e32 v222, v220, v14
	v_fmac_f32_e32 v222, v221, v15
	ds_read_b128 v[14:17], v224 offset:28464
	v_fmac_f32_e32 v222, v223, v132
	s_waitcnt lgkmcnt(0)
	v_fma_f32 v132, v182, v14, v194
	v_fmac_f32_e32 v132, v99, v15
	v_fmac_f32_e32 v132, v101, v16
	v_fmac_f32_e32 v132, v97, v17
	ds_read_b128 v[14:17], v224 offset:28480
	s_waitcnt lgkmcnt(0)
	v_fmac_f32_e32 v132, v103, v14
	v_fmac_f32_e32 v132, v218, v15
	v_fmac_f32_e32 v132, v219, v16
	v_fmac_f32_e32 v132, v217, v17
	ds_read_b128 v[14:17], v224 offset:28496
	s_waitcnt lgkmcnt(0)
	v_fmac_f32_e32 v132, v220, v14
	v_mov_b32_e32 v14, s0
	v_readlane_b32 s0, v234, 29
	ds_read2_b32 v[144:145], v14 offset1:1
	v_fmac_f32_e32 v132, v221, v15
	v_mov_b32_e32 v14, s0
	v_readlane_b32 s0, v234, 30
	ds_read2_b32 v[142:143], v14 offset1:1
	v_fmac_f32_e32 v132, v223, v16
	v_mov_b32_e32 v14, s0
	v_readlane_b32 s0, v234, 31
	ds_read2_b32 v[140:141], v14 offset1:1
	v_fmac_f32_e32 v132, v222, v17
	v_mov_b32_e32 v14, s0
	v_readlane_b32 s0, v234, 32
	ds_read2_b32 v[138:139], v14 offset1:1
	s_nop 0
	v_mov_b32_e32 v14, s0
	ds_read2_b32 v[136:137], v14 offset1:1
	v_mov_b32_e32 v14, s91
	v_readlane_b32 s0, v234, 33
	ds_read2_b32 v[134:135], v14 offset1:1
	s_nop 0
	v_mov_b32_e32 v14, s0
	v_readlane_b32 s0, v234, 34
	ds_read2_b64 v[22:25], v14 offset1:1
	s_nop 0
	v_mov_b32_e32 v14, s0
	v_readlane_b32 s0, v234, 35
	ds_read2_b64 v[18:21], v14 offset1:1
	s_nop 0
	v_mov_b32_e32 v14, s0
	v_readlane_b32 s0, v234, 36
	ds_read2_b64 v[14:17], v14 offset1:1
	ds_read_b64 v[162:163], v224 offset:28648
	v_mov_b32_e32 v148, s0
	v_readlane_b32 s0, v234, 37
	ds_read2_b32 v[160:161], v148 offset1:1
	s_nop 0
	v_mov_b32_e32 v148, s0
	v_readlane_b32 s0, v234, 38
	ds_read2_b32 v[158:159], v148 offset1:1
	s_nop 0
	v_mov_b32_e32 v148, s0
	ds_read2_b32 v[156:157], v148 offset1:1
	v_mov_b32_e32 v148, s51
	ds_read2_b32 v[154:155], v148 offset1:1
	v_mov_b32_e32 v148, s33
	v_readlane_b32 s0, v234, 39
	ds_read2_b32 v[152:153], v148 offset1:1
	s_nop 0
	v_mov_b32_e32 v148, s0
	ds_read2_b32 v[150:151], v148 offset1:1
	v_mov_b32_e32 v148, s88
	ds_read2_b32 v[148:149], v148 offset1:1
	ds_read_b32 v224, v224 offset:28724
	s_and_saveexec_b64 s[2:3], s[36:37]
	s_cbranch_execz .LBB0_1826
	v_cmp_lt_i32_e32 vcc, 1, v169
	s_mov_b64 s[44:45], 0
	s_and_saveexec_b64 s[46:47], vcc
	s_xor_b64 s[46:47], exec, s[46:47]
	s_cbranch_execnz .LBB0_1861
	s_or_saveexec_b64 s[46:47], s[46:47]
	v_mov_b32_e32 v225, v220
	s_xor_b64 exec, exec, s[46:47]
	s_cbranch_execnz .LBB0_1864
